# PEER v-sweep: loop-invariant gather offsets hoisted out of the slice loop + workgroup barrier every second slice (on top of v12)
# speedup vs baseline: 1.0092x; 1.0092x over previous
; __device__ __forceinline__ float gelu_tanh(float x) { const float u = 0.7978845608028654f * (x + 0.044715f * x * x * x); return 0.5f * x * (1.0f + tanhf(u)); }
; __device__ __forceinline__ void peer_expert_phase(const Args& a, int layer, LAS unsigned char* lds, int G, int bid) {
;     ...
;             wa[i] = ga * gelu_tanh(pa[i] * SCU[ea[i]] * rx) * SCV[ea[i]]; wb[i] = gb * gelu_tanh(pb[i] * SCU[eb[i]] * rx) * SCV[eb[i]]; ssq[i] = 0.f; }
;         unsigned W4[4][4]; float wsc[4];
; #pragma unroll
;         for (int i = 0; i < 4; ++i) { const float wm = wave_max(fmaxf(fabsf(wa[i]), fabsf(wb[i]))); const float qw = wm > 0.f ? 127.0f / wm : 0.f; wsc[i] = wm * (1.0f / 127.0f);
;             const unsigned qa = __float_as_uint(wa[i] * qw + 12582912.0f), qb = __float_as_uint(wb[i] * qw + 12582912.0f);
; #pragma unroll
;             for (int G4 = 0; G4 < 4; ++G4) { unsigned t[4];
; #pragma unroll
;                 for (int k = 0; k < 4; ++k) { const int c = 4 * G4 + k; t[k] = (unsigned)__shfl((int)(c < 8 ? qa : qb), (8 * c + g8) & 63); }
;                 W4[i][G4] = __builtin_amdgcn_perm(__builtin_amdgcn_perm(t[3], t[2], 0x0c0c0400u), __builtin_amdgcn_perm(t[1], t[0], 0x0c0c0400u), 0x05040100u); } }
.LBB0_1237:
	s_andn2_saveexec_b64 s[28:29], s[28:29]
	v_mul_f32_e32 v65, v7, v7
	v_fmamk_f32 v66, v65, 0xbbbac73d, v54
	v_fmaak_f32 v66, v65, v66, 0xbd5c1c4e
	v_fmaak_f32 v66, v65, v66, 0x3e088382
	v_fmaak_f32 v66, v65, v66, 0xbeaaaa99
	v_mul_f32_e64 v66, |v7|, v66
	v_fma_f32 v65, v65, v66, |v7|
	s_or_b64 exec, exec, s[28:29]
	v_lshl_add_u64 v[30:31], v[30:31], 2, s[46:47]
	global_load_dword v30, v[30:31], off
	v_bfi_b32 v33, s90, v110, v33
	v_bfi_b32 v67, s90, v68, v67
	v_mul_f32_e32 v25, 0.5, v25
	v_mul_f32_e32 v32, 0.5, v32
	v_add_f32_e32 v33, 1.0, v33
	v_add_f32_e32 v67, 1.0, v67
	v_mul_f32_e32 v25, v25, v33
	v_mul_f32_e32 v32, v32, v67
	v_mul_f32_e32 v25, v35, v25
	v_mul_f32_e32 v32, v34, v32
	v_mul_f32_e32 v25, v115, v25
	v_mul_f32_e32 v24, v24, v32
	v_max_f32_e64 v32, |v24|, |v25|
	ds_bpermute_b32 v33, v36, v32
	v_bfi_b32 v9, s90, v92, v9
	v_mul_f32_e32 v5, 0.5, v5
	v_add_f32_e32 v9, 1.0, v9
	v_mul_f32_e32 v5, v5, v9
	s_waitcnt lgkmcnt(0)
	v_max_f32_e32 v33, v33, v33
	v_max_f32_e32 v32, v32, v33
	ds_bpermute_b32 v33, v37, v32
	v_bfi_b32 v66, s90, v75, v74
	v_mul_f32_e32 v29, 0.5, v29
	v_bfi_b32 v7, s90, v65, v7
	v_add_f32_e32 v34, 1.0, v66
	s_waitcnt lgkmcnt(0)
	v_max_f32_e32 v33, v33, v33
	v_max_f32_e32 v32, v32, v33
	ds_bpermute_b32 v33, v38, v32
	v_mul_f32_e32 v3, 0.5, v3
	v_add_f32_e32 v7, 1.0, v7
	v_mul_f32_e32 v29, v29, v34
	v_mul_f32_e32 v3, v3, v7
	s_waitcnt lgkmcnt(0)
	v_max_f32_e32 v9, v33, v33
	v_max_f32_e32 v9, v32, v9
	ds_bpermute_b32 v32, v39, v9
	v_mul_f32_e32 v7, v95, v29
	v_mul_f32_e32 v3, v27, v3
	v_bfi_b32 v31, s90, v70, v69
	v_mul_f32_e32 v2, 0.5, v2
	s_waitcnt lgkmcnt(0)
	v_max_f32_e32 v29, v32, v32
	v_max_f32_e32 v9, v9, v29
	ds_bpermute_b32 v29, v40, v9
	v_add_f32_e32 v31, 1.0, v31
	v_mul_f32_e32 v2, v2, v31
	v_mul_f32_e32 v2, v76, v2
	s_waitcnt vmcnt(1)
	v_mul_f32_e32 v2, v6, v2
	s_waitcnt lgkmcnt(0)
	v_max_f32_e32 v27, v29, v29
	v_max_f32_e32 v9, v9, v27
	ds_bpermute_b32 v27, v41, v9
	v_mul_f32_e32 v6, v26, v7
	v_bfi_b32 v70, s90, v83, v82
	v_mul_f32_e32 v69, 0.5, v81
	v_bfi_b32 v71, s90, v100, v99
	s_waitcnt lgkmcnt(0)
	v_max_f32_e32 v26, v27, v27
	v_max_f32_e32 v9, v9, v26
	v_div_scale_f32 v26, s[28:29], v9, v9, s82
	v_rcp_f32_e32 v27, v26
	v_add_f32_e32 v35, 1.0, v70
	v_mul_f32_e32 v4, 0.5, v4
	v_add_f32_e32 v65, 1.0, v71
	v_mul_f32_e32 v31, v69, v35
	v_mul_f32_e32 v4, v4, v65
	v_mul_f32_e32 v31, v94, v31
	v_mul_f32_e32 v4, v111, v4
	v_mul_f32_e32 v7, v28, v31
	v_fma_f32 v28, -v26, v27, 1.0
	v_mul_f32_e32 v4, v8, v4
	v_div_scale_f32 v8, vcc, s82, v9, s82
	v_fmac_f32_e32 v27, v28, v27
	v_mul_f32_e32 v28, v8, v27
	v_fma_f32 v29, -v26, v28, v8
	v_fmac_f32_e32 v28, v29, v27
	v_fma_f32 v8, -v26, v28, v8
	v_div_fmas_f32 v8, v8, v27, v28
	v_mul_f32_e32 v5, v112, v5
	v_div_fixup_f32 v8, v8, v9, s82
	v_cmp_lt_f32_e32 vcc, 0, v9
	v_mul_f32_e32 v5, v93, v5
	v_max_f32_e64 v31, |v4|, |v5|
	v_cndmask_b32_e32 v8, 0, v8, vcc
	v_fmaak_f32 v26, v24, v8, 0x4b400000
	ds_bpermute_b32 v27, v10, v26
	ds_bpermute_b32 v28, v45, v26
	ds_bpermute_b32 v32, v36, v31
	s_waitcnt vmcnt(0)
	v_mul_f32_e32 v3, v30, v3
	ds_bpermute_b32 v29, v46, v26
	ds_bpermute_b32 v30, v47, v26
	s_waitcnt lgkmcnt(3)
	v_perm_b32 v27, v28, v27, s83
	s_waitcnt lgkmcnt(2)
	v_max_f32_e32 v28, v32, v32
	v_max_f32_e32 v28, v31, v28
	v_mul_f32_e32 v24, 0x3c010204, v9
	s_waitcnt lgkmcnt(0)
	v_perm_b32 v9, v30, v29, s83
	ds_bpermute_b32 v29, v37, v28
	v_fmaak_f32 v8, v25, v8, 0x4b400000
	v_perm_b32 v73, v9, v27, s84
	ds_bpermute_b32 v30, v48, v26
	ds_bpermute_b32 v31, v49, v26
	s_waitcnt lgkmcnt(2)
	v_max_f32_e32 v29, v29, v29
	v_max_f32_e32 v28, v28, v29
	ds_bpermute_b32 v29, v38, v28
	ds_bpermute_b32 v32, v50, v26
	ds_bpermute_b32 v26, v51, v26
	v_mov_b32_e32 v65, 0
	s_mov_b32 s39, 0
	s_waitcnt lgkmcnt(2)
	v_max_f32_e32 v25, v29, v29
	v_max_f32_e32 v25, v28, v25
	ds_bpermute_b32 v27, v39, v25
	s_waitcnt lgkmcnt(1)
	v_perm_b32 v9, v26, v32, s83
	v_perm_b32 v26, v31, v30, s83
	ds_bpermute_b32 v28, v10, v8
	ds_bpermute_b32 v29, v45, v8
	s_waitcnt lgkmcnt(2)
	v_max_f32_e32 v27, v27, v27
	ds_bpermute_b32 v30, v46, v8
	ds_bpermute_b32 v31, v47, v8
	v_max_f32_e32 v25, v25, v27
	ds_bpermute_b32 v27, v40, v25
	v_perm_b32 v74, v9, v26, s84
	s_waitcnt lgkmcnt(3)
	v_perm_b32 v26, v29, v28, s83
	s_waitcnt lgkmcnt(1)
	v_perm_b32 v9, v31, v30, s83
	v_perm_b32 v75, v9, v26, s84
	s_waitcnt lgkmcnt(0)
	v_max_f32_e32 v9, v27, v27
	v_max_f32_e32 v9, v25, v9
	ds_bpermute_b32 v25, v41, v9
	ds_bpermute_b32 v26, v48, v8
	ds_bpermute_b32 v27, v49, v8
	ds_bpermute_b32 v28, v50, v8
	ds_bpermute_b32 v8, v51, v8
	s_waitcnt lgkmcnt(4)
	v_max_f32_e32 v25, v25, v25
	v_max_f32_e32 v9, v9, v25
	v_div_scale_f32 v25, s[28:29], v9, v9, s82
	v_rcp_f32_e32 v29, v25
	s_waitcnt lgkmcnt(0)
	v_perm_b32 v8, v8, v28, s83
	v_perm_b32 v26, v27, v26, s83
	v_perm_b32 v76, v8, v26, s84
	v_fma_f32 v8, -v25, v29, 1.0
	v_fmac_f32_e32 v29, v8, v29
	v_div_scale_f32 v8, vcc, s82, v9, s82
	v_mul_f32_e32 v26, v8, v29
	v_fma_f32 v27, -v25, v26, v8
	v_fmac_f32_e32 v26, v27, v29
	v_fma_f32 v8, -v25, v26, v8
	v_div_fmas_f32 v8, v8, v29, v26
	v_div_fixup_f32 v8, v8, v9, s82
	v_cmp_lt_f32_e32 vcc, 0, v9
	v_max_f32_e64 v28, |v7|, |v6|
	ds_bpermute_b32 v29, v36, v28
	v_cndmask_b32_e32 v8, 0, v8, vcc
	v_fmaak_f32 v4, v4, v8, 0x4b400000
	ds_bpermute_b32 v25, v46, v4
	ds_bpermute_b32 v27, v47, v4
	v_mul_f32_e32 v26, 0x3c010204, v9
	ds_bpermute_b32 v9, v10, v4
	ds_bpermute_b32 v30, v45, v4
	v_fmaak_f32 v5, v5, v8, 0x4b400000
	s_waitcnt lgkmcnt(2)
	v_perm_b32 v25, v27, v25, s83
	v_max_f32_e32 v27, v29, v29
	v_max_f32_e32 v27, v28, v27
	ds_bpermute_b32 v28, v37, v27
	s_waitcnt lgkmcnt(1)
; __device__ __forceinline__ float gelu_tanh(float x) { const float u = 0.7978845608028654f * (x + 0.044715f * x * x * x); return 0.5f * x * (1.0f + tanhf(u)); }
; __device__ __forceinline__ void peer_expert_phase(const Args& a, int layer, LAS unsigned char* lds, int G, int bid) {
;     ...
;             wa[i] = ga * gelu_tanh(pa[i] * SCU[ea[i]] * rx) * SCV[ea[i]]; wb[i] = gb * gelu_tanh(pb[i] * SCU[eb[i]] * rx) * SCV[eb[i]]; ssq[i] = 0.f; }
;         unsigned W4[4][4]; float wsc[4];
; #pragma unroll
;         for (int i = 0; i < 4; ++i) { const float wm = wave_max(fmaxf(fabsf(wa[i]), fabsf(wb[i]))); const float qw = wm > 0.f ? 127.0f / wm : 0.f; wsc[i] = wm * (1.0f / 127.0f);
;             const unsigned qa = __float_as_uint(wa[i] * qw + 12582912.0f), qb = __float_as_uint(wb[i] * qw + 12582912.0f);
; #pragma unroll
;             for (int G4 = 0; G4 < 4; ++G4) { unsigned t[4];
; #pragma unroll
;                 for (int k = 0; k < 4; ++k) { const int c = 4 * G4 + k; t[k] = (unsigned)__shfl((int)(c < 8 ? qa : qb), (8 * c + g8) & 63); }
;                 W4[i][G4] = __builtin_amdgcn_perm(__builtin_amdgcn_perm(t[3], t[2], 0x0c0c0400u), __builtin_amdgcn_perm(t[1], t[0], 0x0c0c0400u), 0x05040100u); } }
;         float* HO = a.out;
; #pragma unroll 1
;         for (int sidx = 0; sidx < 32; ++sidx) { const int s = (sidx + srot) & 31; const unsigned char* pvs = PV + s * 128; const f32x2 gsl = *(const f32x2*)(gnext + s * 128 + 16 * l7 + 2 * g8);
; #pragma unroll
;             for (int i = 0; i < 4; ++i) {
;                 int tok = tb + i * NGW; const bool ok = tok < NTOK; tok = ok ? tok : tb;
;                 u32x4 r[16];
; #pragma unroll
;                 for (int c = 0; c < 16; ++c) { const unsigned eo = (unsigned)__shfl((int)(c < 8 ? eoa[i] : eob[i]), (8 * c + g8) & 63); r[c] = *(const u32x4*)(pvs + (eo + lo16)); }
	v_perm_b32 v9, v30, v9, s83
	v_perm_b32 v77, v25, v9, s84
	ds_bpermute_b32 v9, v50, v4
	ds_bpermute_b32 v25, v51, v4
	s_waitcnt lgkmcnt(2)
	v_max_f32_e32 v28, v28, v28
	v_max_f32_e32 v27, v27, v28
	ds_bpermute_b32 v28, v38, v27
	ds_bpermute_b32 v29, v48, v4
	s_waitcnt lgkmcnt(2)
	v_perm_b32 v9, v25, v9, s83
	ds_bpermute_b32 v4, v49, v4
	ds_bpermute_b32 v30, v46, v5
	s_waitcnt lgkmcnt(3)
	v_max_f32_e32 v8, v28, v28
	v_max_f32_e32 v8, v27, v8
	ds_bpermute_b32 v25, v39, v8
	ds_bpermute_b32 v31, v47, v5
	ds_bpermute_b32 v27, v10, v5
	ds_bpermute_b32 v28, v45, v5
	s_waitcnt lgkmcnt(5)
	v_perm_b32 v4, v4, v29, s83
	s_waitcnt lgkmcnt(3)
	v_max_f32_e32 v25, v25, v25
	v_max_f32_e32 v8, v8, v25
	ds_bpermute_b32 v25, v40, v8
	v_perm_b32 v78, v9, v4, s84
	s_waitcnt lgkmcnt(3)
	v_perm_b32 v4, v31, v30, s83
	s_waitcnt lgkmcnt(1)
	v_perm_b32 v9, v28, v27, s83
	ds_bpermute_b32 v27, v48, v5
	s_waitcnt lgkmcnt(1)
	v_max_f32_e32 v25, v25, v25
	v_max_f32_e32 v8, v8, v25
	ds_bpermute_b32 v25, v41, v8
	ds_bpermute_b32 v28, v49, v5
	ds_bpermute_b32 v29, v50, v5
	ds_bpermute_b32 v5, v51, v5
	v_perm_b32 v79, v4, v9, s84
	s_waitcnt lgkmcnt(3)
	v_max_f32_e32 v25, v25, v25
	v_max_f32_e32 v8, v8, v25
	v_div_scale_f32 v25, s[28:29], v8, v8, s82
	v_rcp_f32_e32 v30, v25
	s_waitcnt lgkmcnt(0)
	v_perm_b32 v4, v5, v29, s83
	v_perm_b32 v5, v28, v27, s83
	v_max_f32_e64 v31, |v2|, |v3|
	v_fma_f32 v9, -v25, v30, 1.0
	v_fmac_f32_e32 v30, v9, v30
	v_div_scale_f32 v9, vcc, s82, v8, s82
	v_mul_f32_e32 v27, v9, v30
	v_fma_f32 v28, -v25, v27, v9
	v_fmac_f32_e32 v27, v28, v30
	v_fma_f32 v9, -v25, v27, v9
	v_div_fmas_f32 v9, v9, v30, v27
	v_div_fixup_f32 v9, v9, v8, s82
	v_cmp_lt_f32_e32 vcc, 0, v8
	ds_bpermute_b32 v32, v36, v31
	v_mul_f32_e32 v28, 0x3c010204, v8
	v_cndmask_b32_e32 v9, 0, v9, vcc
	v_fmaak_f32 v7, v7, v9, 0x4b400000
	ds_bpermute_b32 v25, v10, v7
	ds_bpermute_b32 v27, v45, v7
	s_waitcnt lgkmcnt(2)
	v_max_f32_e32 v8, v32, v32
	v_max_f32_e32 v8, v31, v8
	v_perm_b32 v80, v4, v5, s84
	ds_bpermute_b32 v29, v46, v7
	s_waitcnt lgkmcnt(1)
	v_perm_b32 v5, v27, v25, s83
	ds_bpermute_b32 v25, v37, v8
	ds_bpermute_b32 v30, v47, v7
	ds_bpermute_b32 v27, v48, v7
	v_fmaak_f32 v6, v6, v9, 0x4b400000
	ds_bpermute_b32 v9, v10, v6
	s_waitcnt lgkmcnt(3)
	v_max_f32_e32 v25, v25, v25
	v_max_f32_e32 v8, v8, v25
	s_waitcnt lgkmcnt(2)
	v_perm_b32 v4, v30, v29, s83
	ds_bpermute_b32 v29, v49, v7
	ds_bpermute_b32 v30, v50, v7
	ds_bpermute_b32 v7, v51, v7
	ds_bpermute_b32 v25, v38, v8
	v_perm_b32 v81, v4, v5, s84
	s_waitcnt lgkmcnt(3)
	v_perm_b32 v5, v29, v27, s83
	ds_bpermute_b32 v27, v46, v6
	s_waitcnt lgkmcnt(2)
	v_perm_b32 v4, v7, v30, s83
	s_waitcnt lgkmcnt(1)
	v_max_f32_e32 v7, v25, v25
	v_max_f32_e32 v7, v8, v7
	ds_bpermute_b32 v8, v39, v7
	ds_bpermute_b32 v25, v45, v6
	ds_bpermute_b32 v29, v47, v6
	v_perm_b32 v82, v4, v5, s84
	v_mov_b32_e32 v66, 0
	s_waitcnt lgkmcnt(2)
	v_max_f32_e32 v8, v8, v8
	v_max_f32_e32 v7, v7, v8
	ds_bpermute_b32 v8, v40, v7
	s_waitcnt lgkmcnt(1)
	v_perm_b32 v4, v29, v27, s83
	v_perm_b32 v5, v25, v9, s83
	v_perm_b32 v83, v4, v5, s84
	ds_bpermute_b32 v9, v50, v6
	s_waitcnt lgkmcnt(1)
	v_max_f32_e32 v4, v8, v8
	v_max_f32_e32 v4, v7, v4
	ds_bpermute_b32 v5, v41, v4
	ds_bpermute_b32 v7, v48, v6
	ds_bpermute_b32 v8, v49, v6
	ds_bpermute_b32 v6, v51, v6
	v_mov_b32_e32 v29, v28
	s_waitcnt lgkmcnt(3)
	v_max_f32_e32 v5, v5, v5
	v_max_f32_e32 v4, v4, v5
	v_div_scale_f32 v5, s[28:29], v4, v4, s82
	v_rcp_f32_e32 v25, v5
	s_waitcnt lgkmcnt(0)
	v_perm_b32 v6, v6, v9, s83
	v_perm_b32 v7, v8, v7, s83
	v_perm_b32 v84, v6, v7, s84
	v_fma_f32 v6, -v5, v25, 1.0
	v_fmac_f32_e32 v25, v6, v25
	v_div_scale_f32 v6, vcc, s82, v4, s82
	v_mul_f32_e32 v7, v6, v25
	v_fma_f32 v8, -v5, v7, v6
	v_fmac_f32_e32 v7, v8, v25
	v_fma_f32 v5, -v5, v7, v6
	v_div_fmas_f32 v5, v5, v25, v7
	v_div_fixup_f32 v5, v5, v4, s82
	v_cmp_lt_f32_e32 vcc, 0, v4
	v_mul_f32_e32 v30, 0x3c010204, v4
	v_mov_b32_e32 v31, v30
	v_cndmask_b32_e32 v5, 0, v5, vcc
	v_fmaak_f32 v2, v2, v5, 0x4b400000
	ds_bpermute_b32 v4, v10, v2
	ds_bpermute_b32 v6, v45, v2
	ds_bpermute_b32 v7, v46, v2
	ds_bpermute_b32 v8, v47, v2
	ds_bpermute_b32 v9, v48, v2
	ds_bpermute_b32 v25, v50, v2
	ds_bpermute_b32 v27, v51, v2
	ds_bpermute_b32 v2, v49, v2
	s_waitcnt lgkmcnt(4)
	v_perm_b32 v7, v8, v7, s83
	v_perm_b32 v4, v6, v4, s83
	v_perm_b32 v85, v7, v4, s84
	s_waitcnt lgkmcnt(1)
	v_perm_b32 v4, v27, v25, s83
	s_waitcnt lgkmcnt(0)
	v_perm_b32 v2, v2, v9, s83
	v_perm_b32 v86, v4, v2, s84
	v_fmaak_f32 v2, v3, v5, 0x4b400000
	ds_bpermute_b32 v3, v10, v2
	ds_bpermute_b32 v4, v45, v2
	ds_bpermute_b32 v5, v46, v2
	ds_bpermute_b32 v6, v47, v2
	ds_bpermute_b32 v7, v48, v2
	ds_bpermute_b32 v8, v50, v2
	ds_bpermute_b32 v9, v51, v2
	ds_bpermute_b32 v2, v49, v2
	s_waitcnt lgkmcnt(4)
	v_perm_b32 v5, v6, v5, s83
	v_perm_b32 v3, v4, v3, s83
	v_perm_b32 v87, v5, v3, s84
	s_waitcnt lgkmcnt(1)
	v_perm_b32 v3, v9, v8, s83
	s_waitcnt lgkmcnt(0)
	v_perm_b32 v2, v2, v7, s83
	v_perm_b32 v88, v3, v2, s84
	v_mov_b32_e32 v25, v24
	v_mov_b32_e32 v27, v26
	v_mov_b32_e32 v67, 0
	v_mov_b32_e32 v68, 0
	v_mov_b32_e32 v69, 0
	v_mov_b32_e32 v70, 0
	v_mov_b32_e32 v71, 0
	v_mov_b32_e32 v72, 0
	ds_bpermute_b32 v157, v10, v57
	ds_bpermute_b32 v158, v45, v57
	ds_bpermute_b32 v159, v46, v57
	ds_bpermute_b32 v160, v47, v57
	ds_bpermute_b32 v161, v48, v57
	ds_bpermute_b32 v162, v49, v57
	ds_bpermute_b32 v163, v50, v57
	ds_bpermute_b32 v164, v51, v57
	s_waitcnt lgkmcnt(7)
; __device__ __forceinline__ void peer_expert_phase(const Args& a, int layer, LAS unsigned char* lds, int G, int bid) {
;     ...
; #pragma unroll 1
;         for (int sidx = 0; sidx < 32; ++sidx) { const int s = (sidx + srot) & 31; const unsigned char* pvs = PV + s * 128; const f32x2 gsl = *(const f32x2*)(gnext + s * 128 + 16 * l7 + 2 * g8);
; #pragma unroll
;             for (int i = 0; i < 4; ++i) {
;                 int tok = tb + i * NGW; const bool ok = tok < NTOK; tok = ok ? tok : tb;
;                 u32x4 r[16];
; #pragma unroll
;                 for (int c = 0; c < 16; ++c) { const unsigned eo = (unsigned)__shfl((int)(c < 8 ? eoa[i] : eob[i]), (8 * c + g8) & 63); r[c] = *(const u32x4*)(pvs + (eo + lo16)); }
	v_add_u32_e32 v157, v157, v42
	s_waitcnt lgkmcnt(6)
	v_add_u32_e32 v158, v158, v42
	s_waitcnt lgkmcnt(5)
	v_add_u32_e32 v159, v159, v42
	s_waitcnt lgkmcnt(4)
	v_add_u32_e32 v160, v160, v42
	s_waitcnt lgkmcnt(3)
	v_add_u32_e32 v161, v161, v42
	s_waitcnt lgkmcnt(2)
	v_add_u32_e32 v162, v162, v42
	s_waitcnt lgkmcnt(1)
	v_add_u32_e32 v163, v163, v42
	s_waitcnt lgkmcnt(0)
	v_add_u32_e32 v164, v164, v42
	ds_bpermute_b32 v165, v10, v58
	ds_bpermute_b32 v166, v45, v58
	ds_bpermute_b32 v167, v46, v58
	ds_bpermute_b32 v168, v47, v58
	ds_bpermute_b32 v169, v48, v58
	ds_bpermute_b32 v170, v49, v58
	ds_bpermute_b32 v171, v50, v58
	ds_bpermute_b32 v172, v51, v58
	s_waitcnt lgkmcnt(7)
	v_add_u32_e32 v165, v165, v42
	s_waitcnt lgkmcnt(6)
	v_add_u32_e32 v166, v166, v42
	s_waitcnt lgkmcnt(5)
	v_add_u32_e32 v167, v167, v42
	s_waitcnt lgkmcnt(4)
	v_add_u32_e32 v168, v168, v42
	s_waitcnt lgkmcnt(3)
	v_add_u32_e32 v169, v169, v42
	s_waitcnt lgkmcnt(2)
	v_add_u32_e32 v170, v170, v42
	s_waitcnt lgkmcnt(1)
	v_add_u32_e32 v171, v171, v42
	s_waitcnt lgkmcnt(0)
	v_add_u32_e32 v172, v172, v42
	ds_bpermute_b32 v173, v10, v59
	ds_bpermute_b32 v174, v45, v59
	ds_bpermute_b32 v175, v46, v59
	ds_bpermute_b32 v176, v47, v59
	ds_bpermute_b32 v177, v48, v59
	ds_bpermute_b32 v178, v49, v59
	ds_bpermute_b32 v179, v50, v59
	ds_bpermute_b32 v180, v51, v59
	s_waitcnt lgkmcnt(7)
	v_add_u32_e32 v173, v173, v42
	s_waitcnt lgkmcnt(6)
	v_add_u32_e32 v174, v174, v42
	s_waitcnt lgkmcnt(5)
	v_add_u32_e32 v175, v175, v42
	s_waitcnt lgkmcnt(4)
	v_add_u32_e32 v176, v176, v42
	s_waitcnt lgkmcnt(3)
	v_add_u32_e32 v177, v177, v42
	s_waitcnt lgkmcnt(2)
	v_add_u32_e32 v178, v178, v42
	s_waitcnt lgkmcnt(1)
	v_add_u32_e32 v179, v179, v42
	s_waitcnt lgkmcnt(0)
	v_add_u32_e32 v180, v180, v42
	ds_bpermute_b32 v181, v10, v60
	ds_bpermute_b32 v182, v45, v60
	ds_bpermute_b32 v183, v46, v60
	ds_bpermute_b32 v184, v47, v60
	ds_bpermute_b32 v185, v48, v60
	ds_bpermute_b32 v186, v49, v60
	ds_bpermute_b32 v187, v50, v60
	ds_bpermute_b32 v188, v51, v60
	s_waitcnt lgkmcnt(7)
	v_add_u32_e32 v181, v181, v42
	s_waitcnt lgkmcnt(6)
	v_add_u32_e32 v182, v182, v42
	s_waitcnt lgkmcnt(5)
	v_add_u32_e32 v183, v183, v42
	s_waitcnt lgkmcnt(4)
	v_add_u32_e32 v184, v184, v42
	s_waitcnt lgkmcnt(3)
	v_add_u32_e32 v185, v185, v42
	s_waitcnt lgkmcnt(2)
	v_add_u32_e32 v186, v186, v42
	s_waitcnt lgkmcnt(1)
	v_add_u32_e32 v187, v187, v42
	s_waitcnt lgkmcnt(0)
	v_add_u32_e32 v188, v188, v42
	ds_bpermute_b32 v189, v10, v61
	ds_bpermute_b32 v190, v45, v61
	ds_bpermute_b32 v191, v46, v61
	ds_bpermute_b32 v192, v47, v61
	ds_bpermute_b32 v193, v48, v61
	ds_bpermute_b32 v194, v49, v61
	ds_bpermute_b32 v195, v50, v61
	ds_bpermute_b32 v196, v51, v61
	s_waitcnt lgkmcnt(7)
	v_add_u32_e32 v189, v189, v42
	s_waitcnt lgkmcnt(6)
	v_add_u32_e32 v190, v190, v42
	s_waitcnt lgkmcnt(5)
	v_add_u32_e32 v191, v191, v42
	s_waitcnt lgkmcnt(4)
	v_add_u32_e32 v192, v192, v42
	s_waitcnt lgkmcnt(3)
	v_add_u32_e32 v193, v193, v42
	s_waitcnt lgkmcnt(2)
	v_add_u32_e32 v194, v194, v42
	s_waitcnt lgkmcnt(1)
	v_add_u32_e32 v195, v195, v42
	s_waitcnt lgkmcnt(0)
	v_add_u32_e32 v196, v196, v42
	ds_bpermute_b32 v197, v10, v62
	ds_bpermute_b32 v198, v45, v62
	ds_bpermute_b32 v199, v46, v62
	ds_bpermute_b32 v200, v47, v62
	ds_bpermute_b32 v201, v48, v62
	ds_bpermute_b32 v202, v49, v62
	ds_bpermute_b32 v203, v50, v62
	ds_bpermute_b32 v204, v51, v62
	s_waitcnt lgkmcnt(7)
	v_add_u32_e32 v197, v197, v42
	s_waitcnt lgkmcnt(6)
	v_add_u32_e32 v198, v198, v42
	s_waitcnt lgkmcnt(5)
	v_add_u32_e32 v199, v199, v42
	s_waitcnt lgkmcnt(4)
	v_add_u32_e32 v200, v200, v42
	s_waitcnt lgkmcnt(3)
	v_add_u32_e32 v201, v201, v42
	s_waitcnt lgkmcnt(2)
	v_add_u32_e32 v202, v202, v42
	s_waitcnt lgkmcnt(1)
	v_add_u32_e32 v203, v203, v42
	s_waitcnt lgkmcnt(0)
	v_add_u32_e32 v204, v204, v42
	ds_bpermute_b32 v205, v10, v63
	ds_bpermute_b32 v206, v45, v63
	ds_bpermute_b32 v207, v46, v63
	ds_bpermute_b32 v208, v47, v63
	ds_bpermute_b32 v209, v48, v63
	ds_bpermute_b32 v210, v49, v63
	ds_bpermute_b32 v211, v50, v63
	ds_bpermute_b32 v212, v51, v63
	s_waitcnt lgkmcnt(7)
	v_add_u32_e32 v205, v205, v42
	s_waitcnt lgkmcnt(6)
	v_add_u32_e32 v206, v206, v42
	s_waitcnt lgkmcnt(5)
	v_add_u32_e32 v207, v207, v42
	s_waitcnt lgkmcnt(4)
	v_add_u32_e32 v208, v208, v42
	s_waitcnt lgkmcnt(3)
	v_add_u32_e32 v209, v209, v42
	s_waitcnt lgkmcnt(2)
	v_add_u32_e32 v210, v210, v42
	s_waitcnt lgkmcnt(1)
	v_add_u32_e32 v211, v211, v42
	s_waitcnt lgkmcnt(0)
	v_add_u32_e32 v212, v212, v42
	ds_bpermute_b32 v213, v10, v64
	ds_bpermute_b32 v214, v45, v64
	ds_bpermute_b32 v215, v46, v64
	ds_bpermute_b32 v216, v47, v64
	ds_bpermute_b32 v217, v48, v64
	ds_bpermute_b32 v218, v49, v64
	ds_bpermute_b32 v219, v50, v64
	ds_bpermute_b32 v220, v51, v64
	s_waitcnt lgkmcnt(7)
	v_add_u32_e32 v213, v213, v42
	s_waitcnt lgkmcnt(6)
	v_add_u32_e32 v214, v214, v42
	s_waitcnt lgkmcnt(5)
	v_add_u32_e32 v215, v215, v42
	s_waitcnt lgkmcnt(4)
	v_add_u32_e32 v216, v216, v42
	s_waitcnt lgkmcnt(3)
	v_add_u32_e32 v217, v217, v42
	s_waitcnt lgkmcnt(2)
	v_add_u32_e32 v218, v218, v42
	s_waitcnt lgkmcnt(1)
	v_add_u32_e32 v219, v219, v42
	s_waitcnt lgkmcnt(0)
	v_add_u32_e32 v220, v220, v42
	s_branch .LBB0_1241

; __device__ __forceinline__ void peer_expert_phase(const Args& a, int layer, LAS unsigned char* lds, int G, int bid) {
;     ...
;         for (int sidx = 0; sidx < 32; ++sidx) { const int s = (sidx + srot) & 31; const unsigned char* pvs = PV + s * 128; const f32x2 gsl = *(const f32x2*)(gnext + s * 128 + 16 * l7 + 2 * g8);
; #pragma unroll
;             for (int i = 0; i < 4; ++i) {
;                 int tok = tb + i * NGW; const bool ok = tok < NTOK; tok = ok ? tok : tb;
;                 u32x4 r[16];
; #pragma unroll
;                 for (int c = 0; c < 16; ++c) { const unsigned eo = (unsigned)__shfl((int)(c < 8 ? eoa[i] : eob[i]), (8 * c + g8) & 63); r[c] = *(const u32x4*)(pvs + (eo + lo16)); }
;                 int iac[16];
; #pragma unroll
;                 for (int q = 0; q < 16; ++q) iac[q] = 0;
; #pragma unroll
;                 for (int G4 = 0; G4 < 4; ++G4)
; #pragma unroll
;                     for (int q = 0; q < 4; ++q) {
;                         const unsigned a_ = r[4 * G4][q], b_ = r[4 * G4 + 1][q], c_ = r[4 * G4 + 2][q], d_ = r[4 * G4 + 3][q];
;                         const unsigned ablo = __builtin_amdgcn_perm(b_, a_, 0x05010400u), abhi = __builtin_amdgcn_perm(b_, a_, 0x07030602u), cdlo = __builtin_amdgcn_perm(d_, c_, 0x05010400u), cdhi = __builtin_amdgcn_perm(d_, c_, 0x07030602u);
;                         iac[4 * q + 0] = __builtin_amdgcn_sdot4((int)__builtin_amdgcn_perm(cdlo, ablo, 0x05040100u), (int)W4[i][G4], iac[4 * q + 0], false);
;                         iac[4 * q + 1] = __builtin_amdgcn_sdot4((int)__builtin_amdgcn_perm(cdlo, ablo, 0x07060302u), (int)W4[i][G4], iac[4 * q + 1], false);
;                         iac[4 * q + 2] = __builtin_amdgcn_sdot4((int)__builtin_amdgcn_perm(cdhi, abhi, 0x05040100u), (int)W4[i][G4], iac[4 * q + 2], false);
;                         iac[4 * q + 3] = __builtin_amdgcn_sdot4((int)__builtin_amdgcn_perm(cdhi, abhi, 0x07060302u), (int)W4[i][G4], iac[4 * q + 3], false); }
.LBB0_1241:
	s_bitcmp0_b32 s39, 7
	s_cbranch_scc0 .Lvbar1_skip
	s_barrier
.Lvbar1_skip:
	s_add_i32 s28, s80, s39
	s_and_b32 s34, s28, 0xf80
	s_lshl_b32 s98, s34, 1
	s_mov_b32 s99, 0
	v_lshl_add_u64 v[230:231], v[22:23], 0, s[98:99]
	v_lshl_add_u64 v[232:233], v[230:231], 0, s[30:31]
	global_load_dword v240, v[232:233], off
	v_lshl_add_u64 v[234:235], v[230:231], 0, s[54:55]
	global_load_dword v241, v[234:235], off
	v_lshl_add_u64 v[236:237], v[230:231], 0, s[58:59]
	global_load_dword v242, v[236:237], off
	v_lshl_add_u64 v[238:239], v[230:231], 0, s[62:63]
	global_load_dword v243, v[238:239], off
	s_add_u32 s28, s73, s34
	s_addc_u32 s29, s74, 0
	s_waitcnt lgkmcnt(0)
	global_load_dwordx4 v[90:93], v157, s[28:29]
	global_load_dwordx4 v[94:97], v158, s[28:29]
	global_load_dwordx4 v[98:101], v159, s[28:29]
	global_load_dwordx4 v[102:105], v160, s[28:29]
	global_load_dwordx4 v[106:109], v161, s[28:29]
	global_load_dwordx4 v[110:113], v162, s[28:29]
	global_load_dwordx4 v[114:117], v163, s[28:29]
	global_load_dwordx4 v[118:121], v164, s[28:29]
	s_lshl_b32 s50, s34, 2
	v_lshl_add_u64 v[2:3], v[20:21], 0, s[50:51]
	global_load_dwordx2 v[32:33], v[2:3], off
	global_load_dwordx4 v[122:125], v165, s[28:29]
	global_load_dwordx4 v[126:129], v166, s[28:29]
	global_load_dwordx4 v[130:133], v167, s[28:29]
	global_load_dwordx4 v[134:137], v168, s[28:29]
	global_load_dwordx4 v[138:141], v169, s[28:29]
	global_load_dwordx4 v[142:145], v170, s[28:29]
	s_nop 0
	global_load_dwordx4 v[2:5], v171, s[28:29]
	s_nop 0
	global_load_dwordx4 v[6:9], v172, s[28:29]
	v_mov_b32_e32 v147, 0
	v_mov_b32_e32 v153, 0
	v_mov_b32_e32 v148, 0
	v_mov_b32_e32 v151, 0
	v_mov_b32_e32 v149, 0
	v_mov_b32_e32 v150, 0
	v_mov_b32_e32 v146, 0
	v_mov_b32_e32 v152, 0
	s_lshl_b32 s50, s34, 1
	v_lshl_add_u64 v[34:35], v[22:23], 0, s[50:51]
	s_waitcnt vmcnt(15)
	v_perm_b32 v89, v94, v90, s91
	v_perm_b32 v90, v94, v90, s92
	s_waitcnt vmcnt(13)
	v_perm_b32 v94, v102, v98, s91
	v_perm_b32 v98, v102, v98, s92
	v_perm_b32 v102, v95, v91, s91
	v_perm_b32 v91, v95, v91, s92
	v_perm_b32 v95, v103, v99, s91
	v_perm_b32 v99, v103, v99, s92
	v_perm_b32 v103, v94, v89, s84
	v_perm_b32 v89, v94, v89, s93
	v_perm_b32 v94, v98, v90, s84
	v_perm_b32 v90, v98, v90, s93
	v_perm_b32 v98, v95, v102, s84
	v_perm_b32 v95, v95, v102, s93
	v_perm_b32 v102, v99, v91, s84
	v_perm_b32 v91, v99, v91, s93
	v_dot4c_i32_i8_e32 v147, v89, v73
	v_dot4c_i32_i8_e32 v153, v91, v73
	v_perm_b32 v89, v96, v92, s91
	v_perm_b32 v91, v104, v100, s91
	v_dot4c_i32_i8_e32 v148, v94, v73
	v_dot4c_i32_i8_e32 v151, v95, v73
	v_perm_b32 v94, v91, v89, s84
	v_mov_b32_e32 v95, 0
	v_dot4c_i32_i8_e32 v149, v90, v73
	v_perm_b32 v90, v96, v92, s92
	v_perm_b32 v92, v104, v100, s92
	v_dot4c_i32_i8_e32 v95, v94, v73
	v_perm_b32 v89, v91, v89, s93
	v_mov_b32_e32 v94, 0
	v_dot4c_i32_i8_e32 v94, v89, v73
	v_perm_b32 v89, v92, v90, s84
	v_mov_b32_e32 v96, 0
	v_dot4c_i32_i8_e32 v150, v98, v73
	v_dot4c_i32_i8_e32 v96, v89, v73
	v_perm_b32 v89, v92, v90, s93
	v_mov_b32_e32 v98, 0
	v_dot4c_i32_i8_e32 v98, v89, v73
	v_perm_b32 v89, v97, v93, s91
	v_perm_b32 v91, v105, v101, s91
	v_perm_b32 v90, v97, v93, s92
	v_perm_b32 v92, v105, v101, s92
	v_perm_b32 v93, v91, v89, s84
	v_perm_b32 v89, v91, v89, s93
	v_mov_b32_e32 v97, 0
	v_dot4c_i32_i8_e32 v97, v89, v73
	v_perm_b32 v89, v92, v90, s84
	v_mov_b32_e32 v100, 0
	v_dot4c_i32_i8_e32 v100, v89, v73
	v_perm_b32 v89, v92, v90, s93
	v_mov_b32_e32 v101, 0
	v_mov_b32_e32 v99, 0
	v_dot4c_i32_i8_e32 v101, v89, v73
	s_waitcnt vmcnt(11)
	v_perm_b32 v89, v110, v106, s91
	s_waitcnt vmcnt(9)
	v_perm_b32 v91, v118, v114, s91
	v_dot4c_i32_i8_e32 v99, v93, v73
	v_perm_b32 v90, v110, v106, s92
	v_perm_b32 v92, v118, v114, s92
	v_perm_b32 v93, v91, v89, s84
	v_perm_b32 v89, v91, v89, s93
	v_dot4c_i32_i8_e32 v147, v89, v74
	v_perm_b32 v89, v92, v90, s84
	v_dot4c_i32_i8_e32 v148, v89, v74
	v_perm_b32 v89, v92, v90, s93
	v_dot4c_i32_i8_e32 v146, v103, v73
	v_dot4c_i32_i8_e32 v149, v89, v74
	v_perm_b32 v89, v111, v107, s91
	v_perm_b32 v91, v119, v115, s91
	v_dot4c_i32_i8_e32 v146, v93, v74
	v_perm_b32 v90, v111, v107, s92
	v_perm_b32 v92, v119, v115, s92
	v_perm_b32 v93, v91, v89, s84
	v_perm_b32 v89, v91, v89, s93
	v_dot4c_i32_i8_e32 v152, v102, v73
	v_dot4c_i32_i8_e32 v151, v89, v74
	v_perm_b32 v89, v92, v90, s84
	v_dot4c_i32_i8_e32 v152, v89, v74
	v_perm_b32 v89, v92, v90, s93
	v_dot4c_i32_i8_e32 v153, v89, v74
	v_perm_b32 v89, v112, v108, s91
	v_perm_b32 v91, v120, v116, s91
	v_dot4c_i32_i8_e32 v150, v93, v74
	v_perm_b32 v90, v112, v108, s92
	v_perm_b32 v92, v120, v116, s92
	v_perm_b32 v93, v91, v89, s84
	v_perm_b32 v89, v91, v89, s93
	v_dot4c_i32_i8_e32 v94, v89, v74
	v_perm_b32 v89, v92, v90, s84
	v_dot4c_i32_i8_e32 v96, v89, v74
	v_perm_b32 v89, v92, v90, s93
	v_dot4c_i32_i8_e32 v98, v89, v74
	v_perm_b32 v89, v113, v109, s91
	v_perm_b32 v91, v121, v117, s91
	v_dot4c_i32_i8_e32 v95, v93, v74
	v_perm_b32 v90, v113, v109, s92
	v_perm_b32 v92, v121, v117, s92
	v_perm_b32 v93, v91, v89, s84
	v_perm_b32 v89, v91, v89, s93
	v_dot4c_i32_i8_e32 v97, v89, v74
	v_perm_b32 v89, v92, v90, s84
	v_dot4c_i32_i8_e32 v100, v89, v74
	v_perm_b32 v89, v92, v90, s93
	v_dot4c_i32_i8_e32 v101, v89, v74
	s_waitcnt vmcnt(6)
	v_perm_b32 v89, v126, v122, s91
	s_waitcnt vmcnt(4)
; __device__ __forceinline__ void peer_expert_phase(const Args& a, int layer, LAS unsigned char* lds, int G, int bid) {
;     ...
; #pragma unroll
;                 for (int G4 = 0; G4 < 4; ++G4)
; #pragma unroll
;                     for (int q = 0; q < 4; ++q) {
;                         const unsigned a_ = r[4 * G4][q], b_ = r[4 * G4 + 1][q], c_ = r[4 * G4 + 2][q], d_ = r[4 * G4 + 3][q];
;                         const unsigned ablo = __builtin_amdgcn_perm(b_, a_, 0x05010400u), abhi = __builtin_amdgcn_perm(b_, a_, 0x07030602u), cdlo = __builtin_amdgcn_perm(d_, c_, 0x05010400u), cdhi = __builtin_amdgcn_perm(d_, c_, 0x07030602u);
;                         iac[4 * q + 0] = __builtin_amdgcn_sdot4((int)__builtin_amdgcn_perm(cdlo, ablo, 0x05040100u), (int)W4[i][G4], iac[4 * q + 0], false);
;                         iac[4 * q + 1] = __builtin_amdgcn_sdot4((int)__builtin_amdgcn_perm(cdlo, ablo, 0x07060302u), (int)W4[i][G4], iac[4 * q + 1], false);
;                         iac[4 * q + 2] = __builtin_amdgcn_sdot4((int)__builtin_amdgcn_perm(cdhi, abhi, 0x05040100u), (int)W4[i][G4], iac[4 * q + 2], false);
;                         iac[4 * q + 3] = __builtin_amdgcn_sdot4((int)__builtin_amdgcn_perm(cdhi, abhi, 0x07060302u), (int)W4[i][G4], iac[4 * q + 3], false); }
;                 f32x2 ac[8];
; #pragma unroll
;                 for (int q = 0; q < 8; ++q) ac[q] = (f32x2){(float)iac[2 * q] * wsc[i], (float)iac[2 * q + 1] * wsc[i]};
;                 f32x2 b4_[4], b2_[2], b1_;
; #pragma unroll
;                 for (int q = 0; q < 4; ++q) { const f32x2 snd = (lane & 32) ? ac[q] : ac[q + 4], kp = (lane & 32) ? ac[q + 4] : ac[q]; b4_[q] = (f32x2){kp.x + __shfl_xor(snd.x, 32), kp.y + __shfl_xor(snd.y, 32)}; }
; #pragma unroll
;                 for (int q = 0; q < 2; ++q) { const f32x2 snd = (lane & 16) ? b4_[q] : b4_[q + 2], kp = (lane & 16) ? b4_[q + 2] : b4_[q]; b2_[q] = (f32x2){kp.x + __shfl_xor(snd.x, 16), kp.y + __shfl_xor(snd.y, 16)}; }
;                 { const f32x2 snd = (lane & 8) ? b2_[0] : b2_[1], kp = (lane & 8) ? b2_[1] : b2_[0]; b1_ = (f32x2){kp.x + __shfl_xor(snd.x, 8), kp.y + __shfl_xor(snd.y, 8)}; }
	v_perm_b32 v91, v134, v130, s91
	v_dot4c_i32_i8_e32 v99, v93, v74
	v_perm_b32 v90, v126, v122, s92
	v_perm_b32 v92, v134, v130, s92
	v_perm_b32 v93, v91, v89, s84
	v_perm_b32 v89, v91, v89, s93
	v_dot4c_i32_i8_e32 v147, v89, v75
	v_perm_b32 v89, v92, v90, s84
	v_dot4c_i32_i8_e32 v148, v89, v75
	v_perm_b32 v89, v92, v90, s93
	v_dot4c_i32_i8_e32 v149, v89, v75
	v_perm_b32 v89, v127, v123, s91
	v_perm_b32 v91, v135, v131, s91
	v_dot4c_i32_i8_e32 v146, v93, v75
	v_perm_b32 v90, v127, v123, s92
	v_perm_b32 v92, v135, v131, s92
	v_perm_b32 v93, v91, v89, s84
	v_perm_b32 v89, v91, v89, s93
	v_dot4c_i32_i8_e32 v151, v89, v75
	v_perm_b32 v89, v92, v90, s84
	v_dot4c_i32_i8_e32 v152, v89, v75
	v_perm_b32 v89, v92, v90, s93
	v_dot4c_i32_i8_e32 v153, v89, v75
	v_perm_b32 v89, v128, v124, s91
	v_perm_b32 v91, v136, v132, s91
	v_dot4c_i32_i8_e32 v150, v93, v75
	v_perm_b32 v90, v128, v124, s92
	v_perm_b32 v92, v136, v132, s92
	v_perm_b32 v93, v91, v89, s84
	v_perm_b32 v89, v91, v89, s93
	v_dot4c_i32_i8_e32 v94, v89, v75
	v_perm_b32 v89, v92, v90, s84
	v_dot4c_i32_i8_e32 v96, v89, v75
	v_perm_b32 v89, v92, v90, s93
	v_dot4c_i32_i8_e32 v98, v89, v75
	v_perm_b32 v89, v129, v125, s91
	v_perm_b32 v91, v137, v133, s91
	v_dot4c_i32_i8_e32 v95, v93, v75
	v_perm_b32 v90, v129, v125, s92
	v_perm_b32 v92, v137, v133, s92
	v_perm_b32 v93, v91, v89, s84
	v_perm_b32 v89, v91, v89, s93
	v_dot4c_i32_i8_e32 v97, v89, v75
	v_perm_b32 v89, v92, v90, s84
	v_dot4c_i32_i8_e32 v100, v89, v75
	v_perm_b32 v89, v92, v90, s93
	v_dot4c_i32_i8_e32 v101, v89, v75
	s_waitcnt vmcnt(2)
	v_perm_b32 v89, v142, v138, s91
	s_waitcnt vmcnt(0)
	v_perm_b32 v91, v6, v2, s91
	v_perm_b32 v2, v6, v2, s92
	v_perm_b32 v6, v91, v89, s84
	v_perm_b32 v90, v142, v138, s92
	v_dot4c_i32_i8_e32 v146, v6, v76
	v_perm_b32 v6, v91, v89, s93
	v_dot4c_i32_i8_e32 v147, v6, v76
	v_perm_b32 v6, v2, v90, s84
	v_perm_b32 v2, v2, v90, s93
	v_dot4c_i32_i8_e32 v149, v2, v76
	v_perm_b32 v2, v143, v139, s91
	v_perm_b32 v89, v7, v3, s91
	v_dot4c_i32_i8_e32 v148, v6, v76
	v_perm_b32 v6, v143, v139, s92
	v_perm_b32 v3, v7, v3, s92
	v_perm_b32 v7, v89, v2, s84
	v_perm_b32 v2, v89, v2, s93
	v_dot4c_i32_i8_e32 v151, v2, v76
	v_perm_b32 v2, v3, v6, s84
	v_dot4c_i32_i8_e32 v152, v2, v76
	v_perm_b32 v2, v3, v6, s93
	v_dot4c_i32_i8_e32 v153, v2, v76
	v_perm_b32 v2, v144, v140, s91
	v_perm_b32 v6, v8, v4, s91
	v_dot4c_i32_i8_e32 v150, v7, v76
	v_perm_b32 v3, v144, v140, s92
	v_perm_b32 v4, v8, v4, s92
	v_perm_b32 v7, v6, v2, s84
	v_perm_b32 v2, v6, v2, s93
	v_dot4c_i32_i8_e32 v94, v2, v76
	v_perm_b32 v2, v4, v3, s84
	v_dot4c_i32_i8_e32 v96, v2, v76
	v_perm_b32 v2, v4, v3, s93
	v_dot4c_i32_i8_e32 v98, v2, v76
	v_lshl_add_u64 v[2:3], v[34:35], 0, s[30:31]
	v_dot4c_i32_i8_e32 v95, v7, v76
	v_perm_b32 v4, v145, v141, s91
	v_perm_b32 v7, v9, v5, s91
	v_perm_b32 v6, v145, v141, s92
	v_perm_b32 v5, v9, v5, s92
	v_perm_b32 v8, v7, v4, s84
	v_perm_b32 v4, v7, v4, s93
	v_dot4c_i32_i8_e32 v97, v4, v76
	v_perm_b32 v4, v5, v6, s84
	v_dot4c_i32_i8_e32 v99, v93, v75
	v_dot4c_i32_i8_e32 v100, v4, v76
	v_perm_b32 v4, v5, v6, s93
	v_dot4c_i32_i8_e32 v99, v8, v76
	v_dot4c_i32_i8_e32 v101, v4, v76
	v_cvt_f32_i32_e32 v5, v147
	v_cvt_f32_i32_e32 v4, v146
	v_cvt_f32_i32_e32 v7, v149
	v_cvt_f32_i32_e32 v6, v148
	v_cvt_f32_i32_e32 v93, v94
	v_cvt_f32_i32_e32 v92, v95
	v_cvt_f32_i32_e32 v95, v98
	v_cvt_f32_i32_e32 v94, v96
	v_cvt_f32_i32_e32 v9, v151
	v_cvt_f32_i32_e32 v8, v150
	v_cvt_f32_i32_e32 v91, v153
	v_cvt_f32_i32_e32 v90, v152
	v_cvt_f32_i32_e32 v97, v97
	v_cvt_f32_i32_e32 v96, v99
	v_cvt_f32_i32_e32 v99, v101
	v_cvt_f32_i32_e32 v98, v100
	v_pk_mul_f32 v[4:5], v[24:25], v[4:5]
	v_pk_mul_f32 v[6:7], v[24:25], v[6:7]
	v_pk_mul_f32 v[92:93], v[24:25], v[92:93]
	v_pk_mul_f32 v[94:95], v[24:25], v[94:95]
	v_pk_mul_f32 v[8:9], v[24:25], v[8:9]
	v_pk_mul_f32 v[90:91], v[24:25], v[90:91]
	v_pk_mul_f32 v[96:97], v[24:25], v[96:97]
	v_pk_mul_f32 v[98:99], v[24:25], v[98:99]
	v_cndmask_b32_e64 v101, v5, v93, s[4:5]
	v_cndmask_b32_e64 v5, v93, v5, s[4:5]
	v_cndmask_b32_e64 v93, v7, v95, s[4:5]
	v_cndmask_b32_e64 v100, v4, v92, s[4:5]
	v_cndmask_b32_e64 v102, v6, v94, s[4:5]
	ds_bpermute_b32 v103, v36, v93
	v_cndmask_b32_e64 v4, v92, v4, s[4:5]
	v_cndmask_b32_e64 v7, v95, v7, s[4:5]
	v_cndmask_b32_e64 v6, v94, v6, s[4:5]
	v_cndmask_b32_e64 v93, v9, v97, s[4:5]
	v_cndmask_b32_e64 v92, v8, v96, s[4:5]
	v_cndmask_b32_e64 v95, v91, v99, s[4:5]
	v_cndmask_b32_e64 v94, v90, v98, s[4:5]
	ds_bpermute_b32 v100, v36, v100
	ds_bpermute_b32 v101, v36, v101
	ds_bpermute_b32 v102, v36, v102
	ds_bpermute_b32 v92, v36, v92
	ds_bpermute_b32 v93, v36, v93
	ds_bpermute_b32 v94, v36, v94
	ds_bpermute_b32 v95, v36, v95
	v_cndmask_b32_e64 v9, v97, v9, s[4:5]
	v_cndmask_b32_e64 v8, v96, v8, s[4:5]
	v_cndmask_b32_e64 v91, v99, v91, s[4:5]
	v_cndmask_b32_e64 v90, v98, v90, s[4:5]
	s_waitcnt lgkmcnt(0)
	v_pk_add_f32 v[4:5], v[4:5], v[100:101]
	v_pk_add_f32 v[6:7], v[6:7], v[102:103]
	v_pk_add_f32 v[8:9], v[8:9], v[92:93]
	v_pk_add_f32 v[90:91], v[90:91], v[94:95]
	v_cndmask_b32_e64 v93, v5, v9, s[6:7]
	v_cndmask_b32_e64 v92, v4, v8, s[6:7]
	v_cndmask_b32_e64 v5, v9, v5, s[6:7]
	v_cndmask_b32_e64 v9, v7, v91, s[6:7]
	v_cndmask_b32_e64 v94, v6, v90, s[6:7]
	ds_bpermute_b32 v92, v37, v92
	ds_bpermute_b32 v93, v37, v93
	ds_bpermute_b32 v94, v37, v94
	ds_bpermute_b32 v95, v37, v9
	v_cndmask_b32_e64 v4, v8, v4, s[6:7]
	v_cndmask_b32_e64 v7, v91, v7, s[6:7]
	v_cndmask_b32_e64 v6, v90, v6, s[6:7]
	s_waitcnt lgkmcnt(2)
	v_pk_add_f32 v[4:5], v[4:5], v[92:93]
	s_waitcnt lgkmcnt(0)
	v_pk_add_f32 v[6:7], v[6:7], v[94:95]
	s_waitcnt vmcnt(0)
; __device__ __forceinline__ void peer_expert_phase(const Args& a, int layer, LAS unsigned char* lds, int G, int bid) {
;     ...
;                 for (int c = 0; c < 16; ++c) { const unsigned eo = (unsigned)__shfl((int)(c < 8 ? eoa[i] : eob[i]), (8 * c + g8) & 63); r[c] = *(const u32x4*)(pvs + (eo + lo16)); }
;                 int iac[16];
; #pragma unroll
;                 for (int q = 0; q < 16; ++q) iac[q] = 0;
; #pragma unroll
;                 for (int G4 = 0; G4 < 4; ++G4)
; #pragma unroll
;                     for (int q = 0; q < 4; ++q) {
;                         const unsigned a_ = r[4 * G4][q], b_ = r[4 * G4 + 1][q], c_ = r[4 * G4 + 2][q], d_ = r[4 * G4 + 3][q];
;                         const unsigned ablo = __builtin_amdgcn_perm(b_, a_, 0x05010400u), abhi = __builtin_amdgcn_perm(b_, a_, 0x07030602u), cdlo = __builtin_amdgcn_perm(d_, c_, 0x05010400u), cdhi = __builtin_amdgcn_perm(d_, c_, 0x07030602u);
;                         iac[4 * q + 0] = __builtin_amdgcn_sdot4((int)__builtin_amdgcn_perm(cdlo, ablo, 0x05040100u), (int)W4[i][G4], iac[4 * q + 0], false);
;                         iac[4 * q + 1] = __builtin_amdgcn_sdot4((int)__builtin_amdgcn_perm(cdlo, ablo, 0x07060302u), (int)W4[i][G4], iac[4 * q + 1], false);
;                         iac[4 * q + 2] = __builtin_amdgcn_sdot4((int)__builtin_amdgcn_perm(cdhi, abhi, 0x05040100u), (int)W4[i][G4], iac[4 * q + 2], false);
;                         iac[4 * q + 3] = __builtin_amdgcn_sdot4((int)__builtin_amdgcn_perm(cdhi, abhi, 0x07060302u), (int)W4[i][G4], iac[4 * q + 3], false); }
;                 f32x2 ac[8];
; #pragma unroll
;                 for (int q = 0; q < 8; ++q) ac[q] = (f32x2){(float)iac[2 * q] * wsc[i], (float)iac[2 * q + 1] * wsc[i]};
;                 f32x2 b4_[4], b2_[2], b1_;
; #pragma unroll
;                 for (int q = 0; q < 4; ++q) { const f32x2 snd = (lane & 32) ? ac[q] : ac[q + 4], kp = (lane & 32) ? ac[q + 4] : ac[q]; b4_[q] = (f32x2){kp.x + __shfl_xor(snd.x, 32), kp.y + __shfl_xor(snd.y, 32)}; }
; #pragma unroll
;                 for (int q = 0; q < 2; ++q) { const f32x2 snd = (lane & 16) ? b4_[q] : b4_[q + 2], kp = (lane & 16) ? b4_[q + 2] : b4_[q]; b2_[q] = (f32x2){kp.x + __shfl_xor(snd.x, 16), kp.y + __shfl_xor(snd.y, 16)}; }
	v_and_b32_e32 v90, 0xffff0000, v240
	v_cndmask_b32_e64 v8, v5, v7, s[8:9]
	v_cndmask_b32_e64 v9, v4, v6, s[8:9]
	ds_bpermute_b32 v9, v38, v9
	ds_bpermute_b32 v8, v38, v8
	v_cndmask_b32_e64 v4, v6, v4, s[8:9]
	v_cndmask_b32_e64 v5, v7, v5, s[8:9]
	v_lshlrev_b32_e32 v89, 16, v240
	s_waitcnt lgkmcnt(1)
	v_add_f32_e32 v4, v4, v9
	s_waitcnt lgkmcnt(0)
	v_add_f32_e32 v5, v5, v8
	v_add_f32_e32 v5, v5, v90
	v_add_f32_e32 v4, v4, v89
	v_cvt_pk_bf16_f32 v6, v4, v5
	global_store_dword v[2:3], v6, off
	global_load_dwordx4 v[2:5], v173, s[28:29]
	s_nop 0
	global_load_dwordx4 v[90:93], v174, s[28:29]
	global_load_dwordx4 v[94:97], v175, s[28:29]
	global_load_dwordx4 v[98:101], v176, s[28:29]
	global_load_dwordx4 v[102:105], v177, s[28:29]
	global_load_dwordx4 v[106:109], v178, s[28:29]
	global_load_dwordx4 v[110:113], v179, s[28:29]
	global_load_dwordx4 v[114:117], v180, s[28:29]
	global_load_dwordx4 v[118:121], v181, s[28:29]
	s_nop 0
	global_load_dwordx4 v[122:125], v182, s[28:29]
	s_nop 0
	global_load_dwordx4 v[126:129], v183, s[28:29]
	s_nop 0
	global_load_dwordx4 v[130:133], v184, s[28:29]
	s_nop 0
	global_load_dwordx4 v[134:137], v185, s[28:29]
	s_nop 0
	global_load_dwordx4 v[138:141], v186, s[28:29]
	s_nop 0
	global_load_dwordx4 v[142:145], v187, s[28:29]
	s_nop 0
	global_load_dwordx4 v[146:149], v188, s[28:29]
	v_mov_b32_e32 v7, 0
	v_mov_b32_e32 v8, 0
	v_mov_b32_e32 v154, 0
	v_mov_b32_e32 v151, 0
	v_mov_b32_e32 v153, 0
	v_mov_b32_e32 v89, 0
	v_mov_b32_e32 v152, 0
	v_mov_b32_e32 v150, 0
	v_mov_b32_e32 v9, 0
	v_mov_b32_e32 v155, 0
	s_andn2_b64 vcc, exec, s[52:53]
	s_waitcnt vmcnt(14)
	v_perm_b32 v156, v90, v2, s91
	v_perm_b32 v2, v90, v2, s92
	s_waitcnt vmcnt(12)
	v_perm_b32 v90, v98, v94, s91
	v_perm_b32 v94, v98, v94, s92
	v_perm_b32 v98, v91, v3, s91
	v_perm_b32 v3, v91, v3, s92
	v_perm_b32 v91, v99, v95, s91
	v_perm_b32 v95, v99, v95, s92
	v_perm_b32 v99, v92, v4, s91
	v_perm_b32 v4, v92, v4, s92
	v_perm_b32 v92, v100, v96, s91
	v_perm_b32 v96, v100, v96, s92
	v_perm_b32 v100, v90, v156, s84
	v_perm_b32 v90, v90, v156, s93
	v_perm_b32 v156, v94, v2, s84
	v_perm_b32 v2, v94, v2, s93
	v_perm_b32 v94, v91, v98, s84
	v_perm_b32 v91, v91, v98, s93
	v_perm_b32 v98, v95, v3, s84
	v_perm_b32 v3, v95, v3, s93
	v_perm_b32 v95, v92, v99, s84
	v_dot4c_i32_i8_e32 v7, v2, v77
	v_dot4c_i32_i8_e32 v8, v94, v77
	v_perm_b32 v2, v96, v4, s84
	v_mov_b32_e32 v94, 0
	v_dot4c_i32_i8_e32 v154, v95, v77
	v_dot4c_i32_i8_e32 v94, v2, v77
	v_perm_b32 v2, v96, v4, s93
	v_mov_b32_e32 v95, 0
	v_dot4c_i32_i8_e32 v95, v2, v77
	v_perm_b32 v2, v93, v5, s91
	v_perm_b32 v4, v101, v97, s91
	v_dot4c_i32_i8_e32 v151, v90, v77
	v_dot4c_i32_i8_e32 v153, v3, v77
	v_perm_b32 v3, v93, v5, s92
	v_perm_b32 v5, v101, v97, s92
	v_perm_b32 v90, v4, v2, s84
	v_perm_b32 v2, v4, v2, s93
	v_mov_b32_e32 v97, 0
	v_dot4c_i32_i8_e32 v89, v98, v77
	v_dot4c_i32_i8_e32 v97, v2, v77
	v_perm_b32 v2, v5, v3, s84
	v_mov_b32_e32 v98, 0
	v_perm_b32 v92, v92, v99, s93
	v_dot4c_i32_i8_e32 v98, v2, v77
	v_perm_b32 v2, v5, v3, s93
	v_mov_b32_e32 v99, 0
	v_mov_b32_e32 v96, 0
	v_dot4c_i32_i8_e32 v99, v2, v77
	s_waitcnt vmcnt(10)
	v_perm_b32 v2, v106, v102, s91
	s_waitcnt vmcnt(8)
	v_perm_b32 v4, v114, v110, s91
	v_dot4c_i32_i8_e32 v96, v90, v77
	v_perm_b32 v3, v106, v102, s92
	v_perm_b32 v5, v114, v110, s92
	v_perm_b32 v90, v4, v2, s84
	v_perm_b32 v2, v4, v2, s93
	v_dot4c_i32_i8_e32 v152, v156, v77
	v_dot4c_i32_i8_e32 v151, v2, v78
	v_perm_b32 v2, v5, v3, s84
	v_dot4c_i32_i8_e32 v152, v2, v78
	v_perm_b32 v2, v5, v3, s93
	v_dot4c_i32_i8_e32 v150, v100, v77
	v_dot4c_i32_i8_e32 v7, v2, v78
	v_perm_b32 v2, v107, v103, s91
	v_perm_b32 v4, v115, v111, s91
	v_dot4c_i32_i8_e32 v9, v91, v77
	v_dot4c_i32_i8_e32 v150, v90, v78
	v_perm_b32 v3, v107, v103, s92
	v_perm_b32 v5, v115, v111, s92
	v_perm_b32 v90, v4, v2, s84
	v_perm_b32 v2, v4, v2, s93
	v_dot4c_i32_i8_e32 v9, v2, v78
	v_perm_b32 v2, v5, v3, s84
	v_dot4c_i32_i8_e32 v89, v2, v78
	v_perm_b32 v2, v5, v3, s93
	v_dot4c_i32_i8_e32 v153, v2, v78
	v_perm_b32 v2, v108, v104, s91
	v_perm_b32 v4, v116, v112, s91
	v_dot4c_i32_i8_e32 v155, v92, v77
	v_dot4c_i32_i8_e32 v8, v90, v78
	v_perm_b32 v3, v108, v104, s92
	v_perm_b32 v5, v116, v112, s92
	v_perm_b32 v90, v4, v2, s84
	v_perm_b32 v2, v4, v2, s93
	v_dot4c_i32_i8_e32 v155, v2, v78
	v_perm_b32 v2, v5, v3, s84
	v_dot4c_i32_i8_e32 v94, v2, v78
	v_perm_b32 v2, v5, v3, s93
	v_dot4c_i32_i8_e32 v95, v2, v78
	v_perm_b32 v2, v109, v105, s91
	v_perm_b32 v4, v117, v113, s91
	v_dot4c_i32_i8_e32 v154, v90, v78
	v_perm_b32 v3, v109, v105, s92
	v_perm_b32 v5, v117, v113, s92
	v_perm_b32 v90, v4, v2, s84
	v_perm_b32 v2, v4, v2, s93
	v_dot4c_i32_i8_e32 v97, v2, v78
	v_perm_b32 v2, v5, v3, s84
	v_dot4c_i32_i8_e32 v98, v2, v78
	v_perm_b32 v2, v5, v3, s93
	v_dot4c_i32_i8_e32 v99, v2, v78
	s_waitcnt vmcnt(6)
	v_perm_b32 v2, v122, v118, s91
	s_waitcnt vmcnt(4)
	v_perm_b32 v4, v130, v126, s91
	v_dot4c_i32_i8_e32 v96, v90, v78
	v_perm_b32 v3, v122, v118, s92
	v_perm_b32 v5, v130, v126, s92
	v_perm_b32 v90, v4, v2, s84
	v_perm_b32 v2, v4, v2, s93
	v_dot4c_i32_i8_e32 v151, v2, v79
	v_perm_b32 v2, v5, v3, s84
	v_dot4c_i32_i8_e32 v152, v2, v79
	v_perm_b32 v2, v5, v3, s93
	v_dot4c_i32_i8_e32 v7, v2, v79
	v_perm_b32 v2, v123, v119, s91
	v_perm_b32 v4, v131, v127, s91
	v_dot4c_i32_i8_e32 v150, v90, v79
	v_perm_b32 v3, v123, v119, s92
	v_perm_b32 v5, v131, v127, s92
	v_perm_b32 v90, v4, v2, s84
	v_perm_b32 v2, v4, v2, s93
	v_dot4c_i32_i8_e32 v9, v2, v79
	v_perm_b32 v2, v5, v3, s84
	v_dot4c_i32_i8_e32 v89, v2, v79
	v_perm_b32 v2, v5, v3, s93
	v_dot4c_i32_i8_e32 v153, v2, v79
	v_perm_b32 v2, v124, v120, s91
	v_perm_b32 v4, v132, v128, s91
	v_dot4c_i32_i8_e32 v8, v90, v79
	v_perm_b32 v3, v124, v120, s92
	v_perm_b32 v5, v132, v128, s92
	v_perm_b32 v90, v4, v2, s84
	v_perm_b32 v2, v4, v2, s93
	v_dot4c_i32_i8_e32 v155, v2, v79
	v_perm_b32 v2, v5, v3, s84
	v_dot4c_i32_i8_e32 v94, v2, v79
	v_perm_b32 v2, v5, v3, s93
	v_dot4c_i32_i8_e32 v95, v2, v79
	v_perm_b32 v2, v125, v121, s91
	v_perm_b32 v4, v133, v129, s91
	v_dot4c_i32_i8_e32 v154, v90, v79
	v_perm_b32 v3, v125, v121, s92
	v_perm_b32 v5, v133, v129, s92
	v_perm_b32 v90, v4, v2, s84
	v_perm_b32 v2, v4, v2, s93
	v_dot4c_i32_i8_e32 v97, v2, v79
	v_perm_b32 v2, v5, v3, s84
	v_dot4c_i32_i8_e32 v98, v2, v79
	v_perm_b32 v2, v5, v3, s93
	v_dot4c_i32_i8_e32 v99, v2, v79
	s_waitcnt vmcnt(2)
; __device__ __forceinline__ void peer_expert_phase(const Args& a, int layer, LAS unsigned char* lds, int G, int bid) {
;     ...
; #pragma unroll
;                 for (int G4 = 0; G4 < 4; ++G4)
; #pragma unroll
;                     for (int q = 0; q < 4; ++q) {
;                         const unsigned a_ = r[4 * G4][q], b_ = r[4 * G4 + 1][q], c_ = r[4 * G4 + 2][q], d_ = r[4 * G4 + 3][q];
;                         const unsigned ablo = __builtin_amdgcn_perm(b_, a_, 0x05010400u), abhi = __builtin_amdgcn_perm(b_, a_, 0x07030602u), cdlo = __builtin_amdgcn_perm(d_, c_, 0x05010400u), cdhi = __builtin_amdgcn_perm(d_, c_, 0x07030602u);
;                         iac[4 * q + 0] = __builtin_amdgcn_sdot4((int)__builtin_amdgcn_perm(cdlo, ablo, 0x05040100u), (int)W4[i][G4], iac[4 * q + 0], false);
;                         iac[4 * q + 1] = __builtin_amdgcn_sdot4((int)__builtin_amdgcn_perm(cdlo, ablo, 0x07060302u), (int)W4[i][G4], iac[4 * q + 1], false);
;                         iac[4 * q + 2] = __builtin_amdgcn_sdot4((int)__builtin_amdgcn_perm(cdhi, abhi, 0x05040100u), (int)W4[i][G4], iac[4 * q + 2], false);
;                         iac[4 * q + 3] = __builtin_amdgcn_sdot4((int)__builtin_amdgcn_perm(cdhi, abhi, 0x07060302u), (int)W4[i][G4], iac[4 * q + 3], false); }
;                 f32x2 ac[8];
; #pragma unroll
;                 for (int q = 0; q < 8; ++q) ac[q] = (f32x2){(float)iac[2 * q] * wsc[i], (float)iac[2 * q + 1] * wsc[i]};
;                 f32x2 b4_[4], b2_[2], b1_;
; #pragma unroll
;                 for (int q = 0; q < 4; ++q) { const f32x2 snd = (lane & 32) ? ac[q] : ac[q + 4], kp = (lane & 32) ? ac[q + 4] : ac[q]; b4_[q] = (f32x2){kp.x + __shfl_xor(snd.x, 32), kp.y + __shfl_xor(snd.y, 32)}; }
; #pragma unroll
;                 for (int q = 0; q < 2; ++q) { const f32x2 snd = (lane & 16) ? b4_[q] : b4_[q + 2], kp = (lane & 16) ? b4_[q + 2] : b4_[q]; b2_[q] = (f32x2){kp.x + __shfl_xor(snd.x, 16), kp.y + __shfl_xor(snd.y, 16)}; }
;                 { const f32x2 snd = (lane & 8) ? b2_[0] : b2_[1], kp = (lane & 8) ? b2_[1] : b2_[0]; b1_ = (f32x2){kp.x + __shfl_xor(snd.x, 8), kp.y + __shfl_xor(snd.y, 8)}; }
;                 const size_t off = (size_t)tok * DM + s * 128 + 16 * l7 + 2 * g8;
;                 const unsigned hb0 = *(const unsigned*)(H + off); f32x2 hn = {bflo(hb0) + b1_.x, bfhi(hb0) + b1_.y};
;                 if (ok) {
	v_perm_b32 v2, v138, v134, s91
	s_waitcnt vmcnt(0)
	v_perm_b32 v4, v146, v142, s91
	v_dot4c_i32_i8_e32 v96, v90, v79
	v_perm_b32 v3, v138, v134, s92
	v_perm_b32 v5, v146, v142, s92
	v_perm_b32 v90, v4, v2, s84
	v_perm_b32 v2, v4, v2, s93
	v_dot4c_i32_i8_e32 v151, v2, v80
	v_perm_b32 v2, v5, v3, s84
	v_dot4c_i32_i8_e32 v152, v2, v80
	v_perm_b32 v2, v5, v3, s93
	v_dot4c_i32_i8_e32 v7, v2, v80
	v_perm_b32 v2, v139, v135, s91
	v_perm_b32 v4, v147, v143, s91
	v_dot4c_i32_i8_e32 v150, v90, v80
	v_perm_b32 v3, v139, v135, s92
	v_perm_b32 v5, v147, v143, s92
	v_perm_b32 v90, v4, v2, s84
	v_perm_b32 v2, v4, v2, s93
	v_dot4c_i32_i8_e32 v9, v2, v80
	v_perm_b32 v2, v5, v3, s84
	v_dot4c_i32_i8_e32 v89, v2, v80
	v_perm_b32 v2, v5, v3, s93
	v_dot4c_i32_i8_e32 v153, v2, v80
	v_perm_b32 v2, v140, v136, s91
	v_perm_b32 v4, v148, v144, s91
	v_dot4c_i32_i8_e32 v8, v90, v80
	v_perm_b32 v3, v140, v136, s92
	v_perm_b32 v5, v148, v144, s92
	v_perm_b32 v90, v4, v2, s84
	v_perm_b32 v2, v4, v2, s93
	v_dot4c_i32_i8_e32 v155, v2, v80
	v_perm_b32 v2, v5, v3, s84
	v_dot4c_i32_i8_e32 v94, v2, v80
	v_perm_b32 v2, v5, v3, s93
	v_dot4c_i32_i8_e32 v95, v2, v80
	v_perm_b32 v2, v141, v137, s91
	v_perm_b32 v4, v149, v145, s91
	v_dot4c_i32_i8_e32 v154, v90, v80
	v_perm_b32 v3, v141, v137, s92
	v_perm_b32 v5, v149, v145, s92
	v_perm_b32 v90, v4, v2, s84
	v_perm_b32 v2, v4, v2, s93
	v_dot4c_i32_i8_e32 v97, v2, v80
	v_perm_b32 v2, v5, v3, s84
	v_dot4c_i32_i8_e32 v98, v2, v80
	v_perm_b32 v2, v5, v3, s93
	v_dot4c_i32_i8_e32 v99, v2, v80
	v_cvt_f32_i32_e32 v3, v151
	v_cvt_f32_i32_e32 v2, v150
	v_cvt_f32_i32_e32 v93, v155
	v_cvt_f32_i32_e32 v92, v154
	v_dot4c_i32_i8_e32 v96, v90, v80
	v_cvt_f32_i32_e32 v5, v7
	v_cvt_f32_i32_e32 v4, v152
	v_cvt_f32_i32_e32 v95, v95
	v_cvt_f32_i32_e32 v94, v94
	v_cvt_f32_i32_e32 v9, v9
	v_cvt_f32_i32_e32 v8, v8
	v_cvt_f32_i32_e32 v97, v97
	v_cvt_f32_i32_e32 v96, v96
	v_cvt_f32_i32_e32 v91, v153
	v_cvt_f32_i32_e32 v90, v89
	v_cvt_f32_i32_e32 v99, v99
	v_cvt_f32_i32_e32 v98, v98
	v_pk_mul_f32 v[2:3], v[26:27], v[2:3]
	v_pk_mul_f32 v[92:93], v[26:27], v[92:93]
	v_pk_mul_f32 v[4:5], v[26:27], v[4:5]
	v_pk_mul_f32 v[94:95], v[26:27], v[94:95]
	v_cndmask_b32_e64 v7, v3, v93, s[4:5]
	v_cndmask_b32_e64 v89, v2, v92, s[4:5]
	v_pk_mul_f32 v[8:9], v[26:27], v[8:9]
	v_pk_mul_f32 v[96:97], v[26:27], v[96:97]
	ds_bpermute_b32 v100, v36, v89
	ds_bpermute_b32 v101, v36, v7
	v_cndmask_b32_e64 v7, v5, v95, s[4:5]
	v_cndmask_b32_e64 v89, v4, v94, s[4:5]
	v_pk_mul_f32 v[90:91], v[26:27], v[90:91]
	v_pk_mul_f32 v[98:99], v[26:27], v[98:99]
	ds_bpermute_b32 v102, v36, v89
	ds_bpermute_b32 v103, v36, v7
	v_cndmask_b32_e64 v7, v9, v97, s[4:5]
	v_cndmask_b32_e64 v89, v8, v96, s[4:5]
	v_cndmask_b32_e64 v3, v93, v3, s[4:5]
	v_cndmask_b32_e64 v2, v92, v2, s[4:5]
	ds_bpermute_b32 v92, v36, v89
	ds_bpermute_b32 v93, v36, v7
	v_cndmask_b32_e64 v7, v91, v99, s[4:5]
	v_cndmask_b32_e64 v89, v90, v98, s[4:5]
	v_cndmask_b32_e64 v5, v95, v5, s[4:5]
	v_cndmask_b32_e64 v4, v94, v4, s[4:5]
	ds_bpermute_b32 v94, v36, v89
	ds_bpermute_b32 v95, v36, v7
	v_cndmask_b32_e64 v9, v97, v9, s[4:5]
	v_cndmask_b32_e64 v8, v96, v8, s[4:5]
	s_waitcnt lgkmcnt(0)
	v_pk_add_f32 v[2:3], v[2:3], v[100:101]
	v_pk_add_f32 v[8:9], v[8:9], v[92:93]
	v_cndmask_b32_e64 v91, v99, v91, s[4:5]
	v_cndmask_b32_e64 v90, v98, v90, s[4:5]
	v_pk_add_f32 v[4:5], v[4:5], v[102:103]
	v_pk_add_f32 v[90:91], v[90:91], v[94:95]
	v_cndmask_b32_e64 v7, v3, v9, s[6:7]
	v_cndmask_b32_e64 v89, v2, v8, s[6:7]
	v_cndmask_b32_e64 v3, v9, v3, s[6:7]
	ds_bpermute_b32 v93, v37, v7
	v_cndmask_b32_e64 v7, v5, v91, s[6:7]
	v_cndmask_b32_e64 v9, v4, v90, s[6:7]
	ds_bpermute_b32 v92, v37, v89
	ds_bpermute_b32 v94, v37, v9
	ds_bpermute_b32 v95, v37, v7
	v_cndmask_b32_e64 v2, v8, v2, s[6:7]
	v_cndmask_b32_e64 v5, v91, v5, s[6:7]
	v_cndmask_b32_e64 v4, v90, v4, s[6:7]
	s_waitcnt lgkmcnt(2)
	v_pk_add_f32 v[2:3], v[2:3], v[92:93]
	s_waitcnt lgkmcnt(0)
	v_pk_add_f32 v[4:5], v[4:5], v[94:95]
	s_nop 0
	v_cndmask_b32_e64 v8, v3, v5, s[8:9]
	v_cndmask_b32_e64 v7, v2, v4, s[8:9]
	ds_bpermute_b32 v7, v38, v7
	ds_bpermute_b32 v8, v38, v8
	s_cbranch_vccnz .LBB0_1243
	v_lshl_add_u64 v[90:91], v[34:35], 0, s[54:55]
	v_cndmask_b32_e64 v3, v5, v3, s[8:9]
	v_cndmask_b32_e64 v2, v4, v2, s[8:9]
	s_waitcnt lgkmcnt(0)
	v_add_f32_e32 v3, v3, v8
	v_add_f32_e32 v2, v2, v7
	s_waitcnt vmcnt(0)
	v_and_b32_e32 v4, 0xffff0000, v241
	v_lshlrev_b32_e32 v5, 16, v241
	v_add_f32_e32 v3, v3, v4
	v_add_f32_e32 v2, v2, v5
	v_cvt_pk_bf16_f32 v3, v2, v3
	global_store_dword v[90:91], v3, off
	v_lshlrev_b32_e32 v2, 16, v3
	v_and_b32_e32 v3, 0xffff0000, v3
	v_pk_mul_f32 v[4:5], v[2:3], v[2:3]
	v_pk_mul_f32 v[2:3], v[32:33], v[2:3]
	v_add_f32_e32 v4, v4, v5
	v_add_f32_e32 v67, v67, v4
	v_max3_f32 v70, v70, |v2|, |v3|
; __device__ __forceinline__ void peer_expert_phase(const Args& a, int layer, LAS unsigned char* lds, int G, int bid) {
;     ...
;                 for (int c = 0; c < 16; ++c) { const unsigned eo = (unsigned)__shfl((int)(c < 8 ? eoa[i] : eob[i]), (8 * c + g8) & 63); r[c] = *(const u32x4*)(pvs + (eo + lo16)); }
;                 int iac[16];
; #pragma unroll
;                 for (int q = 0; q < 16; ++q) iac[q] = 0;
; #pragma unroll
;                 for (int G4 = 0; G4 < 4; ++G4)
; #pragma unroll
;                     for (int q = 0; q < 4; ++q) {
;                         const unsigned a_ = r[4 * G4][q], b_ = r[4 * G4 + 1][q], c_ = r[4 * G4 + 2][q], d_ = r[4 * G4 + 3][q];
;                         const unsigned ablo = __builtin_amdgcn_perm(b_, a_, 0x05010400u), abhi = __builtin_amdgcn_perm(b_, a_, 0x07030602u), cdlo = __builtin_amdgcn_perm(d_, c_, 0x05010400u), cdhi = __builtin_amdgcn_perm(d_, c_, 0x07030602u);
;                         iac[4 * q + 0] = __builtin_amdgcn_sdot4((int)__builtin_amdgcn_perm(cdlo, ablo, 0x05040100u), (int)W4[i][G4], iac[4 * q + 0], false);
;                         iac[4 * q + 1] = __builtin_amdgcn_sdot4((int)__builtin_amdgcn_perm(cdlo, ablo, 0x07060302u), (int)W4[i][G4], iac[4 * q + 1], false);
;                         iac[4 * q + 2] = __builtin_amdgcn_sdot4((int)__builtin_amdgcn_perm(cdhi, abhi, 0x05040100u), (int)W4[i][G4], iac[4 * q + 2], false);
;                         iac[4 * q + 3] = __builtin_amdgcn_sdot4((int)__builtin_amdgcn_perm(cdhi, abhi, 0x07060302u), (int)W4[i][G4], iac[4 * q + 3], false); }
.LBB0_1243:
	s_waitcnt lgkmcnt(1)
	s_waitcnt lgkmcnt(0)
	global_load_dwordx4 v[2:5], v189, s[28:29]
	s_nop 0
	global_load_dwordx4 v[90:93], v190, s[28:29]
	global_load_dwordx4 v[94:97], v191, s[28:29]
	global_load_dwordx4 v[98:101], v192, s[28:29]
	global_load_dwordx4 v[102:105], v193, s[28:29]
	global_load_dwordx4 v[106:109], v194, s[28:29]
	global_load_dwordx4 v[110:113], v195, s[28:29]
	global_load_dwordx4 v[114:117], v196, s[28:29]
	global_load_dwordx4 v[118:121], v197, s[28:29]
	s_nop 0
	global_load_dwordx4 v[122:125], v198, s[28:29]
	s_nop 0
	global_load_dwordx4 v[126:129], v199, s[28:29]
	s_nop 0
	global_load_dwordx4 v[130:133], v200, s[28:29]
	s_nop 0
	global_load_dwordx4 v[134:137], v201, s[28:29]
	s_nop 0
	global_load_dwordx4 v[138:141], v202, s[28:29]
	s_nop 0
	global_load_dwordx4 v[142:145], v203, s[28:29]
	s_nop 0
	global_load_dwordx4 v[146:149], v204, s[28:29]
	v_mov_b32_e32 v7, 0
	v_mov_b32_e32 v8, 0
	v_mov_b32_e32 v154, 0
	v_mov_b32_e32 v151, 0
	v_mov_b32_e32 v153, 0
	v_mov_b32_e32 v89, 0
	v_mov_b32_e32 v152, 0
	v_mov_b32_e32 v150, 0
	v_mov_b32_e32 v9, 0
	v_mov_b32_e32 v155, 0
	s_andn2_b64 vcc, exec, s[56:57]
	s_waitcnt vmcnt(14)
	v_perm_b32 v156, v90, v2, s91
	v_perm_b32 v2, v90, v2, s92
	s_waitcnt vmcnt(12)
	v_perm_b32 v90, v98, v94, s91
	v_perm_b32 v94, v98, v94, s92
	v_perm_b32 v98, v91, v3, s91
	v_perm_b32 v3, v91, v3, s92
	v_perm_b32 v91, v99, v95, s91
	v_perm_b32 v95, v99, v95, s92
	v_perm_b32 v99, v92, v4, s91
	v_perm_b32 v4, v92, v4, s92
	v_perm_b32 v92, v100, v96, s91
	v_perm_b32 v96, v100, v96, s92
	v_perm_b32 v100, v90, v156, s84
	v_perm_b32 v90, v90, v156, s93
	v_perm_b32 v156, v94, v2, s84
	v_perm_b32 v2, v94, v2, s93
	v_perm_b32 v94, v91, v98, s84
	v_perm_b32 v91, v91, v98, s93
	v_perm_b32 v98, v95, v3, s84
	v_perm_b32 v3, v95, v3, s93
	v_perm_b32 v95, v92, v99, s84
	v_dot4c_i32_i8_e32 v7, v2, v81
	v_dot4c_i32_i8_e32 v8, v94, v81
	v_perm_b32 v2, v96, v4, s84
	v_mov_b32_e32 v94, 0
	v_dot4c_i32_i8_e32 v154, v95, v81
	v_dot4c_i32_i8_e32 v94, v2, v81
	v_perm_b32 v2, v96, v4, s93
	v_mov_b32_e32 v95, 0
	v_dot4c_i32_i8_e32 v95, v2, v81
	v_perm_b32 v2, v93, v5, s91
	v_perm_b32 v4, v101, v97, s91
	v_dot4c_i32_i8_e32 v151, v90, v81
	v_dot4c_i32_i8_e32 v153, v3, v81
	v_perm_b32 v3, v93, v5, s92
	v_perm_b32 v5, v101, v97, s92
	v_perm_b32 v90, v4, v2, s84
	v_perm_b32 v2, v4, v2, s93
	v_mov_b32_e32 v97, 0
	v_dot4c_i32_i8_e32 v89, v98, v81
	v_dot4c_i32_i8_e32 v97, v2, v81
	v_perm_b32 v2, v5, v3, s84
	v_mov_b32_e32 v98, 0
	v_perm_b32 v92, v92, v99, s93
	v_dot4c_i32_i8_e32 v98, v2, v81
	v_perm_b32 v2, v5, v3, s93
	v_mov_b32_e32 v99, 0
	v_mov_b32_e32 v96, 0
	v_dot4c_i32_i8_e32 v99, v2, v81
	s_waitcnt vmcnt(10)
	v_perm_b32 v2, v106, v102, s91
	s_waitcnt vmcnt(8)
	v_perm_b32 v4, v114, v110, s91
	v_dot4c_i32_i8_e32 v96, v90, v81
	v_perm_b32 v3, v106, v102, s92
	v_perm_b32 v5, v114, v110, s92
	v_perm_b32 v90, v4, v2, s84
	v_perm_b32 v2, v4, v2, s93
	v_dot4c_i32_i8_e32 v152, v156, v81
	v_dot4c_i32_i8_e32 v151, v2, v82
	v_perm_b32 v2, v5, v3, s84
	v_dot4c_i32_i8_e32 v152, v2, v82
	v_perm_b32 v2, v5, v3, s93
	v_dot4c_i32_i8_e32 v150, v100, v81
	v_dot4c_i32_i8_e32 v7, v2, v82
	v_perm_b32 v2, v107, v103, s91
	v_perm_b32 v4, v115, v111, s91
	v_dot4c_i32_i8_e32 v9, v91, v81
	v_dot4c_i32_i8_e32 v150, v90, v82
	v_perm_b32 v3, v107, v103, s92
	v_perm_b32 v5, v115, v111, s92
	v_perm_b32 v90, v4, v2, s84
	v_perm_b32 v2, v4, v2, s93
	v_dot4c_i32_i8_e32 v9, v2, v82
	v_perm_b32 v2, v5, v3, s84
	v_dot4c_i32_i8_e32 v89, v2, v82
	v_perm_b32 v2, v5, v3, s93
	v_dot4c_i32_i8_e32 v153, v2, v82
	v_perm_b32 v2, v108, v104, s91
	v_perm_b32 v4, v116, v112, s91
	v_dot4c_i32_i8_e32 v155, v92, v81
	v_dot4c_i32_i8_e32 v8, v90, v82
	v_perm_b32 v3, v108, v104, s92
	v_perm_b32 v5, v116, v112, s92
	v_perm_b32 v90, v4, v2, s84
	v_perm_b32 v2, v4, v2, s93
	v_dot4c_i32_i8_e32 v155, v2, v82
	v_perm_b32 v2, v5, v3, s84
	v_dot4c_i32_i8_e32 v94, v2, v82
	v_perm_b32 v2, v5, v3, s93
	v_dot4c_i32_i8_e32 v95, v2, v82
	v_perm_b32 v2, v109, v105, s91
	v_perm_b32 v4, v117, v113, s91
	v_dot4c_i32_i8_e32 v154, v90, v82
	v_perm_b32 v3, v109, v105, s92
	v_perm_b32 v5, v117, v113, s92
	v_perm_b32 v90, v4, v2, s84
	v_perm_b32 v2, v4, v2, s93
	v_dot4c_i32_i8_e32 v97, v2, v82
	v_perm_b32 v2, v5, v3, s84
	v_dot4c_i32_i8_e32 v98, v2, v82
	v_perm_b32 v2, v5, v3, s93
	v_dot4c_i32_i8_e32 v99, v2, v82
	s_waitcnt vmcnt(6)
	v_perm_b32 v2, v122, v118, s91
	s_waitcnt vmcnt(4)
	v_perm_b32 v4, v130, v126, s91
	v_dot4c_i32_i8_e32 v96, v90, v82
	v_perm_b32 v3, v122, v118, s92
	v_perm_b32 v5, v130, v126, s92
	v_perm_b32 v90, v4, v2, s84
	v_perm_b32 v2, v4, v2, s93
	v_dot4c_i32_i8_e32 v151, v2, v83
	v_perm_b32 v2, v5, v3, s84
	v_dot4c_i32_i8_e32 v152, v2, v83
	v_perm_b32 v2, v5, v3, s93
	v_dot4c_i32_i8_e32 v7, v2, v83
	v_perm_b32 v2, v123, v119, s91
	v_perm_b32 v4, v131, v127, s91
	v_dot4c_i32_i8_e32 v150, v90, v83
	v_perm_b32 v3, v123, v119, s92
	v_perm_b32 v5, v131, v127, s92
	v_perm_b32 v90, v4, v2, s84
	v_perm_b32 v2, v4, v2, s93
	v_dot4c_i32_i8_e32 v9, v2, v83
	v_perm_b32 v2, v5, v3, s84
	v_dot4c_i32_i8_e32 v89, v2, v83
	v_perm_b32 v2, v5, v3, s93
	v_dot4c_i32_i8_e32 v153, v2, v83
	v_perm_b32 v2, v124, v120, s91
	v_perm_b32 v4, v132, v128, s91
	v_dot4c_i32_i8_e32 v8, v90, v83
	v_perm_b32 v3, v124, v120, s92
	v_perm_b32 v5, v132, v128, s92
	v_perm_b32 v90, v4, v2, s84
	v_perm_b32 v2, v4, v2, s93
	v_dot4c_i32_i8_e32 v155, v2, v83
	v_perm_b32 v2, v5, v3, s84
	v_dot4c_i32_i8_e32 v94, v2, v83
	v_perm_b32 v2, v5, v3, s93
	v_dot4c_i32_i8_e32 v95, v2, v83
	v_perm_b32 v2, v125, v121, s91
	v_perm_b32 v4, v133, v129, s91
	v_dot4c_i32_i8_e32 v154, v90, v83
	v_perm_b32 v3, v125, v121, s92
	v_perm_b32 v5, v133, v129, s92
	v_perm_b32 v90, v4, v2, s84
	v_perm_b32 v2, v4, v2, s93
	v_dot4c_i32_i8_e32 v97, v2, v83
	v_perm_b32 v2, v5, v3, s84
	v_dot4c_i32_i8_e32 v98, v2, v83
	v_perm_b32 v2, v5, v3, s93
	v_dot4c_i32_i8_e32 v99, v2, v83
	s_waitcnt vmcnt(2)
; __device__ __forceinline__ unsigned pk2(float lo, float hi) { unsigned r; asm volatile("v_cvt_pk_bf16_f32 %0, %1, %2" : "=v"(r) : "v"(lo), "v"(hi)); return r; }
; __device__ __forceinline__ float bflo(unsigned u) { return __uint_as_float(u << 16); }
; __device__ __forceinline__ void peer_expert_phase(const Args& a, int layer, LAS unsigned char* lds, int G, int bid) {
;     ...
;                         iac[4 * q + 0] = __builtin_amdgcn_sdot4((int)__builtin_amdgcn_perm(cdlo, ablo, 0x05040100u), (int)W4[i][G4], iac[4 * q + 0], false);
;                         iac[4 * q + 1] = __builtin_amdgcn_sdot4((int)__builtin_amdgcn_perm(cdlo, ablo, 0x07060302u), (int)W4[i][G4], iac[4 * q + 1], false);
;                         iac[4 * q + 2] = __builtin_amdgcn_sdot4((int)__builtin_amdgcn_perm(cdhi, abhi, 0x05040100u), (int)W4[i][G4], iac[4 * q + 2], false);
;                         iac[4 * q + 3] = __builtin_amdgcn_sdot4((int)__builtin_amdgcn_perm(cdhi, abhi, 0x07060302u), (int)W4[i][G4], iac[4 * q + 3], false); }
;                 f32x2 ac[8];
; #pragma unroll
;                 for (int q = 0; q < 8; ++q) ac[q] = (f32x2){(float)iac[2 * q] * wsc[i], (float)iac[2 * q + 1] * wsc[i]};
;                 f32x2 b4_[4], b2_[2], b1_;
; #pragma unroll
;                 for (int q = 0; q < 4; ++q) { const f32x2 snd = (lane & 32) ? ac[q] : ac[q + 4], kp = (lane & 32) ? ac[q + 4] : ac[q]; b4_[q] = (f32x2){kp.x + __shfl_xor(snd.x, 32), kp.y + __shfl_xor(snd.y, 32)}; }
; #pragma unroll
;                 for (int q = 0; q < 2; ++q) { const f32x2 snd = (lane & 16) ? b4_[q] : b4_[q + 2], kp = (lane & 16) ? b4_[q + 2] : b4_[q]; b2_[q] = (f32x2){kp.x + __shfl_xor(snd.x, 16), kp.y + __shfl_xor(snd.y, 16)}; }
;                 { const f32x2 snd = (lane & 8) ? b2_[0] : b2_[1], kp = (lane & 8) ? b2_[1] : b2_[0]; b1_ = (f32x2){kp.x + __shfl_xor(snd.x, 8), kp.y + __shfl_xor(snd.y, 8)}; }
;                 const size_t off = (size_t)tok * DM + s * 128 + 16 * l7 + 2 * g8;
;                 const unsigned hb0 = *(const unsigned*)(H + off); f32x2 hn = {bflo(hb0) + b1_.x, bfhi(hb0) + b1_.y};
;                 if (ok) {
;                     { const unsigned hb1 = pk2(hn.x, hn.y); *(unsigned*)(H + off) = hb1; hn = (f32x2){bflo(hb1), bfhi(hb1)}; }
;                     ssq[i] += hn.x * hn.x + hn.y * hn.y; hgm[i] = fmaxf(hgm[i], fmaxf(fabsf(hn.x * gsl.x), fabsf(hn.y * gsl.y))); }
	v_perm_b32 v2, v138, v134, s91
	s_waitcnt vmcnt(0)
	v_perm_b32 v4, v146, v142, s91
	v_dot4c_i32_i8_e32 v96, v90, v83
	v_perm_b32 v3, v138, v134, s92
	v_perm_b32 v5, v146, v142, s92
	v_perm_b32 v90, v4, v2, s84
	v_perm_b32 v2, v4, v2, s93
	v_dot4c_i32_i8_e32 v151, v2, v84
	v_perm_b32 v2, v5, v3, s84
	v_dot4c_i32_i8_e32 v152, v2, v84
	v_perm_b32 v2, v5, v3, s93
	v_dot4c_i32_i8_e32 v7, v2, v84
	v_perm_b32 v2, v139, v135, s91
	v_perm_b32 v4, v147, v143, s91
	v_dot4c_i32_i8_e32 v150, v90, v84
	v_perm_b32 v3, v139, v135, s92
	v_perm_b32 v5, v147, v143, s92
	v_perm_b32 v90, v4, v2, s84
	v_perm_b32 v2, v4, v2, s93
	v_dot4c_i32_i8_e32 v9, v2, v84
	v_perm_b32 v2, v5, v3, s84
	v_dot4c_i32_i8_e32 v89, v2, v84
	v_perm_b32 v2, v5, v3, s93
	v_dot4c_i32_i8_e32 v153, v2, v84
	v_perm_b32 v2, v140, v136, s91
	v_perm_b32 v4, v148, v144, s91
	v_dot4c_i32_i8_e32 v8, v90, v84
	v_perm_b32 v3, v140, v136, s92
	v_perm_b32 v5, v148, v144, s92
	v_perm_b32 v90, v4, v2, s84
	v_perm_b32 v2, v4, v2, s93
	v_dot4c_i32_i8_e32 v155, v2, v84
	v_perm_b32 v2, v5, v3, s84
	v_dot4c_i32_i8_e32 v94, v2, v84
	v_perm_b32 v2, v5, v3, s93
	v_dot4c_i32_i8_e32 v95, v2, v84
	v_perm_b32 v2, v141, v137, s91
	v_perm_b32 v4, v149, v145, s91
	v_dot4c_i32_i8_e32 v154, v90, v84
	v_perm_b32 v3, v141, v137, s92
	v_perm_b32 v5, v149, v145, s92
	v_perm_b32 v90, v4, v2, s84
	v_perm_b32 v2, v4, v2, s93
	v_dot4c_i32_i8_e32 v97, v2, v84
	v_perm_b32 v2, v5, v3, s84
	v_dot4c_i32_i8_e32 v98, v2, v84
	v_perm_b32 v2, v5, v3, s93
	v_dot4c_i32_i8_e32 v99, v2, v84
	v_cvt_f32_i32_e32 v3, v151
	v_cvt_f32_i32_e32 v2, v150
	v_cvt_f32_i32_e32 v93, v155
	v_cvt_f32_i32_e32 v92, v154
	v_dot4c_i32_i8_e32 v96, v90, v84
	v_cvt_f32_i32_e32 v5, v7
	v_cvt_f32_i32_e32 v4, v152
	v_cvt_f32_i32_e32 v95, v95
	v_cvt_f32_i32_e32 v94, v94
	v_cvt_f32_i32_e32 v9, v9
	v_cvt_f32_i32_e32 v8, v8
	v_cvt_f32_i32_e32 v97, v97
	v_cvt_f32_i32_e32 v96, v96
	v_cvt_f32_i32_e32 v91, v153
	v_cvt_f32_i32_e32 v90, v89
	v_cvt_f32_i32_e32 v99, v99
	v_cvt_f32_i32_e32 v98, v98
	v_pk_mul_f32 v[2:3], v[28:29], v[2:3]
	v_pk_mul_f32 v[92:93], v[28:29], v[92:93]
	v_pk_mul_f32 v[4:5], v[28:29], v[4:5]
	v_pk_mul_f32 v[94:95], v[28:29], v[94:95]
	v_cndmask_b32_e64 v7, v3, v93, s[4:5]
	v_cndmask_b32_e64 v89, v2, v92, s[4:5]
	v_pk_mul_f32 v[8:9], v[28:29], v[8:9]
	v_pk_mul_f32 v[96:97], v[28:29], v[96:97]
	ds_bpermute_b32 v100, v36, v89
	ds_bpermute_b32 v101, v36, v7
	v_cndmask_b32_e64 v7, v5, v95, s[4:5]
	v_cndmask_b32_e64 v89, v4, v94, s[4:5]
	v_pk_mul_f32 v[90:91], v[28:29], v[90:91]
	v_pk_mul_f32 v[98:99], v[28:29], v[98:99]
	ds_bpermute_b32 v102, v36, v89
	ds_bpermute_b32 v103, v36, v7
	v_cndmask_b32_e64 v7, v9, v97, s[4:5]
	v_cndmask_b32_e64 v89, v8, v96, s[4:5]
	v_cndmask_b32_e64 v3, v93, v3, s[4:5]
	v_cndmask_b32_e64 v2, v92, v2, s[4:5]
	ds_bpermute_b32 v92, v36, v89
	ds_bpermute_b32 v93, v36, v7
	v_cndmask_b32_e64 v7, v91, v99, s[4:5]
	v_cndmask_b32_e64 v89, v90, v98, s[4:5]
	v_cndmask_b32_e64 v5, v95, v5, s[4:5]
	v_cndmask_b32_e64 v4, v94, v4, s[4:5]
	ds_bpermute_b32 v94, v36, v89
	ds_bpermute_b32 v95, v36, v7
	v_cndmask_b32_e64 v9, v97, v9, s[4:5]
	v_cndmask_b32_e64 v8, v96, v8, s[4:5]
	s_waitcnt lgkmcnt(0)
	v_pk_add_f32 v[2:3], v[2:3], v[100:101]
	v_pk_add_f32 v[8:9], v[8:9], v[92:93]
	v_cndmask_b32_e64 v91, v99, v91, s[4:5]
	v_cndmask_b32_e64 v90, v98, v90, s[4:5]
	v_pk_add_f32 v[4:5], v[4:5], v[102:103]
	v_pk_add_f32 v[90:91], v[90:91], v[94:95]
	v_cndmask_b32_e64 v7, v3, v9, s[6:7]
	v_cndmask_b32_e64 v89, v2, v8, s[6:7]
	v_cndmask_b32_e64 v3, v9, v3, s[6:7]
	ds_bpermute_b32 v93, v37, v7
	v_cndmask_b32_e64 v7, v5, v91, s[6:7]
	v_cndmask_b32_e64 v9, v4, v90, s[6:7]
	ds_bpermute_b32 v92, v37, v89
	ds_bpermute_b32 v94, v37, v9
	ds_bpermute_b32 v95, v37, v7
	v_cndmask_b32_e64 v2, v8, v2, s[6:7]
	v_cndmask_b32_e64 v5, v91, v5, s[6:7]
	v_cndmask_b32_e64 v4, v90, v4, s[6:7]
	s_waitcnt lgkmcnt(2)
	v_pk_add_f32 v[2:3], v[2:3], v[92:93]
	s_waitcnt lgkmcnt(0)
	v_pk_add_f32 v[4:5], v[4:5], v[94:95]
	s_nop 0
	v_cndmask_b32_e64 v8, v3, v5, s[8:9]
	v_cndmask_b32_e64 v7, v2, v4, s[8:9]
	ds_bpermute_b32 v7, v38, v7
	ds_bpermute_b32 v8, v38, v8
	s_cbranch_vccnz .LBB0_1245
	v_lshl_add_u64 v[90:91], v[34:35], 0, s[58:59]
	v_cndmask_b32_e64 v3, v5, v3, s[8:9]
	v_cndmask_b32_e64 v2, v4, v2, s[8:9]
	s_waitcnt lgkmcnt(0)
	v_add_f32_e32 v3, v3, v8
	v_add_f32_e32 v2, v2, v7
	s_waitcnt vmcnt(0)
	v_and_b32_e32 v4, 0xffff0000, v242
	v_lshlrev_b32_e32 v5, 16, v242
	v_add_f32_e32 v3, v3, v4
	v_add_f32_e32 v2, v2, v5
	v_cvt_pk_bf16_f32 v3, v2, v3
	global_store_dword v[90:91], v3, off
	v_lshlrev_b32_e32 v2, 16, v3
	v_and_b32_e32 v3, 0xffff0000, v3
	v_pk_mul_f32 v[4:5], v[2:3], v[2:3]
	v_pk_mul_f32 v[2:3], v[32:33], v[2:3]
	v_add_f32_e32 v4, v4, v5
	v_add_f32_e32 v66, v66, v4
	v_max3_f32 v71, v71, |v2|, |v3|
; __device__ __forceinline__ void peer_expert_phase(const Args& a, int layer, LAS unsigned char* lds, int G, int bid) {
;     ...
;                 for (int c = 0; c < 16; ++c) { const unsigned eo = (unsigned)__shfl((int)(c < 8 ? eoa[i] : eob[i]), (8 * c + g8) & 63); r[c] = *(const u32x4*)(pvs + (eo + lo16)); }
;                 int iac[16];
; #pragma unroll
;                 for (int q = 0; q < 16; ++q) iac[q] = 0;
; #pragma unroll
;                 for (int G4 = 0; G4 < 4; ++G4)
; #pragma unroll
;                     for (int q = 0; q < 4; ++q) {
;                         const unsigned a_ = r[4 * G4][q], b_ = r[4 * G4 + 1][q], c_ = r[4 * G4 + 2][q], d_ = r[4 * G4 + 3][q];
;                         const unsigned ablo = __builtin_amdgcn_perm(b_, a_, 0x05010400u), abhi = __builtin_amdgcn_perm(b_, a_, 0x07030602u), cdlo = __builtin_amdgcn_perm(d_, c_, 0x05010400u), cdhi = __builtin_amdgcn_perm(d_, c_, 0x07030602u);
;                         iac[4 * q + 0] = __builtin_amdgcn_sdot4((int)__builtin_amdgcn_perm(cdlo, ablo, 0x05040100u), (int)W4[i][G4], iac[4 * q + 0], false);
;                         iac[4 * q + 1] = __builtin_amdgcn_sdot4((int)__builtin_amdgcn_perm(cdlo, ablo, 0x07060302u), (int)W4[i][G4], iac[4 * q + 1], false);
;                         iac[4 * q + 2] = __builtin_amdgcn_sdot4((int)__builtin_amdgcn_perm(cdhi, abhi, 0x05040100u), (int)W4[i][G4], iac[4 * q + 2], false);
;                         iac[4 * q + 3] = __builtin_amdgcn_sdot4((int)__builtin_amdgcn_perm(cdhi, abhi, 0x07060302u), (int)W4[i][G4], iac[4 * q + 3], false); }
.LBB0_1245:
	s_waitcnt lgkmcnt(1)
	s_waitcnt lgkmcnt(0)
	global_load_dwordx4 v[2:5], v205, s[28:29]
	s_nop 0
	global_load_dwordx4 v[90:93], v206, s[28:29]
	global_load_dwordx4 v[94:97], v207, s[28:29]
	global_load_dwordx4 v[98:101], v208, s[28:29]
	global_load_dwordx4 v[102:105], v209, s[28:29]
	global_load_dwordx4 v[106:109], v210, s[28:29]
	global_load_dwordx4 v[110:113], v211, s[28:29]
	global_load_dwordx4 v[114:117], v212, s[28:29]
	global_load_dwordx4 v[118:121], v213, s[28:29]
	s_nop 0
	global_load_dwordx4 v[122:125], v214, s[28:29]
	s_nop 0
	global_load_dwordx4 v[126:129], v215, s[28:29]
	s_nop 0
	global_load_dwordx4 v[130:133], v216, s[28:29]
	s_nop 0
	global_load_dwordx4 v[134:137], v217, s[28:29]
	s_nop 0
	global_load_dwordx4 v[138:141], v218, s[28:29]
	s_nop 0
	global_load_dwordx4 v[142:145], v219, s[28:29]
	s_nop 0
	global_load_dwordx4 v[146:149], v220, s[28:29]
	v_mov_b32_e32 v7, 0
	v_mov_b32_e32 v8, 0
	v_mov_b32_e32 v154, 0
	v_mov_b32_e32 v151, 0
	v_mov_b32_e32 v153, 0
	v_mov_b32_e32 v89, 0
	v_mov_b32_e32 v152, 0
	v_mov_b32_e32 v150, 0
	v_mov_b32_e32 v9, 0
	v_mov_b32_e32 v155, 0
	s_andn2_b64 vcc, exec, s[60:61]
	s_waitcnt vmcnt(14)
	v_perm_b32 v156, v90, v2, s91
	v_perm_b32 v2, v90, v2, s92
	s_waitcnt vmcnt(12)
	v_perm_b32 v90, v98, v94, s91
	v_perm_b32 v94, v98, v94, s92
	v_perm_b32 v98, v91, v3, s91
	v_perm_b32 v3, v91, v3, s92
	v_perm_b32 v91, v99, v95, s91
	v_perm_b32 v95, v99, v95, s92
	v_perm_b32 v99, v92, v4, s91
	v_perm_b32 v4, v92, v4, s92
	v_perm_b32 v92, v100, v96, s91
	v_perm_b32 v96, v100, v96, s92
	v_perm_b32 v100, v90, v156, s84
	v_perm_b32 v90, v90, v156, s93
	v_perm_b32 v156, v94, v2, s84
	v_perm_b32 v2, v94, v2, s93
	v_perm_b32 v94, v91, v98, s84
	v_perm_b32 v91, v91, v98, s93
	v_perm_b32 v98, v95, v3, s84
	v_perm_b32 v3, v95, v3, s93
	v_perm_b32 v95, v92, v99, s84
	v_dot4c_i32_i8_e32 v7, v2, v85
	v_dot4c_i32_i8_e32 v8, v94, v85
	v_perm_b32 v2, v96, v4, s84
	v_mov_b32_e32 v94, 0
	v_dot4c_i32_i8_e32 v154, v95, v85
	v_dot4c_i32_i8_e32 v94, v2, v85
	v_perm_b32 v2, v96, v4, s93
	v_mov_b32_e32 v95, 0
	v_dot4c_i32_i8_e32 v95, v2, v85
	v_perm_b32 v2, v93, v5, s91
	v_perm_b32 v4, v101, v97, s91
	v_dot4c_i32_i8_e32 v151, v90, v85
	v_dot4c_i32_i8_e32 v153, v3, v85
	v_perm_b32 v3, v93, v5, s92
	v_perm_b32 v5, v101, v97, s92
	v_perm_b32 v90, v4, v2, s84
	v_perm_b32 v2, v4, v2, s93
	v_mov_b32_e32 v97, 0
	v_dot4c_i32_i8_e32 v89, v98, v85
	v_dot4c_i32_i8_e32 v97, v2, v85
	v_perm_b32 v2, v5, v3, s84
	v_mov_b32_e32 v98, 0
	v_perm_b32 v92, v92, v99, s93
	v_dot4c_i32_i8_e32 v98, v2, v85
	v_perm_b32 v2, v5, v3, s93
	v_mov_b32_e32 v99, 0
	v_mov_b32_e32 v96, 0
	v_dot4c_i32_i8_e32 v99, v2, v85
	s_waitcnt vmcnt(10)
	v_perm_b32 v2, v106, v102, s91
	s_waitcnt vmcnt(8)
	v_perm_b32 v4, v114, v110, s91
	v_dot4c_i32_i8_e32 v96, v90, v85
	v_perm_b32 v3, v106, v102, s92
	v_perm_b32 v5, v114, v110, s92
	v_perm_b32 v90, v4, v2, s84
	v_perm_b32 v2, v4, v2, s93
	v_dot4c_i32_i8_e32 v152, v156, v85
	v_dot4c_i32_i8_e32 v151, v2, v86
	v_perm_b32 v2, v5, v3, s84
	v_dot4c_i32_i8_e32 v152, v2, v86
	v_perm_b32 v2, v5, v3, s93
	v_dot4c_i32_i8_e32 v150, v100, v85
	v_dot4c_i32_i8_e32 v7, v2, v86
	v_perm_b32 v2, v107, v103, s91
	v_perm_b32 v4, v115, v111, s91
	v_dot4c_i32_i8_e32 v9, v91, v85
	v_dot4c_i32_i8_e32 v150, v90, v86
	v_perm_b32 v3, v107, v103, s92
	v_perm_b32 v5, v115, v111, s92
	v_perm_b32 v90, v4, v2, s84
	v_perm_b32 v2, v4, v2, s93
	v_dot4c_i32_i8_e32 v9, v2, v86
	v_perm_b32 v2, v5, v3, s84
	v_dot4c_i32_i8_e32 v89, v2, v86
	v_perm_b32 v2, v5, v3, s93
	v_dot4c_i32_i8_e32 v153, v2, v86
	v_perm_b32 v2, v108, v104, s91
	v_perm_b32 v4, v116, v112, s91
	v_dot4c_i32_i8_e32 v155, v92, v85
	v_dot4c_i32_i8_e32 v8, v90, v86
	v_perm_b32 v3, v108, v104, s92
	v_perm_b32 v5, v116, v112, s92
	v_perm_b32 v90, v4, v2, s84
	v_perm_b32 v2, v4, v2, s93
	v_dot4c_i32_i8_e32 v155, v2, v86
	v_perm_b32 v2, v5, v3, s84
	v_dot4c_i32_i8_e32 v94, v2, v86
	v_perm_b32 v2, v5, v3, s93
	v_dot4c_i32_i8_e32 v95, v2, v86
	v_perm_b32 v2, v109, v105, s91
	v_perm_b32 v4, v117, v113, s91
	v_dot4c_i32_i8_e32 v154, v90, v86
	v_perm_b32 v3, v109, v105, s92
	v_perm_b32 v5, v117, v113, s92
	v_perm_b32 v90, v4, v2, s84
	v_perm_b32 v2, v4, v2, s93
	v_dot4c_i32_i8_e32 v97, v2, v86
	v_perm_b32 v2, v5, v3, s84
	v_dot4c_i32_i8_e32 v98, v2, v86
	v_perm_b32 v2, v5, v3, s93
	v_dot4c_i32_i8_e32 v99, v2, v86
	s_waitcnt vmcnt(6)
	v_perm_b32 v2, v122, v118, s91
	s_waitcnt vmcnt(4)
	v_perm_b32 v4, v130, v126, s91
	v_dot4c_i32_i8_e32 v96, v90, v86
	v_perm_b32 v3, v122, v118, s92
	v_perm_b32 v5, v130, v126, s92
	v_perm_b32 v90, v4, v2, s84
	v_perm_b32 v2, v4, v2, s93
	v_dot4c_i32_i8_e32 v151, v2, v87
	v_perm_b32 v2, v5, v3, s84
	v_dot4c_i32_i8_e32 v152, v2, v87
	v_perm_b32 v2, v5, v3, s93
	v_dot4c_i32_i8_e32 v7, v2, v87
	v_perm_b32 v2, v123, v119, s91
	v_perm_b32 v4, v131, v127, s91
	v_dot4c_i32_i8_e32 v150, v90, v87
	v_perm_b32 v3, v123, v119, s92
	v_perm_b32 v5, v131, v127, s92
	v_perm_b32 v90, v4, v2, s84
	v_perm_b32 v2, v4, v2, s93
	v_dot4c_i32_i8_e32 v9, v2, v87
	v_perm_b32 v2, v5, v3, s84
	v_dot4c_i32_i8_e32 v89, v2, v87
	v_perm_b32 v2, v5, v3, s93
	v_dot4c_i32_i8_e32 v153, v2, v87
	v_perm_b32 v2, v124, v120, s91
	v_perm_b32 v4, v132, v128, s91
	v_dot4c_i32_i8_e32 v8, v90, v87
	v_perm_b32 v3, v124, v120, s92
	v_perm_b32 v5, v132, v128, s92
	v_perm_b32 v90, v4, v2, s84
	v_perm_b32 v2, v4, v2, s93
	v_dot4c_i32_i8_e32 v155, v2, v87
	v_perm_b32 v2, v5, v3, s84
	v_dot4c_i32_i8_e32 v94, v2, v87
	v_perm_b32 v2, v5, v3, s93
	v_dot4c_i32_i8_e32 v95, v2, v87
	v_perm_b32 v2, v125, v121, s91
	v_perm_b32 v4, v133, v129, s91
	v_dot4c_i32_i8_e32 v154, v90, v87
	v_perm_b32 v3, v125, v121, s92
	v_perm_b32 v5, v133, v129, s92
	v_perm_b32 v90, v4, v2, s84
	v_perm_b32 v2, v4, v2, s93
	v_dot4c_i32_i8_e32 v97, v2, v87
	v_perm_b32 v2, v5, v3, s84
	v_dot4c_i32_i8_e32 v98, v2, v87
	v_perm_b32 v2, v5, v3, s93
	v_dot4c_i32_i8_e32 v99, v2, v87
	s_waitcnt vmcnt(2)
; __device__ __forceinline__ unsigned pk2(float lo, float hi) { unsigned r; asm volatile("v_cvt_pk_bf16_f32 %0, %1, %2" : "=v"(r) : "v"(lo), "v"(hi)); return r; }
; __device__ __forceinline__ void peer_expert_phase(const Args& a, int layer, LAS unsigned char* lds, int G, int bid) {
;     ...
;                         iac[4 * q + 0] = __builtin_amdgcn_sdot4((int)__builtin_amdgcn_perm(cdlo, ablo, 0x05040100u), (int)W4[i][G4], iac[4 * q + 0], false);
;                         iac[4 * q + 1] = __builtin_amdgcn_sdot4((int)__builtin_amdgcn_perm(cdlo, ablo, 0x07060302u), (int)W4[i][G4], iac[4 * q + 1], false);
;                         iac[4 * q + 2] = __builtin_amdgcn_sdot4((int)__builtin_amdgcn_perm(cdhi, abhi, 0x05040100u), (int)W4[i][G4], iac[4 * q + 2], false);
;                         iac[4 * q + 3] = __builtin_amdgcn_sdot4((int)__builtin_amdgcn_perm(cdhi, abhi, 0x07060302u), (int)W4[i][G4], iac[4 * q + 3], false); }
;                 f32x2 ac[8];
; #pragma unroll
;                 for (int q = 0; q < 8; ++q) ac[q] = (f32x2){(float)iac[2 * q] * wsc[i], (float)iac[2 * q + 1] * wsc[i]};
;                 f32x2 b4_[4], b2_[2], b1_;
; #pragma unroll
;                 for (int q = 0; q < 4; ++q) { const f32x2 snd = (lane & 32) ? ac[q] : ac[q + 4], kp = (lane & 32) ? ac[q + 4] : ac[q]; b4_[q] = (f32x2){kp.x + __shfl_xor(snd.x, 32), kp.y + __shfl_xor(snd.y, 32)}; }
; #pragma unroll
;                 for (int q = 0; q < 2; ++q) { const f32x2 snd = (lane & 16) ? b4_[q] : b4_[q + 2], kp = (lane & 16) ? b4_[q + 2] : b4_[q]; b2_[q] = (f32x2){kp.x + __shfl_xor(snd.x, 16), kp.y + __shfl_xor(snd.y, 16)}; }
;                 { const f32x2 snd = (lane & 8) ? b2_[0] : b2_[1], kp = (lane & 8) ? b2_[1] : b2_[0]; b1_ = (f32x2){kp.x + __shfl_xor(snd.x, 8), kp.y + __shfl_xor(snd.y, 8)}; }
;                 const size_t off = (size_t)tok * DM + s * 128 + 16 * l7 + 2 * g8;
;                 const unsigned hb0 = *(const unsigned*)(H + off); f32x2 hn = {bflo(hb0) + b1_.x, bfhi(hb0) + b1_.y};
;                 if (ok) {
;                     { const unsigned hb1 = pk2(hn.x, hn.y); *(unsigned*)(H + off) = hb1; hn = (f32x2){bflo(hb1), bfhi(hb1)}; }
;                     ssq[i] += hn.x * hn.x + hn.y * hn.y; hgm[i] = fmaxf(hgm[i], fmaxf(fabsf(hn.x * gsl.x), fabsf(hn.y * gsl.y))); }
;                 __builtin_amdgcn_sched_barrier(0);
;             }
;         }
	v_perm_b32 v2, v138, v134, s91
	s_waitcnt vmcnt(0)
	v_perm_b32 v4, v146, v142, s91
	v_dot4c_i32_i8_e32 v96, v90, v87
	v_perm_b32 v3, v138, v134, s92
	v_perm_b32 v5, v146, v142, s92
	v_perm_b32 v90, v4, v2, s84
	v_perm_b32 v2, v4, v2, s93
	v_dot4c_i32_i8_e32 v151, v2, v88
	v_perm_b32 v2, v5, v3, s84
	v_dot4c_i32_i8_e32 v152, v2, v88
	v_perm_b32 v2, v5, v3, s93
	v_dot4c_i32_i8_e32 v7, v2, v88
	v_perm_b32 v2, v139, v135, s91
	v_perm_b32 v4, v147, v143, s91
	v_dot4c_i32_i8_e32 v150, v90, v88
	v_perm_b32 v3, v139, v135, s92
	v_perm_b32 v5, v147, v143, s92
	v_perm_b32 v90, v4, v2, s84
	v_perm_b32 v2, v4, v2, s93
	v_dot4c_i32_i8_e32 v9, v2, v88
	v_perm_b32 v2, v5, v3, s84
	v_dot4c_i32_i8_e32 v89, v2, v88
	v_perm_b32 v2, v5, v3, s93
	v_dot4c_i32_i8_e32 v153, v2, v88
	v_perm_b32 v2, v140, v136, s91
	v_perm_b32 v4, v148, v144, s91
	v_dot4c_i32_i8_e32 v8, v90, v88
	v_perm_b32 v3, v140, v136, s92
	v_perm_b32 v5, v148, v144, s92
	v_perm_b32 v90, v4, v2, s84
	v_perm_b32 v2, v4, v2, s93
	v_dot4c_i32_i8_e32 v155, v2, v88
	v_perm_b32 v2, v5, v3, s84
	v_dot4c_i32_i8_e32 v94, v2, v88
	v_perm_b32 v2, v5, v3, s93
	v_dot4c_i32_i8_e32 v95, v2, v88
	v_perm_b32 v2, v141, v137, s91
	v_perm_b32 v4, v149, v145, s91
	v_dot4c_i32_i8_e32 v154, v90, v88
	v_perm_b32 v3, v141, v137, s92
	v_perm_b32 v5, v149, v145, s92
	v_perm_b32 v90, v4, v2, s84
	v_perm_b32 v2, v4, v2, s93
	v_dot4c_i32_i8_e32 v97, v2, v88
	v_perm_b32 v2, v5, v3, s84
	v_dot4c_i32_i8_e32 v98, v2, v88
	v_perm_b32 v2, v5, v3, s93
	v_dot4c_i32_i8_e32 v99, v2, v88
	v_cvt_f32_i32_e32 v3, v151
	v_cvt_f32_i32_e32 v2, v150
	v_cvt_f32_i32_e32 v93, v155
	v_cvt_f32_i32_e32 v92, v154
	v_dot4c_i32_i8_e32 v96, v90, v88
	v_cvt_f32_i32_e32 v5, v7
	v_cvt_f32_i32_e32 v4, v152
	v_cvt_f32_i32_e32 v95, v95
	v_cvt_f32_i32_e32 v94, v94
	v_cvt_f32_i32_e32 v9, v9
	v_cvt_f32_i32_e32 v8, v8
	v_cvt_f32_i32_e32 v97, v97
	v_cvt_f32_i32_e32 v96, v96
	v_cvt_f32_i32_e32 v91, v153
	v_cvt_f32_i32_e32 v90, v89
	v_cvt_f32_i32_e32 v99, v99
	v_cvt_f32_i32_e32 v98, v98
	v_pk_mul_f32 v[2:3], v[30:31], v[2:3]
	v_pk_mul_f32 v[92:93], v[30:31], v[92:93]
	v_pk_mul_f32 v[4:5], v[30:31], v[4:5]
	v_pk_mul_f32 v[94:95], v[30:31], v[94:95]
	v_cndmask_b32_e64 v7, v3, v93, s[4:5]
	v_cndmask_b32_e64 v89, v2, v92, s[4:5]
	v_pk_mul_f32 v[8:9], v[30:31], v[8:9]
	v_pk_mul_f32 v[96:97], v[30:31], v[96:97]
	ds_bpermute_b32 v100, v36, v89
	ds_bpermute_b32 v101, v36, v7
	v_cndmask_b32_e64 v7, v5, v95, s[4:5]
	v_cndmask_b32_e64 v89, v4, v94, s[4:5]
	v_pk_mul_f32 v[90:91], v[30:31], v[90:91]
	v_pk_mul_f32 v[98:99], v[30:31], v[98:99]
	ds_bpermute_b32 v102, v36, v89
	ds_bpermute_b32 v103, v36, v7
	v_cndmask_b32_e64 v7, v9, v97, s[4:5]
	v_cndmask_b32_e64 v89, v8, v96, s[4:5]
	v_cndmask_b32_e64 v3, v93, v3, s[4:5]
	v_cndmask_b32_e64 v2, v92, v2, s[4:5]
	ds_bpermute_b32 v92, v36, v89
	ds_bpermute_b32 v93, v36, v7
	v_cndmask_b32_e64 v7, v91, v99, s[4:5]
	v_cndmask_b32_e64 v89, v90, v98, s[4:5]
	v_cndmask_b32_e64 v5, v95, v5, s[4:5]
	v_cndmask_b32_e64 v4, v94, v4, s[4:5]
	ds_bpermute_b32 v94, v36, v89
	ds_bpermute_b32 v95, v36, v7
	v_cndmask_b32_e64 v9, v97, v9, s[4:5]
	v_cndmask_b32_e64 v8, v96, v8, s[4:5]
	s_waitcnt lgkmcnt(0)
	v_pk_add_f32 v[2:3], v[2:3], v[100:101]
	v_pk_add_f32 v[8:9], v[8:9], v[92:93]
	v_cndmask_b32_e64 v91, v99, v91, s[4:5]
	v_cndmask_b32_e64 v90, v98, v90, s[4:5]
	v_pk_add_f32 v[4:5], v[4:5], v[102:103]
	v_pk_add_f32 v[90:91], v[90:91], v[94:95]
	v_cndmask_b32_e64 v7, v3, v9, s[6:7]
	v_cndmask_b32_e64 v89, v2, v8, s[6:7]
	v_cndmask_b32_e64 v3, v9, v3, s[6:7]
	ds_bpermute_b32 v93, v37, v7
	v_cndmask_b32_e64 v7, v5, v91, s[6:7]
	v_cndmask_b32_e64 v9, v4, v90, s[6:7]
	ds_bpermute_b32 v92, v37, v89
	ds_bpermute_b32 v94, v37, v9
	ds_bpermute_b32 v95, v37, v7
	v_cndmask_b32_e64 v2, v8, v2, s[6:7]
	v_cndmask_b32_e64 v5, v91, v5, s[6:7]
	v_cndmask_b32_e64 v4, v90, v4, s[6:7]
	s_waitcnt lgkmcnt(2)
	v_pk_add_f32 v[2:3], v[2:3], v[92:93]
	s_waitcnt lgkmcnt(0)
	v_pk_add_f32 v[4:5], v[4:5], v[94:95]
	s_nop 0
	v_cndmask_b32_e64 v8, v3, v5, s[8:9]
	v_cndmask_b32_e64 v7, v2, v4, s[8:9]
	ds_bpermute_b32 v7, v38, v7
	ds_bpermute_b32 v8, v38, v8
	s_cbranch_vccnz .LBB0_1240
	v_lshl_add_u64 v[34:35], v[34:35], 0, s[62:63]
	v_cndmask_b32_e64 v3, v5, v3, s[8:9]
	v_cndmask_b32_e64 v2, v4, v2, s[8:9]
	s_waitcnt lgkmcnt(0)
	v_add_f32_e32 v3, v3, v8
	v_add_f32_e32 v2, v2, v7
	s_waitcnt vmcnt(0)
	v_and_b32_e32 v4, 0xffff0000, v243
	v_lshlrev_b32_e32 v5, 16, v243
	v_add_f32_e32 v3, v3, v4
	v_add_f32_e32 v2, v2, v5
	v_cvt_pk_bf16_f32 v3, v2, v3
	global_store_dword v[34:35], v3, off
	v_lshlrev_b32_e32 v2, 16, v3
	v_and_b32_e32 v3, 0xffff0000, v3
	v_pk_mul_f32 v[4:5], v[2:3], v[2:3]
	v_pk_mul_f32 v[2:3], v[32:33], v[2:3]
	v_add_f32_e32 v4, v4, v5
	v_add_f32_e32 v65, v65, v4
	v_max3_f32 v72, v72, |v2|, |v3|
	s_branch .LBB0_1240

; __device__ __forceinline__ float gelu_tanh(float x) { const float u = 0.7978845608028654f * (x + 0.044715f * x * x * x); return 0.5f * x * (1.0f + tanhf(u)); }
; __device__ __forceinline__ void peer_expert_phase(const Args& a, int layer, LAS unsigned char* lds, int G, int bid) {
;     ...
;         for (int i = 0; i < 4; ++i) { int tok = tb + i * NGW; tok = tok < NTOK ? tok : tb;
;             const float rstd_t = 1.0f / sqrtf(wave_sum(((const float*)(ws + WS_SSP))[((size_t)layer * NTOK + tok) * 64 + lane]) * (1.0f / DM) + EPS);
;             const float ga = GATE[(size_t)tok * 128 + lane], gb = GATE[(size_t)tok * 128 + 64 + lane];
;             const float rx = rstd_t * xs[i];
;             wa[i] = ga * gelu_tanh(pa[i] * SCU[ea[i]] * rx) * SCV[ea[i]]; wb[i] = gb * gelu_tanh(pb[i] * SCU[eb[i]] * rx) * SCV[eb[i]]; ssq[i] = 0.f; }
;         unsigned W4[4][4]; float wsc[4];
; #pragma unroll
;         for (int i = 0; i < 4; ++i) { const float wm = wave_max(fmaxf(fabsf(wa[i]), fabsf(wb[i]))); const float qw = wm > 0.f ? 127.0f / wm : 0.f; wsc[i] = wm * (1.0f / 127.0f);
;             const unsigned qa = __float_as_uint(wa[i] * qw + 12582912.0f), qb = __float_as_uint(wb[i] * qw + 12582912.0f);
; #pragma unroll
;             for (int G4 = 0; G4 < 4; ++G4) { unsigned t[4];
; #pragma unroll
;                 for (int k = 0; k < 4; ++k) { const int c = 4 * G4 + k; t[k] = (unsigned)__shfl((int)(c < 8 ? qa : qb), (8 * c + g8) & 63); }
;                 W4[i][G4] = __builtin_amdgcn_perm(__builtin_amdgcn_perm(t[3], t[2], 0x0c0c0400u), __builtin_amdgcn_perm(t[1], t[0], 0x0c0c0400u), 0x05040100u); } }
.LBB0_2298:
	s_andn2_saveexec_b64 s[22:23], s[22:23]
	v_mul_f32_e32 v61, v5, v5
	v_fmamk_f32 v62, v61, 0xbbbac73d, v49
	v_fmaak_f32 v62, v61, v62, 0xbd5c1c4e
	v_fmaak_f32 v62, v61, v62, 0x3e088382
	v_fmaak_f32 v62, v61, v62, 0xbeaaaa99
	v_mul_f32_e64 v62, |v5|, v62
	v_fma_f32 v61, v61, v62, |v5|
	s_or_b64 exec, exec, s[22:23]
	v_lshl_add_u64 v[24:25], v[24:25], 2, s[38:39]
	global_load_dword v24, v[24:25], off
	v_bfi_b32 v27, s77, v106, v27
	v_bfi_b32 v63, s77, v64, v63
	v_mul_f32_e32 v19, 0.5, v19
	v_mul_f32_e32 v26, 0.5, v26
	v_add_f32_e32 v27, 1.0, v27
	v_add_f32_e32 v63, 1.0, v63
	v_mul_f32_e32 v19, v19, v27
	v_mul_f32_e32 v26, v26, v63
	v_mul_f32_e32 v19, v60, v19
	v_mul_f32_e32 v26, v59, v26
	v_mul_f32_e32 v19, v111, v19
	v_mul_f32_e32 v18, v18, v26
	v_max_f32_e64 v26, |v18|, |v19|
	ds_bpermute_b32 v27, v29, v26
	v_bfi_b32 v7, s77, v88, v7
	v_mul_f32_e32 v3, 0.5, v3
	v_add_f32_e32 v7, 1.0, v7
	v_mul_f32_e32 v3, v3, v7
	s_waitcnt lgkmcnt(0)
	v_max_f32_e32 v27, v27, v27
	v_max_f32_e32 v26, v26, v27
	ds_bpermute_b32 v27, v30, v26
	v_bfi_b32 v62, s77, v71, v70
	v_mul_f32_e32 v23, 0.5, v23
	v_bfi_b32 v5, s77, v61, v5
	v_add_f32_e32 v59, 1.0, v62
	s_waitcnt lgkmcnt(0)
	v_max_f32_e32 v27, v27, v27
	v_max_f32_e32 v26, v26, v27
	ds_bpermute_b32 v27, v31, v26
	v_mul_f32_e32 v1, 0.5, v1
	v_add_f32_e32 v5, 1.0, v5
	v_mul_f32_e32 v23, v23, v59
	v_mul_f32_e32 v1, v1, v5
	s_waitcnt lgkmcnt(0)
	v_max_f32_e32 v7, v27, v27
	v_max_f32_e32 v7, v26, v7
	ds_bpermute_b32 v26, v32, v7
	v_mul_f32_e32 v5, v91, v23
	v_mul_f32_e32 v1, v21, v1
	v_bfi_b32 v25, s77, v66, v65
	v_mul_f32_e32 v0, 0.5, v0
	s_waitcnt lgkmcnt(0)
	v_max_f32_e32 v23, v26, v26
	v_max_f32_e32 v7, v7, v23
	ds_bpermute_b32 v23, v33, v7
	v_add_f32_e32 v25, 1.0, v25
	v_mul_f32_e32 v0, v0, v25
	v_mul_f32_e32 v0, v72, v0
	s_waitcnt vmcnt(1)
	v_mul_f32_e32 v0, v4, v0
	s_waitcnt lgkmcnt(0)
	v_max_f32_e32 v21, v23, v23
	v_max_f32_e32 v7, v7, v21
	ds_bpermute_b32 v21, v34, v7
	v_mul_f32_e32 v4, v20, v5
	v_bfi_b32 v66, s77, v79, v78
	v_mul_f32_e32 v65, 0.5, v77
	v_bfi_b32 v67, s77, v96, v95
	s_waitcnt lgkmcnt(0)
	v_max_f32_e32 v20, v21, v21
	v_max_f32_e32 v7, v7, v20
	v_div_scale_f32 v20, s[22:23], v7, v7, s69
	v_rcp_f32_e32 v21, v20
	v_add_f32_e32 v60, 1.0, v66
	v_mul_f32_e32 v2, 0.5, v2
	v_add_f32_e32 v61, 1.0, v67
	v_mul_f32_e32 v25, v65, v60
	v_mul_f32_e32 v2, v2, v61
	v_mul_f32_e32 v25, v90, v25
	v_mul_f32_e32 v2, v107, v2
	v_mul_f32_e32 v5, v22, v25
	v_fma_f32 v22, -v20, v21, 1.0
	v_mul_f32_e32 v2, v6, v2
	v_div_scale_f32 v6, vcc, s69, v7, s69
	v_fmac_f32_e32 v21, v22, v21
	v_mul_f32_e32 v22, v6, v21
	v_fma_f32 v23, -v20, v22, v6
	v_fmac_f32_e32 v22, v23, v21
	v_fma_f32 v6, -v20, v22, v6
	v_div_fmas_f32 v6, v6, v21, v22
	v_mul_f32_e32 v3, v108, v3
	v_div_fixup_f32 v6, v6, v7, s69
	v_cmp_lt_f32_e32 vcc, 0, v7
	v_mul_f32_e32 v3, v89, v3
	v_max_f32_e64 v25, |v2|, |v3|
	v_cndmask_b32_e32 v6, 0, v6, vcc
	v_fmaak_f32 v20, v18, v6, 0x4b400000
	ds_bpermute_b32 v21, v38, v20
	ds_bpermute_b32 v22, v39, v20
	ds_bpermute_b32 v26, v29, v25
	s_waitcnt vmcnt(0)
	v_mul_f32_e32 v1, v24, v1
	ds_bpermute_b32 v23, v40, v20
	ds_bpermute_b32 v24, v41, v20
	s_waitcnt lgkmcnt(3)
	v_perm_b32 v21, v22, v21, s70
	s_waitcnt lgkmcnt(2)
	v_max_f32_e32 v22, v26, v26
	v_max_f32_e32 v22, v25, v22
	v_mul_f32_e32 v18, 0x3c010204, v7
	s_waitcnt lgkmcnt(0)
	v_perm_b32 v7, v24, v23, s70
	ds_bpermute_b32 v23, v30, v22
	v_fmaak_f32 v6, v19, v6, 0x4b400000
	v_perm_b32 v63, v7, v21, s71
	ds_bpermute_b32 v24, v42, v20
	ds_bpermute_b32 v25, v43, v20
	s_waitcnt lgkmcnt(2)
	v_max_f32_e32 v23, v23, v23
	v_max_f32_e32 v22, v22, v23
	ds_bpermute_b32 v23, v31, v22
	ds_bpermute_b32 v26, v44, v20
	ds_bpermute_b32 v20, v45, v20
	v_mov_b32_e32 v59, 0
	s_mov_b32 s27, 0
	s_waitcnt lgkmcnt(2)
	v_max_f32_e32 v19, v23, v23
	v_max_f32_e32 v19, v22, v19
	ds_bpermute_b32 v21, v32, v19
	s_waitcnt lgkmcnt(1)
	v_perm_b32 v7, v20, v26, s70
	v_perm_b32 v20, v25, v24, s70
	ds_bpermute_b32 v22, v38, v6
	ds_bpermute_b32 v23, v39, v6
	s_waitcnt lgkmcnt(2)
	v_max_f32_e32 v21, v21, v21
	ds_bpermute_b32 v24, v40, v6
	ds_bpermute_b32 v25, v41, v6
	v_max_f32_e32 v19, v19, v21
	ds_bpermute_b32 v21, v33, v19
	v_perm_b32 v64, v7, v20, s71
	s_waitcnt lgkmcnt(3)
	v_perm_b32 v20, v23, v22, s70
	s_waitcnt lgkmcnt(1)
	v_perm_b32 v7, v25, v24, s70
	v_perm_b32 v65, v7, v20, s71
	s_waitcnt lgkmcnt(0)
	v_max_f32_e32 v7, v21, v21
	v_max_f32_e32 v7, v19, v7
	ds_bpermute_b32 v19, v34, v7
	ds_bpermute_b32 v20, v42, v6
	ds_bpermute_b32 v21, v43, v6
	ds_bpermute_b32 v22, v44, v6
	ds_bpermute_b32 v6, v45, v6
	s_waitcnt lgkmcnt(4)
	v_max_f32_e32 v19, v19, v19
	v_max_f32_e32 v7, v7, v19
	v_div_scale_f32 v19, s[22:23], v7, v7, s69
	v_rcp_f32_e32 v23, v19
	s_waitcnt lgkmcnt(0)
	v_perm_b32 v6, v6, v22, s70
	v_perm_b32 v20, v21, v20, s70
	v_perm_b32 v66, v6, v20, s71
	v_fma_f32 v6, -v19, v23, 1.0
	v_fmac_f32_e32 v23, v6, v23
	v_div_scale_f32 v6, vcc, s69, v7, s69
	v_mul_f32_e32 v20, v6, v23
	v_fma_f32 v21, -v19, v20, v6
	v_fmac_f32_e32 v20, v21, v23
	v_fma_f32 v6, -v19, v20, v6
	v_div_fmas_f32 v6, v6, v23, v20
	v_div_fixup_f32 v6, v6, v7, s69
	v_cmp_lt_f32_e32 vcc, 0, v7
	v_max_f32_e64 v22, |v5|, |v4|
	ds_bpermute_b32 v23, v29, v22
	v_cndmask_b32_e32 v6, 0, v6, vcc
	v_fmaak_f32 v2, v2, v6, 0x4b400000
	ds_bpermute_b32 v19, v40, v2
	ds_bpermute_b32 v21, v41, v2
	v_mul_f32_e32 v20, 0x3c010204, v7
	ds_bpermute_b32 v7, v38, v2
	ds_bpermute_b32 v24, v39, v2
	v_fmaak_f32 v3, v3, v6, 0x4b400000
	s_waitcnt lgkmcnt(2)
	v_perm_b32 v19, v21, v19, s70
	v_max_f32_e32 v21, v23, v23
	v_max_f32_e32 v21, v22, v21
	ds_bpermute_b32 v22, v30, v21
	s_waitcnt lgkmcnt(1)
; __device__ __forceinline__ void peer_expert_phase(const Args& a, int layer, LAS unsigned char* lds, int G, int bid) {
;     ...
;         for (int i = 0; i < 4; ++i) { const float wm = wave_max(fmaxf(fabsf(wa[i]), fabsf(wb[i]))); const float qw = wm > 0.f ? 127.0f / wm : 0.f; wsc[i] = wm * (1.0f / 127.0f);
;             const unsigned qa = __float_as_uint(wa[i] * qw + 12582912.0f), qb = __float_as_uint(wb[i] * qw + 12582912.0f);
; #pragma unroll
;             for (int G4 = 0; G4 < 4; ++G4) { unsigned t[4];
; #pragma unroll
;                 for (int k = 0; k < 4; ++k) { const int c = 4 * G4 + k; t[k] = (unsigned)__shfl((int)(c < 8 ? qa : qb), (8 * c + g8) & 63); }
;                 W4[i][G4] = __builtin_amdgcn_perm(__builtin_amdgcn_perm(t[3], t[2], 0x0c0c0400u), __builtin_amdgcn_perm(t[1], t[0], 0x0c0c0400u), 0x05040100u); } }
;         float* HO = a.out;
; #pragma unroll 1
;         for (int sidx = 0; sidx < 32; ++sidx) { const int s = (sidx + srot) & 31; const unsigned char* pvs = PV + s * 128; const f32x2 gsl = *(const f32x2*)(gnext + s * 128 + 16 * l7 + 2 * g8);
; #pragma unroll
;             for (int i = 0; i < 4; ++i) {
;                 int tok = tb + i * NGW; const bool ok = tok < NTOK; tok = ok ? tok : tb;
;                 u32x4 r[16];
; #pragma unroll
;                 for (int c = 0; c < 16; ++c) { const unsigned eo = (unsigned)__shfl((int)(c < 8 ? eoa[i] : eob[i]), (8 * c + g8) & 63); r[c] = *(const u32x4*)(pvs + (eo + lo16)); }
	v_perm_b32 v7, v24, v7, s70
	v_perm_b32 v67, v19, v7, s71
	ds_bpermute_b32 v7, v44, v2
	ds_bpermute_b32 v19, v45, v2
	s_waitcnt lgkmcnt(2)
	v_max_f32_e32 v22, v22, v22
	v_max_f32_e32 v21, v21, v22
	ds_bpermute_b32 v22, v31, v21
	ds_bpermute_b32 v23, v42, v2
	s_waitcnt lgkmcnt(2)
	v_perm_b32 v7, v19, v7, s70
	ds_bpermute_b32 v2, v43, v2
	ds_bpermute_b32 v24, v40, v3
	s_waitcnt lgkmcnt(3)
	v_max_f32_e32 v6, v22, v22
	v_max_f32_e32 v6, v21, v6
	ds_bpermute_b32 v19, v32, v6
	ds_bpermute_b32 v25, v41, v3
	ds_bpermute_b32 v21, v38, v3
	ds_bpermute_b32 v22, v39, v3
	s_waitcnt lgkmcnt(5)
	v_perm_b32 v2, v2, v23, s70
	s_waitcnt lgkmcnt(3)
	v_max_f32_e32 v19, v19, v19
	v_max_f32_e32 v6, v6, v19
	ds_bpermute_b32 v19, v33, v6
	v_perm_b32 v68, v7, v2, s71
	s_waitcnt lgkmcnt(3)
	v_perm_b32 v2, v25, v24, s70
	s_waitcnt lgkmcnt(1)
	v_perm_b32 v7, v22, v21, s70
	ds_bpermute_b32 v21, v42, v3
	s_waitcnt lgkmcnt(1)
	v_max_f32_e32 v19, v19, v19
	v_max_f32_e32 v6, v6, v19
	ds_bpermute_b32 v19, v34, v6
	ds_bpermute_b32 v22, v43, v3
	ds_bpermute_b32 v23, v44, v3
	ds_bpermute_b32 v3, v45, v3
	v_perm_b32 v69, v2, v7, s71
	s_waitcnt lgkmcnt(3)
	v_max_f32_e32 v19, v19, v19
	v_max_f32_e32 v6, v6, v19
	v_div_scale_f32 v19, s[22:23], v6, v6, s69
	v_rcp_f32_e32 v24, v19
	s_waitcnt lgkmcnt(0)
	v_perm_b32 v2, v3, v23, s70
	v_perm_b32 v3, v22, v21, s70
	v_max_f32_e64 v25, |v0|, |v1|
	v_fma_f32 v7, -v19, v24, 1.0
	v_fmac_f32_e32 v24, v7, v24
	v_div_scale_f32 v7, vcc, s69, v6, s69
	v_mul_f32_e32 v21, v7, v24
	v_fma_f32 v22, -v19, v21, v7
	v_fmac_f32_e32 v21, v22, v24
	v_fma_f32 v7, -v19, v21, v7
	v_div_fmas_f32 v7, v7, v24, v21
	v_div_fixup_f32 v7, v7, v6, s69
	v_cmp_lt_f32_e32 vcc, 0, v6
	ds_bpermute_b32 v26, v29, v25
	v_mul_f32_e32 v22, 0x3c010204, v6
	v_cndmask_b32_e32 v7, 0, v7, vcc
	v_fmaak_f32 v5, v5, v7, 0x4b400000
	ds_bpermute_b32 v19, v38, v5
	ds_bpermute_b32 v21, v39, v5
	s_waitcnt lgkmcnt(2)
	v_max_f32_e32 v6, v26, v26
	v_max_f32_e32 v6, v25, v6
	v_perm_b32 v70, v2, v3, s71
	ds_bpermute_b32 v23, v40, v5
	s_waitcnt lgkmcnt(1)
	v_perm_b32 v3, v21, v19, s70
	ds_bpermute_b32 v19, v30, v6
	ds_bpermute_b32 v24, v41, v5
	ds_bpermute_b32 v21, v42, v5
	v_fmaak_f32 v4, v4, v7, 0x4b400000
	ds_bpermute_b32 v7, v38, v4
	s_waitcnt lgkmcnt(3)
	v_max_f32_e32 v19, v19, v19
	v_max_f32_e32 v6, v6, v19
	s_waitcnt lgkmcnt(2)
	v_perm_b32 v2, v24, v23, s70
	ds_bpermute_b32 v23, v43, v5
	ds_bpermute_b32 v24, v44, v5
	ds_bpermute_b32 v5, v45, v5
	ds_bpermute_b32 v19, v31, v6
	v_perm_b32 v71, v2, v3, s71
	s_waitcnt lgkmcnt(3)
	v_perm_b32 v3, v23, v21, s70
	ds_bpermute_b32 v21, v40, v4
	s_waitcnt lgkmcnt(2)
	v_perm_b32 v2, v5, v24, s70
	s_waitcnt lgkmcnt(1)
	v_max_f32_e32 v5, v19, v19
	v_max_f32_e32 v5, v6, v5
	ds_bpermute_b32 v6, v32, v5
	ds_bpermute_b32 v19, v39, v4
	ds_bpermute_b32 v23, v41, v4
	v_perm_b32 v72, v2, v3, s71
	v_mov_b32_e32 v60, 0
	s_waitcnt lgkmcnt(2)
	v_max_f32_e32 v6, v6, v6
	v_max_f32_e32 v5, v5, v6
	ds_bpermute_b32 v6, v33, v5
	s_waitcnt lgkmcnt(1)
	v_perm_b32 v2, v23, v21, s70
	v_perm_b32 v3, v19, v7, s70
	v_perm_b32 v73, v2, v3, s71
	ds_bpermute_b32 v7, v44, v4
	s_waitcnt lgkmcnt(1)
	v_max_f32_e32 v2, v6, v6
	v_max_f32_e32 v2, v5, v2
	ds_bpermute_b32 v3, v34, v2
	ds_bpermute_b32 v5, v42, v4
	ds_bpermute_b32 v6, v43, v4
	ds_bpermute_b32 v4, v45, v4
	v_mov_b32_e32 v23, v22
	s_waitcnt lgkmcnt(3)
	v_max_f32_e32 v3, v3, v3
	v_max_f32_e32 v2, v2, v3
	v_div_scale_f32 v3, s[22:23], v2, v2, s69
	v_rcp_f32_e32 v19, v3
	s_waitcnt lgkmcnt(0)
	v_perm_b32 v4, v4, v7, s70
	v_perm_b32 v5, v6, v5, s70
	v_perm_b32 v74, v4, v5, s71
	v_fma_f32 v4, -v3, v19, 1.0
	v_fmac_f32_e32 v19, v4, v19
	v_div_scale_f32 v4, vcc, s69, v2, s69
	v_mul_f32_e32 v5, v4, v19
	v_fma_f32 v6, -v3, v5, v4
	v_fmac_f32_e32 v5, v6, v19
	v_fma_f32 v3, -v3, v5, v4
	v_div_fmas_f32 v3, v3, v19, v5
	v_div_fixup_f32 v3, v3, v2, s69
	v_cmp_lt_f32_e32 vcc, 0, v2
	v_mul_f32_e32 v24, 0x3c010204, v2
	v_mov_b32_e32 v25, v24
	v_cndmask_b32_e32 v3, 0, v3, vcc
	v_fmaak_f32 v0, v0, v3, 0x4b400000
	ds_bpermute_b32 v2, v38, v0
	ds_bpermute_b32 v4, v39, v0
	ds_bpermute_b32 v5, v40, v0
	ds_bpermute_b32 v6, v41, v0
	ds_bpermute_b32 v7, v42, v0
	ds_bpermute_b32 v19, v44, v0
	ds_bpermute_b32 v21, v45, v0
	ds_bpermute_b32 v0, v43, v0
	s_waitcnt lgkmcnt(4)
	v_perm_b32 v5, v6, v5, s70
	v_perm_b32 v2, v4, v2, s70
	v_perm_b32 v75, v5, v2, s71
	s_waitcnt lgkmcnt(1)
	v_perm_b32 v2, v21, v19, s70
	s_waitcnt lgkmcnt(0)
	v_perm_b32 v0, v0, v7, s70
	v_perm_b32 v76, v2, v0, s71
	v_fmaak_f32 v0, v1, v3, 0x4b400000
	ds_bpermute_b32 v1, v38, v0
	ds_bpermute_b32 v2, v39, v0
	ds_bpermute_b32 v3, v40, v0
	ds_bpermute_b32 v4, v41, v0
	ds_bpermute_b32 v5, v42, v0
	ds_bpermute_b32 v6, v44, v0
	ds_bpermute_b32 v7, v45, v0
	ds_bpermute_b32 v0, v43, v0
	s_waitcnt lgkmcnt(4)
	v_perm_b32 v3, v4, v3, s70
	v_perm_b32 v1, v2, v1, s70
	v_perm_b32 v77, v3, v1, s71
	s_waitcnt lgkmcnt(1)
	v_perm_b32 v1, v7, v6, s70
	s_waitcnt lgkmcnt(0)
	v_perm_b32 v0, v0, v5, s70
	v_perm_b32 v78, v1, v0, s71
	v_mov_b32_e32 v19, v18
	v_mov_b32_e32 v21, v20
	v_mov_b32_e32 v61, 0
	v_mov_b32_e32 v62, 0
	ds_bpermute_b32 v147, v38, v51
	ds_bpermute_b32 v148, v39, v51
	ds_bpermute_b32 v149, v40, v51
	ds_bpermute_b32 v150, v41, v51
	ds_bpermute_b32 v151, v42, v51
	ds_bpermute_b32 v152, v43, v51
	ds_bpermute_b32 v153, v44, v51
	ds_bpermute_b32 v154, v45, v51
	s_waitcnt lgkmcnt(7)
; __device__ __forceinline__ void peer_expert_phase(const Args& a, int layer, LAS unsigned char* lds, int G, int bid) {
;     ...
; #pragma unroll
;         for (int i = 0; i < 4; ++i) { eoa[i] = (unsigned)ea[i] << 12; eob[i] = (unsigned)eb[i] << 12; }
;         const unsigned lo16 = 16u * (unsigned)l7;
;     ...
;                 for (int c = 0; c < 16; ++c) { const unsigned eo = (unsigned)__shfl((int)(c < 8 ? eoa[i] : eob[i]), (8 * c + g8) & 63); r[c] = *(const u32x4*)(pvs + (eo + lo16)); }
	v_add_u32_e32 v147, v147, v35
	s_waitcnt lgkmcnt(6)
	v_add_u32_e32 v148, v148, v35
	s_waitcnt lgkmcnt(5)
	v_add_u32_e32 v149, v149, v35
	s_waitcnt lgkmcnt(4)
	v_add_u32_e32 v150, v150, v35
	s_waitcnt lgkmcnt(3)
	v_add_u32_e32 v151, v151, v35
	s_waitcnt lgkmcnt(2)
	v_add_u32_e32 v152, v152, v35
	s_waitcnt lgkmcnt(1)
	v_add_u32_e32 v153, v153, v35
	s_waitcnt lgkmcnt(0)
	v_add_u32_e32 v154, v154, v35
	ds_bpermute_b32 v155, v38, v52
	ds_bpermute_b32 v156, v39, v52
	ds_bpermute_b32 v157, v40, v52
	ds_bpermute_b32 v158, v41, v52
	ds_bpermute_b32 v159, v42, v52
	ds_bpermute_b32 v160, v43, v52
	ds_bpermute_b32 v161, v44, v52
	ds_bpermute_b32 v162, v45, v52
	s_waitcnt lgkmcnt(7)
	v_add_u32_e32 v155, v155, v35
	s_waitcnt lgkmcnt(6)
	v_add_u32_e32 v156, v156, v35
	s_waitcnt lgkmcnt(5)
	v_add_u32_e32 v157, v157, v35
	s_waitcnt lgkmcnt(4)
	v_add_u32_e32 v158, v158, v35
	s_waitcnt lgkmcnt(3)
	v_add_u32_e32 v159, v159, v35
	s_waitcnt lgkmcnt(2)
	v_add_u32_e32 v160, v160, v35
	s_waitcnt lgkmcnt(1)
	v_add_u32_e32 v161, v161, v35
	s_waitcnt lgkmcnt(0)
	v_add_u32_e32 v162, v162, v35
	ds_bpermute_b32 v163, v38, v53
	ds_bpermute_b32 v164, v39, v53
	ds_bpermute_b32 v165, v40, v53
	ds_bpermute_b32 v166, v41, v53
	ds_bpermute_b32 v167, v42, v53
	ds_bpermute_b32 v168, v43, v53
	ds_bpermute_b32 v169, v44, v53
	ds_bpermute_b32 v170, v45, v53
	s_waitcnt lgkmcnt(7)
	v_add_u32_e32 v163, v163, v35
	s_waitcnt lgkmcnt(6)
	v_add_u32_e32 v164, v164, v35
	s_waitcnt lgkmcnt(5)
	v_add_u32_e32 v165, v165, v35
	s_waitcnt lgkmcnt(4)
	v_add_u32_e32 v166, v166, v35
	s_waitcnt lgkmcnt(3)
	v_add_u32_e32 v167, v167, v35
	s_waitcnt lgkmcnt(2)
	v_add_u32_e32 v168, v168, v35
	s_waitcnt lgkmcnt(1)
	v_add_u32_e32 v169, v169, v35
	s_waitcnt lgkmcnt(0)
	v_add_u32_e32 v170, v170, v35
	ds_bpermute_b32 v171, v38, v54
	ds_bpermute_b32 v172, v39, v54
	ds_bpermute_b32 v173, v40, v54
	ds_bpermute_b32 v174, v41, v54
	ds_bpermute_b32 v175, v42, v54
	ds_bpermute_b32 v176, v43, v54
	ds_bpermute_b32 v177, v44, v54
	ds_bpermute_b32 v178, v45, v54
	s_waitcnt lgkmcnt(7)
	v_add_u32_e32 v171, v171, v35
	s_waitcnt lgkmcnt(6)
	v_add_u32_e32 v172, v172, v35
	s_waitcnt lgkmcnt(5)
	v_add_u32_e32 v173, v173, v35
	s_waitcnt lgkmcnt(4)
	v_add_u32_e32 v174, v174, v35
	s_waitcnt lgkmcnt(3)
	v_add_u32_e32 v175, v175, v35
	s_waitcnt lgkmcnt(2)
	v_add_u32_e32 v176, v176, v35
	s_waitcnt lgkmcnt(1)
	v_add_u32_e32 v177, v177, v35
	s_waitcnt lgkmcnt(0)
	v_add_u32_e32 v178, v178, v35
	ds_bpermute_b32 v179, v38, v55
	ds_bpermute_b32 v180, v39, v55
	ds_bpermute_b32 v181, v40, v55
	ds_bpermute_b32 v182, v41, v55
	ds_bpermute_b32 v183, v42, v55
	ds_bpermute_b32 v184, v43, v55
	ds_bpermute_b32 v185, v44, v55
	ds_bpermute_b32 v186, v45, v55
	s_waitcnt lgkmcnt(7)
	v_add_u32_e32 v179, v179, v35
	s_waitcnt lgkmcnt(6)
	v_add_u32_e32 v180, v180, v35
	s_waitcnt lgkmcnt(5)
	v_add_u32_e32 v181, v181, v35
	s_waitcnt lgkmcnt(4)
	v_add_u32_e32 v182, v182, v35
	s_waitcnt lgkmcnt(3)
	v_add_u32_e32 v183, v183, v35
	s_waitcnt lgkmcnt(2)
	v_add_u32_e32 v184, v184, v35
	s_waitcnt lgkmcnt(1)
	v_add_u32_e32 v185, v185, v35
	s_waitcnt lgkmcnt(0)
	v_add_u32_e32 v186, v186, v35
	ds_bpermute_b32 v187, v38, v56
	ds_bpermute_b32 v188, v39, v56
	ds_bpermute_b32 v189, v40, v56
	ds_bpermute_b32 v190, v41, v56
	ds_bpermute_b32 v191, v42, v56
	ds_bpermute_b32 v192, v43, v56
	ds_bpermute_b32 v193, v44, v56
	ds_bpermute_b32 v194, v45, v56
	s_waitcnt lgkmcnt(7)
	v_add_u32_e32 v187, v187, v35
	s_waitcnt lgkmcnt(6)
	v_add_u32_e32 v188, v188, v35
	s_waitcnt lgkmcnt(5)
	v_add_u32_e32 v189, v189, v35
	s_waitcnt lgkmcnt(4)
	v_add_u32_e32 v190, v190, v35
	s_waitcnt lgkmcnt(3)
	v_add_u32_e32 v191, v191, v35
	s_waitcnt lgkmcnt(2)
	v_add_u32_e32 v192, v192, v35
	s_waitcnt lgkmcnt(1)
	v_add_u32_e32 v193, v193, v35
	s_waitcnt lgkmcnt(0)
	v_add_u32_e32 v194, v194, v35
	ds_bpermute_b32 v195, v38, v57
	ds_bpermute_b32 v196, v39, v57
	ds_bpermute_b32 v197, v40, v57
	ds_bpermute_b32 v198, v41, v57
	ds_bpermute_b32 v199, v42, v57
	ds_bpermute_b32 v200, v43, v57
	ds_bpermute_b32 v201, v44, v57
	ds_bpermute_b32 v202, v45, v57
	s_waitcnt lgkmcnt(7)
	v_add_u32_e32 v195, v195, v35
	s_waitcnt lgkmcnt(6)
	v_add_u32_e32 v196, v196, v35
	s_waitcnt lgkmcnt(5)
	v_add_u32_e32 v197, v197, v35
	s_waitcnt lgkmcnt(4)
	v_add_u32_e32 v198, v198, v35
	s_waitcnt lgkmcnt(3)
	v_add_u32_e32 v199, v199, v35
	s_waitcnt lgkmcnt(2)
	v_add_u32_e32 v200, v200, v35
	s_waitcnt lgkmcnt(1)
	v_add_u32_e32 v201, v201, v35
	s_waitcnt lgkmcnt(0)
	v_add_u32_e32 v202, v202, v35
	ds_bpermute_b32 v203, v38, v58
	ds_bpermute_b32 v204, v39, v58
	ds_bpermute_b32 v205, v40, v58
	ds_bpermute_b32 v206, v41, v58
	ds_bpermute_b32 v207, v42, v58
	ds_bpermute_b32 v208, v43, v58
	ds_bpermute_b32 v209, v44, v58
	ds_bpermute_b32 v210, v45, v58
	s_waitcnt lgkmcnt(7)
	v_add_u32_e32 v203, v203, v35
	s_waitcnt lgkmcnt(6)
	v_add_u32_e32 v204, v204, v35
	s_waitcnt lgkmcnt(5)
	v_add_u32_e32 v205, v205, v35
	s_waitcnt lgkmcnt(4)
	v_add_u32_e32 v206, v206, v35
	s_waitcnt lgkmcnt(3)
	v_add_u32_e32 v207, v207, v35
	s_waitcnt lgkmcnt(2)
	v_add_u32_e32 v208, v208, v35
	s_waitcnt lgkmcnt(1)
	v_add_u32_e32 v209, v209, v35
	s_waitcnt lgkmcnt(0)
	v_add_u32_e32 v210, v210, v35
	s_branch .LBB0_2302

; __device__ __forceinline__ void peer_expert_phase(const Args& a, int layer, LAS unsigned char* lds, int G, int bid) {
;     ...
; #pragma unroll 1
;         for (int sidx = 0; sidx < 32; ++sidx) { const int s = (sidx + srot) & 31; const unsigned char* pvs = PV + s * 128; const f32x2 gsl = *(const f32x2*)(gnext + s * 128 + 16 * l7 + 2 * g8);
; #pragma unroll
;             for (int i = 0; i < 4; ++i) {
;                 int tok = tb + i * NGW; const bool ok = tok < NTOK; tok = ok ? tok : tb;
;                 u32x4 r[16];
; #pragma unroll
;                 for (int c = 0; c < 16; ++c) { const unsigned eo = (unsigned)__shfl((int)(c < 8 ? eoa[i] : eob[i]), (8 * c + g8) & 63); r[c] = *(const u32x4*)(pvs + (eo + lo16)); }
;                 int iac[16];
; #pragma unroll
;                 for (int q = 0; q < 16; ++q) iac[q] = 0;
; #pragma unroll
;                 for (int G4 = 0; G4 < 4; ++G4)
; #pragma unroll
;                     for (int q = 0; q < 4; ++q) {
;                         const unsigned a_ = r[4 * G4][q], b_ = r[4 * G4 + 1][q], c_ = r[4 * G4 + 2][q], d_ = r[4 * G4 + 3][q];
;                         const unsigned ablo = __builtin_amdgcn_perm(b_, a_, 0x05010400u), abhi = __builtin_amdgcn_perm(b_, a_, 0x07030602u), cdlo = __builtin_amdgcn_perm(d_, c_, 0x05010400u), cdhi = __builtin_amdgcn_perm(d_, c_, 0x07030602u);
;                         iac[4 * q + 0] = __builtin_amdgcn_sdot4((int)__builtin_amdgcn_perm(cdlo, ablo, 0x05040100u), (int)W4[i][G4], iac[4 * q + 0], false);
;                         iac[4 * q + 1] = __builtin_amdgcn_sdot4((int)__builtin_amdgcn_perm(cdlo, ablo, 0x07060302u), (int)W4[i][G4], iac[4 * q + 1], false);
;                         iac[4 * q + 2] = __builtin_amdgcn_sdot4((int)__builtin_amdgcn_perm(cdhi, abhi, 0x05040100u), (int)W4[i][G4], iac[4 * q + 2], false);
;                         iac[4 * q + 3] = __builtin_amdgcn_sdot4((int)__builtin_amdgcn_perm(cdhi, abhi, 0x07060302u), (int)W4[i][G4], iac[4 * q + 3], false); }
.LBB0_2302:
	s_bitcmp0_b32 s27, 7
	s_cbranch_scc0 .Lvbar0_skip
	s_barrier
.Lvbar0_skip:
	s_add_i32 s22, s67, s27
	s_and_b32 s40, s22, 0xf80
	s_lshl_b32 s98, s40, 1
	s_mov_b32 s99, 0
	v_lshl_add_u64 v[230:231], v[16:17], 0, s[98:99]
	v_lshl_add_u64 v[232:233], v[230:231], 0, s[24:25]
	global_load_dword v240, v[232:233], off
	v_lshl_add_u64 v[234:235], v[230:231], 0, s[44:45]
	global_load_dword v241, v[234:235], off
	v_lshl_add_u64 v[236:237], v[230:231], 0, s[48:49]
	global_load_dword v242, v[236:237], off
	v_lshl_add_u64 v[238:239], v[230:231], 0, s[52:53]
	global_load_dword v243, v[238:239], off
	s_add_u32 s22, s64, s40
	s_addc_u32 s23, s65, 0
	s_waitcnt lgkmcnt(0)
	global_load_dwordx4 v[80:83], v147, s[22:23]
	global_load_dwordx4 v[84:87], v148, s[22:23]
	global_load_dwordx4 v[88:91], v149, s[22:23]
	global_load_dwordx4 v[92:95], v150, s[22:23]
	global_load_dwordx4 v[96:99], v151, s[22:23]
	global_load_dwordx4 v[100:103], v152, s[22:23]
	global_load_dwordx4 v[104:107], v153, s[22:23]
	global_load_dwordx4 v[108:111], v154, s[22:23]
	global_load_dwordx4 v[112:115], v155, s[22:23]
	global_load_dwordx4 v[116:119], v156, s[22:23]
	global_load_dwordx4 v[120:123], v157, s[22:23]
	global_load_dwordx4 v[124:127], v158, s[22:23]
	global_load_dwordx4 v[128:131], v159, s[22:23]
	global_load_dwordx4 v[132:135], v160, s[22:23]
	s_nop 0
	global_load_dwordx4 v[0:3], v161, s[22:23]
	s_nop 0
	global_load_dwordx4 v[4:7], v162, s[22:23]
	v_mov_b32_e32 v138, 0
	v_mov_b32_e32 v139, 0
	v_mov_b32_e32 v137, 0
	v_mov_b32_e32 v141, 0
	v_mov_b32_e32 v140, 0
	v_mov_b32_e32 v143, 0
	v_mov_b32_e32 v136, 0
	v_mov_b32_e32 v142, 0
	s_lshl_b32 s40, s40, 1
	v_lshl_add_u64 v[26:27], v[16:17], 0, s[40:41]
	s_waitcnt vmcnt(14)
	v_perm_b32 v79, v84, v80, s78
	v_perm_b32 v80, v84, v80, s79
	s_waitcnt vmcnt(12)
	v_perm_b32 v84, v92, v88, s78
	v_perm_b32 v88, v92, v88, s79
	v_perm_b32 v92, v85, v81, s78
	v_perm_b32 v81, v85, v81, s79
	v_perm_b32 v85, v93, v89, s78
	v_perm_b32 v89, v93, v89, s79
	v_perm_b32 v93, v86, v82, s78
	v_perm_b32 v82, v86, v82, s79
	v_perm_b32 v86, v94, v90, s78
	v_perm_b32 v144, v84, v79, s71
	v_perm_b32 v79, v84, v79, s80
	v_perm_b32 v84, v88, v80, s71
	v_perm_b32 v80, v88, v80, s80
	v_perm_b32 v88, v85, v92, s71
	v_perm_b32 v85, v85, v92, s80
	v_dot4c_i32_i8_e32 v138, v84, v63
	v_dot4c_i32_i8_e32 v139, v80, v63
	v_perm_b32 v80, v86, v93, s71
	v_mov_b32_e32 v84, 0
	v_dot4c_i32_i8_e32 v137, v79, v63
	v_dot4c_i32_i8_e32 v141, v85, v63
	v_perm_b32 v79, v94, v90, s79
	v_dot4c_i32_i8_e32 v84, v80, v63
	v_perm_b32 v80, v86, v93, s80
	v_mov_b32_e32 v85, 0
	v_perm_b32 v92, v89, v81, s71
	v_perm_b32 v81, v89, v81, s80
	v_dot4c_i32_i8_e32 v140, v88, v63
	v_dot4c_i32_i8_e32 v85, v80, v63
	v_perm_b32 v80, v79, v82, s71
	v_perm_b32 v79, v79, v82, s80
	v_mov_b32_e32 v88, 0
	v_dot4c_i32_i8_e32 v143, v81, v63
	v_mov_b32_e32 v86, 0
	v_dot4c_i32_i8_e32 v88, v79, v63
	v_perm_b32 v79, v87, v83, s78
	v_perm_b32 v81, v95, v91, s78
	v_dot4c_i32_i8_e32 v86, v80, v63
	v_perm_b32 v80, v87, v83, s79
	v_perm_b32 v82, v95, v91, s79
	v_perm_b32 v83, v81, v79, s71
	v_perm_b32 v79, v81, v79, s80
	v_mov_b32_e32 v87, 0
	v_dot4c_i32_i8_e32 v87, v79, v63
	v_perm_b32 v79, v82, v80, s71
	v_mov_b32_e32 v90, 0
	v_dot4c_i32_i8_e32 v90, v79, v63
	v_perm_b32 v79, v82, v80, s80
	v_mov_b32_e32 v91, 0
	v_mov_b32_e32 v89, 0
	v_dot4c_i32_i8_e32 v91, v79, v63
	s_waitcnt vmcnt(10)
	v_perm_b32 v79, v100, v96, s78
	s_waitcnt vmcnt(8)
	v_perm_b32 v81, v108, v104, s78
	v_dot4c_i32_i8_e32 v89, v83, v63
	v_perm_b32 v80, v100, v96, s79
	v_perm_b32 v82, v108, v104, s79
	v_perm_b32 v83, v81, v79, s71
	v_perm_b32 v79, v81, v79, s80
	v_dot4c_i32_i8_e32 v137, v79, v64
	v_perm_b32 v79, v82, v80, s71
	v_dot4c_i32_i8_e32 v138, v79, v64
	v_perm_b32 v79, v82, v80, s80
	v_dot4c_i32_i8_e32 v136, v144, v63
	v_dot4c_i32_i8_e32 v139, v79, v64
	v_perm_b32 v79, v101, v97, s78
	v_perm_b32 v81, v109, v105, s78
	v_dot4c_i32_i8_e32 v136, v83, v64
	v_perm_b32 v80, v101, v97, s79
	v_perm_b32 v82, v109, v105, s79
	v_perm_b32 v83, v81, v79, s71
	v_perm_b32 v79, v81, v79, s80
	v_dot4c_i32_i8_e32 v142, v92, v63
	v_dot4c_i32_i8_e32 v141, v79, v64
	v_perm_b32 v79, v82, v80, s71
	v_dot4c_i32_i8_e32 v142, v79, v64
	v_perm_b32 v79, v82, v80, s80
	v_dot4c_i32_i8_e32 v143, v79, v64
	v_perm_b32 v79, v102, v98, s78
	v_perm_b32 v81, v110, v106, s78
	v_dot4c_i32_i8_e32 v140, v83, v64
	v_perm_b32 v80, v102, v98, s79
	v_perm_b32 v82, v110, v106, s79
	v_perm_b32 v83, v81, v79, s71
	v_perm_b32 v79, v81, v79, s80
	v_dot4c_i32_i8_e32 v85, v79, v64
	v_perm_b32 v79, v82, v80, s71
	v_dot4c_i32_i8_e32 v86, v79, v64
	v_perm_b32 v79, v82, v80, s80
	v_dot4c_i32_i8_e32 v88, v79, v64
	v_perm_b32 v79, v103, v99, s78
	v_perm_b32 v81, v111, v107, s78
	v_dot4c_i32_i8_e32 v84, v83, v64
	v_perm_b32 v80, v103, v99, s79
	v_perm_b32 v82, v111, v107, s79
	v_perm_b32 v83, v81, v79, s71
	v_perm_b32 v79, v81, v79, s80
	v_dot4c_i32_i8_e32 v87, v79, v64
	v_perm_b32 v79, v82, v80, s71
	v_dot4c_i32_i8_e32 v90, v79, v64
	v_perm_b32 v79, v82, v80, s80
	v_dot4c_i32_i8_e32 v91, v79, v64
	s_waitcnt vmcnt(6)
	v_perm_b32 v79, v116, v112, s78
	s_waitcnt vmcnt(4)
; __device__ __forceinline__ void peer_expert_phase(const Args& a, int layer, LAS unsigned char* lds, int G, int bid) {
;     ...
; #pragma unroll
;                 for (int G4 = 0; G4 < 4; ++G4)
; #pragma unroll
;                     for (int q = 0; q < 4; ++q) {
;                         const unsigned a_ = r[4 * G4][q], b_ = r[4 * G4 + 1][q], c_ = r[4 * G4 + 2][q], d_ = r[4 * G4 + 3][q];
;                         const unsigned ablo = __builtin_amdgcn_perm(b_, a_, 0x05010400u), abhi = __builtin_amdgcn_perm(b_, a_, 0x07030602u), cdlo = __builtin_amdgcn_perm(d_, c_, 0x05010400u), cdhi = __builtin_amdgcn_perm(d_, c_, 0x07030602u);
;                         iac[4 * q + 0] = __builtin_amdgcn_sdot4((int)__builtin_amdgcn_perm(cdlo, ablo, 0x05040100u), (int)W4[i][G4], iac[4 * q + 0], false);
;                         iac[4 * q + 1] = __builtin_amdgcn_sdot4((int)__builtin_amdgcn_perm(cdlo, ablo, 0x07060302u), (int)W4[i][G4], iac[4 * q + 1], false);
;                         iac[4 * q + 2] = __builtin_amdgcn_sdot4((int)__builtin_amdgcn_perm(cdhi, abhi, 0x05040100u), (int)W4[i][G4], iac[4 * q + 2], false);
;                         iac[4 * q + 3] = __builtin_amdgcn_sdot4((int)__builtin_amdgcn_perm(cdhi, abhi, 0x07060302u), (int)W4[i][G4], iac[4 * q + 3], false); }
;                 f32x2 ac[8];
; #pragma unroll
;                 for (int q = 0; q < 8; ++q) ac[q] = (f32x2){(float)iac[2 * q] * wsc[i], (float)iac[2 * q + 1] * wsc[i]};
;                 f32x2 b4_[4], b2_[2], b1_;
; #pragma unroll
;                 for (int q = 0; q < 4; ++q) { const f32x2 snd = (lane & 32) ? ac[q] : ac[q + 4], kp = (lane & 32) ? ac[q + 4] : ac[q]; b4_[q] = (f32x2){kp.x + __shfl_xor(snd.x, 32), kp.y + __shfl_xor(snd.y, 32)}; }
; #pragma unroll
;                 for (int q = 0; q < 2; ++q) { const f32x2 snd = (lane & 16) ? b4_[q] : b4_[q + 2], kp = (lane & 16) ? b4_[q + 2] : b4_[q]; b2_[q] = (f32x2){kp.x + __shfl_xor(snd.x, 16), kp.y + __shfl_xor(snd.y, 16)}; }
;                 { const f32x2 snd = (lane & 8) ? b2_[0] : b2_[1], kp = (lane & 8) ? b2_[1] : b2_[0]; b1_ = (f32x2){kp.x + __shfl_xor(snd.x, 8), kp.y + __shfl_xor(snd.y, 8)}; }
	v_perm_b32 v81, v124, v120, s78
	v_dot4c_i32_i8_e32 v89, v83, v64
	v_perm_b32 v80, v116, v112, s79
	v_perm_b32 v82, v124, v120, s79
	v_perm_b32 v83, v81, v79, s71
	v_perm_b32 v79, v81, v79, s80
	v_dot4c_i32_i8_e32 v137, v79, v65
	v_perm_b32 v79, v82, v80, s71
	v_dot4c_i32_i8_e32 v138, v79, v65
	v_perm_b32 v79, v82, v80, s80
	v_dot4c_i32_i8_e32 v139, v79, v65
	v_perm_b32 v79, v117, v113, s78
	v_perm_b32 v81, v125, v121, s78
	v_dot4c_i32_i8_e32 v136, v83, v65
	v_perm_b32 v80, v117, v113, s79
	v_perm_b32 v82, v125, v121, s79
	v_perm_b32 v83, v81, v79, s71
	v_perm_b32 v79, v81, v79, s80
	v_dot4c_i32_i8_e32 v141, v79, v65
	v_perm_b32 v79, v82, v80, s71
	v_dot4c_i32_i8_e32 v142, v79, v65
	v_perm_b32 v79, v82, v80, s80
	v_dot4c_i32_i8_e32 v143, v79, v65
	v_perm_b32 v79, v118, v114, s78
	v_perm_b32 v81, v126, v122, s78
	v_dot4c_i32_i8_e32 v140, v83, v65
	v_perm_b32 v80, v118, v114, s79
	v_perm_b32 v82, v126, v122, s79
	v_perm_b32 v83, v81, v79, s71
	v_perm_b32 v79, v81, v79, s80
	v_dot4c_i32_i8_e32 v85, v79, v65
	v_perm_b32 v79, v82, v80, s71
	v_dot4c_i32_i8_e32 v86, v79, v65
	v_perm_b32 v79, v82, v80, s80
	v_dot4c_i32_i8_e32 v88, v79, v65
	v_perm_b32 v79, v119, v115, s78
	v_perm_b32 v81, v127, v123, s78
	v_dot4c_i32_i8_e32 v84, v83, v65
	v_perm_b32 v80, v119, v115, s79
	v_perm_b32 v82, v127, v123, s79
	v_perm_b32 v83, v81, v79, s71
	v_perm_b32 v79, v81, v79, s80
	v_dot4c_i32_i8_e32 v87, v79, v65
	v_perm_b32 v79, v82, v80, s71
	v_dot4c_i32_i8_e32 v90, v79, v65
	v_perm_b32 v79, v82, v80, s80
	v_dot4c_i32_i8_e32 v91, v79, v65
	s_waitcnt vmcnt(2)
	v_perm_b32 v79, v132, v128, s78
	s_waitcnt vmcnt(0)
	v_perm_b32 v81, v4, v0, s78
	v_perm_b32 v0, v4, v0, s79
	v_perm_b32 v4, v81, v79, s71
	v_perm_b32 v80, v132, v128, s79
	v_dot4c_i32_i8_e32 v136, v4, v66
	v_perm_b32 v4, v81, v79, s80
	v_dot4c_i32_i8_e32 v137, v4, v66
	v_perm_b32 v4, v0, v80, s71
	v_perm_b32 v0, v0, v80, s80
	v_dot4c_i32_i8_e32 v139, v0, v66
	v_perm_b32 v0, v133, v129, s78
	v_perm_b32 v79, v5, v1, s78
	v_dot4c_i32_i8_e32 v138, v4, v66
	v_perm_b32 v4, v133, v129, s79
	v_perm_b32 v1, v5, v1, s79
	v_perm_b32 v5, v79, v0, s71
	v_perm_b32 v0, v79, v0, s80
	v_dot4c_i32_i8_e32 v141, v0, v66
	v_perm_b32 v0, v1, v4, s71
	v_dot4c_i32_i8_e32 v142, v0, v66
	v_perm_b32 v0, v1, v4, s80
	v_dot4c_i32_i8_e32 v143, v0, v66
	v_perm_b32 v0, v134, v130, s78
	v_perm_b32 v4, v6, v2, s78
	v_dot4c_i32_i8_e32 v140, v5, v66
	v_perm_b32 v1, v134, v130, s79
	v_perm_b32 v2, v6, v2, s79
	v_perm_b32 v5, v4, v0, s71
	v_perm_b32 v0, v4, v0, s80
	v_dot4c_i32_i8_e32 v85, v0, v66
	v_perm_b32 v0, v2, v1, s71
	v_dot4c_i32_i8_e32 v86, v0, v66
	v_perm_b32 v0, v2, v1, s80
	v_dot4c_i32_i8_e32 v88, v0, v66
	v_lshl_add_u64 v[0:1], v[26:27], 0, s[24:25]
	v_dot4c_i32_i8_e32 v84, v5, v66
	v_perm_b32 v2, v135, v131, s78
	v_perm_b32 v5, v7, v3, s78
	v_perm_b32 v4, v135, v131, s79
	v_perm_b32 v3, v7, v3, s79
	v_perm_b32 v6, v5, v2, s71
	v_perm_b32 v2, v5, v2, s80
	v_dot4c_i32_i8_e32 v87, v2, v66
	v_perm_b32 v2, v3, v4, s71
	v_dot4c_i32_i8_e32 v89, v83, v65
	v_dot4c_i32_i8_e32 v90, v2, v66
	v_perm_b32 v2, v3, v4, s80
	v_dot4c_i32_i8_e32 v89, v6, v66
	v_dot4c_i32_i8_e32 v91, v2, v66
	v_cvt_f32_i32_e32 v3, v137
	v_cvt_f32_i32_e32 v2, v136
	v_cvt_f32_i32_e32 v5, v139
	v_cvt_f32_i32_e32 v4, v138
	v_cvt_f32_i32_e32 v83, v85
	v_cvt_f32_i32_e32 v82, v84
	v_cvt_f32_i32_e32 v85, v88
	v_cvt_f32_i32_e32 v84, v86
	v_cvt_f32_i32_e32 v7, v141
	v_cvt_f32_i32_e32 v6, v140
	v_cvt_f32_i32_e32 v81, v143
	v_cvt_f32_i32_e32 v80, v142
	v_cvt_f32_i32_e32 v87, v87
	v_cvt_f32_i32_e32 v86, v89
	v_cvt_f32_i32_e32 v89, v91
	v_cvt_f32_i32_e32 v88, v90
	v_pk_mul_f32 v[2:3], v[18:19], v[2:3]
	v_pk_mul_f32 v[4:5], v[18:19], v[4:5]
	v_pk_mul_f32 v[82:83], v[18:19], v[82:83]
	v_pk_mul_f32 v[84:85], v[18:19], v[84:85]
	v_pk_mul_f32 v[6:7], v[18:19], v[6:7]
	v_pk_mul_f32 v[80:81], v[18:19], v[80:81]
	v_pk_mul_f32 v[86:87], v[18:19], v[86:87]
	v_pk_mul_f32 v[88:89], v[18:19], v[88:89]
	v_cndmask_b32_e64 v91, v3, v83, s[0:1]
	v_cndmask_b32_e64 v3, v83, v3, s[0:1]
	v_cndmask_b32_e64 v83, v5, v85, s[0:1]
	v_cndmask_b32_e64 v90, v2, v82, s[0:1]
	v_cndmask_b32_e64 v92, v4, v84, s[0:1]
	ds_bpermute_b32 v93, v29, v83
	v_cndmask_b32_e64 v2, v82, v2, s[0:1]
	v_cndmask_b32_e64 v5, v85, v5, s[0:1]
	v_cndmask_b32_e64 v4, v84, v4, s[0:1]
	v_cndmask_b32_e64 v83, v7, v87, s[0:1]
	v_cndmask_b32_e64 v82, v6, v86, s[0:1]
	v_cndmask_b32_e64 v85, v81, v89, s[0:1]
	v_cndmask_b32_e64 v84, v80, v88, s[0:1]
	ds_bpermute_b32 v90, v29, v90
	ds_bpermute_b32 v91, v29, v91
	ds_bpermute_b32 v92, v29, v92
	ds_bpermute_b32 v82, v29, v82
	ds_bpermute_b32 v83, v29, v83
	ds_bpermute_b32 v84, v29, v84
	ds_bpermute_b32 v85, v29, v85
	v_cndmask_b32_e64 v7, v87, v7, s[0:1]
	v_cndmask_b32_e64 v6, v86, v6, s[0:1]
	v_cndmask_b32_e64 v81, v89, v81, s[0:1]
	v_cndmask_b32_e64 v80, v88, v80, s[0:1]
	s_waitcnt lgkmcnt(0)
	v_pk_add_f32 v[2:3], v[2:3], v[90:91]
	v_pk_add_f32 v[4:5], v[4:5], v[92:93]
	v_pk_add_f32 v[6:7], v[6:7], v[82:83]
	v_pk_add_f32 v[80:81], v[80:81], v[84:85]
	v_cndmask_b32_e64 v83, v3, v7, s[2:3]
	v_cndmask_b32_e64 v82, v2, v6, s[2:3]
	v_cndmask_b32_e64 v3, v7, v3, s[2:3]
	v_cndmask_b32_e64 v7, v5, v81, s[2:3]
	v_cndmask_b32_e64 v84, v4, v80, s[2:3]
	ds_bpermute_b32 v82, v30, v82
	ds_bpermute_b32 v83, v30, v83
	ds_bpermute_b32 v84, v30, v84
	ds_bpermute_b32 v85, v30, v7
	v_cndmask_b32_e64 v2, v6, v2, s[2:3]
	v_cndmask_b32_e64 v5, v81, v5, s[2:3]
	v_cndmask_b32_e64 v4, v80, v4, s[2:3]
	s_waitcnt lgkmcnt(2)
	v_pk_add_f32 v[2:3], v[2:3], v[82:83]
	s_waitcnt lgkmcnt(0)
	v_pk_add_f32 v[4:5], v[4:5], v[84:85]
	s_waitcnt vmcnt(0)
; __device__ __forceinline__ void peer_expert_phase(const Args& a, int layer, LAS unsigned char* lds, int G, int bid) {
;     ...
;                 for (int c = 0; c < 16; ++c) { const unsigned eo = (unsigned)__shfl((int)(c < 8 ? eoa[i] : eob[i]), (8 * c + g8) & 63); r[c] = *(const u32x4*)(pvs + (eo + lo16)); }
;                 int iac[16];
; #pragma unroll
;                 for (int q = 0; q < 16; ++q) iac[q] = 0;
; #pragma unroll
;                 for (int G4 = 0; G4 < 4; ++G4)
; #pragma unroll
;                     for (int q = 0; q < 4; ++q) {
;                         const unsigned a_ = r[4 * G4][q], b_ = r[4 * G4 + 1][q], c_ = r[4 * G4 + 2][q], d_ = r[4 * G4 + 3][q];
;                         const unsigned ablo = __builtin_amdgcn_perm(b_, a_, 0x05010400u), abhi = __builtin_amdgcn_perm(b_, a_, 0x07030602u), cdlo = __builtin_amdgcn_perm(d_, c_, 0x05010400u), cdhi = __builtin_amdgcn_perm(d_, c_, 0x07030602u);
;                         iac[4 * q + 0] = __builtin_amdgcn_sdot4((int)__builtin_amdgcn_perm(cdlo, ablo, 0x05040100u), (int)W4[i][G4], iac[4 * q + 0], false);
;                         iac[4 * q + 1] = __builtin_amdgcn_sdot4((int)__builtin_amdgcn_perm(cdlo, ablo, 0x07060302u), (int)W4[i][G4], iac[4 * q + 1], false);
;                         iac[4 * q + 2] = __builtin_amdgcn_sdot4((int)__builtin_amdgcn_perm(cdhi, abhi, 0x05040100u), (int)W4[i][G4], iac[4 * q + 2], false);
;                         iac[4 * q + 3] = __builtin_amdgcn_sdot4((int)__builtin_amdgcn_perm(cdhi, abhi, 0x07060302u), (int)W4[i][G4], iac[4 * q + 3], false); }
;                 f32x2 ac[8];
; #pragma unroll
;                 for (int q = 0; q < 8; ++q) ac[q] = (f32x2){(float)iac[2 * q] * wsc[i], (float)iac[2 * q + 1] * wsc[i]};
;                 f32x2 b4_[4], b2_[2], b1_;
; #pragma unroll
;                 for (int q = 0; q < 4; ++q) { const f32x2 snd = (lane & 32) ? ac[q] : ac[q + 4], kp = (lane & 32) ? ac[q + 4] : ac[q]; b4_[q] = (f32x2){kp.x + __shfl_xor(snd.x, 32), kp.y + __shfl_xor(snd.y, 32)}; }
; #pragma unroll
;                 for (int q = 0; q < 2; ++q) { const f32x2 snd = (lane & 16) ? b4_[q] : b4_[q + 2], kp = (lane & 16) ? b4_[q + 2] : b4_[q]; b2_[q] = (f32x2){kp.x + __shfl_xor(snd.x, 16), kp.y + __shfl_xor(snd.y, 16)}; }
	v_and_b32_e32 v80, 0xffff0000, v240
	v_cndmask_b32_e64 v6, v3, v5, s[4:5]
	v_cndmask_b32_e64 v7, v2, v4, s[4:5]
	ds_bpermute_b32 v7, v31, v7
	ds_bpermute_b32 v6, v31, v6
	v_cndmask_b32_e64 v2, v4, v2, s[4:5]
	v_cndmask_b32_e64 v3, v5, v3, s[4:5]
	v_lshlrev_b32_e32 v79, 16, v240
	s_waitcnt lgkmcnt(1)
	v_add_f32_e32 v2, v2, v7
	s_waitcnt lgkmcnt(0)
	v_add_f32_e32 v3, v3, v6
	v_add_f32_e32 v3, v3, v80
	v_add_f32_e32 v2, v2, v79
	v_cvt_pk_bf16_f32 v4, v2, v3
	global_store_dword v[0:1], v4, off
	global_load_dwordx4 v[0:3], v163, s[22:23]
	s_nop 0
	global_load_dwordx4 v[80:83], v164, s[22:23]
	global_load_dwordx4 v[84:87], v165, s[22:23]
	global_load_dwordx4 v[88:91], v166, s[22:23]
	global_load_dwordx4 v[92:95], v167, s[22:23]
	global_load_dwordx4 v[96:99], v168, s[22:23]
	global_load_dwordx4 v[100:103], v169, s[22:23]
	global_load_dwordx4 v[104:107], v170, s[22:23]
	global_load_dwordx4 v[108:111], v171, s[22:23]
	s_nop 0
	global_load_dwordx4 v[112:115], v172, s[22:23]
	s_nop 0
	global_load_dwordx4 v[116:119], v173, s[22:23]
	s_nop 0
	global_load_dwordx4 v[120:123], v174, s[22:23]
	s_nop 0
	global_load_dwordx4 v[124:127], v175, s[22:23]
	s_nop 0
	global_load_dwordx4 v[128:131], v176, s[22:23]
	s_nop 0
	global_load_dwordx4 v[132:135], v177, s[22:23]
	s_nop 0
	global_load_dwordx4 v[136:139], v178, s[22:23]
	v_mov_b32_e32 v5, 0
	v_mov_b32_e32 v6, 0
	v_mov_b32_e32 v144, 0
	v_mov_b32_e32 v141, 0
	v_mov_b32_e32 v143, 0
	v_mov_b32_e32 v79, 0
	v_mov_b32_e32 v142, 0
	v_mov_b32_e32 v140, 0
	v_mov_b32_e32 v7, 0
	v_mov_b32_e32 v145, 0
	s_andn2_b64 vcc, exec, s[42:43]
	s_waitcnt vmcnt(14)
	v_perm_b32 v146, v80, v0, s78
	v_perm_b32 v0, v80, v0, s79
	s_waitcnt vmcnt(12)
	v_perm_b32 v80, v88, v84, s78
	v_perm_b32 v84, v88, v84, s79
	v_perm_b32 v88, v81, v1, s78
	v_perm_b32 v1, v81, v1, s79
	v_perm_b32 v81, v89, v85, s78
	v_perm_b32 v85, v89, v85, s79
	v_perm_b32 v89, v82, v2, s78
	v_perm_b32 v2, v82, v2, s79
	v_perm_b32 v82, v90, v86, s78
	v_perm_b32 v86, v90, v86, s79
	v_perm_b32 v90, v80, v146, s71
	v_perm_b32 v80, v80, v146, s80
	v_perm_b32 v146, v84, v0, s71
	v_perm_b32 v0, v84, v0, s80
	v_perm_b32 v84, v81, v88, s71
	v_perm_b32 v81, v81, v88, s80
	v_perm_b32 v88, v85, v1, s71
	v_perm_b32 v1, v85, v1, s80
	v_perm_b32 v85, v82, v89, s71
	v_dot4c_i32_i8_e32 v5, v0, v67
	v_dot4c_i32_i8_e32 v6, v84, v67
	v_perm_b32 v0, v86, v2, s71
	v_mov_b32_e32 v84, 0
	v_dot4c_i32_i8_e32 v144, v85, v67
	v_dot4c_i32_i8_e32 v84, v0, v67
	v_perm_b32 v0, v86, v2, s80
	v_mov_b32_e32 v85, 0
	v_dot4c_i32_i8_e32 v85, v0, v67
	v_perm_b32 v0, v83, v3, s78
	v_perm_b32 v2, v91, v87, s78
	v_dot4c_i32_i8_e32 v141, v80, v67
	v_dot4c_i32_i8_e32 v143, v1, v67
	v_perm_b32 v1, v83, v3, s79
	v_perm_b32 v3, v91, v87, s79
	v_perm_b32 v80, v2, v0, s71
	v_perm_b32 v0, v2, v0, s80
	v_mov_b32_e32 v87, 0
	v_dot4c_i32_i8_e32 v79, v88, v67
	v_dot4c_i32_i8_e32 v87, v0, v67
	v_perm_b32 v0, v3, v1, s71
	v_mov_b32_e32 v88, 0
	v_perm_b32 v82, v82, v89, s80
	v_dot4c_i32_i8_e32 v88, v0, v67
	v_perm_b32 v0, v3, v1, s80
	v_mov_b32_e32 v89, 0
	v_mov_b32_e32 v86, 0
	v_dot4c_i32_i8_e32 v89, v0, v67
	s_waitcnt vmcnt(10)
	v_perm_b32 v0, v96, v92, s78
	s_waitcnt vmcnt(8)
	v_perm_b32 v2, v104, v100, s78
	v_dot4c_i32_i8_e32 v86, v80, v67
	v_perm_b32 v1, v96, v92, s79
	v_perm_b32 v3, v104, v100, s79
	v_perm_b32 v80, v2, v0, s71
	v_perm_b32 v0, v2, v0, s80
	v_dot4c_i32_i8_e32 v142, v146, v67
	v_dot4c_i32_i8_e32 v141, v0, v68
	v_perm_b32 v0, v3, v1, s71
	v_dot4c_i32_i8_e32 v142, v0, v68
	v_perm_b32 v0, v3, v1, s80
	v_dot4c_i32_i8_e32 v140, v90, v67
	v_dot4c_i32_i8_e32 v5, v0, v68
	v_perm_b32 v0, v97, v93, s78
	v_perm_b32 v2, v105, v101, s78
	v_dot4c_i32_i8_e32 v7, v81, v67
	v_dot4c_i32_i8_e32 v140, v80, v68
	v_perm_b32 v1, v97, v93, s79
	v_perm_b32 v3, v105, v101, s79
	v_perm_b32 v80, v2, v0, s71
	v_perm_b32 v0, v2, v0, s80
	v_dot4c_i32_i8_e32 v7, v0, v68
	v_perm_b32 v0, v3, v1, s71
	v_dot4c_i32_i8_e32 v79, v0, v68
	v_perm_b32 v0, v3, v1, s80
	v_dot4c_i32_i8_e32 v143, v0, v68
	v_perm_b32 v0, v98, v94, s78
	v_perm_b32 v2, v106, v102, s78
	v_dot4c_i32_i8_e32 v145, v82, v67
	v_dot4c_i32_i8_e32 v6, v80, v68
	v_perm_b32 v1, v98, v94, s79
	v_perm_b32 v3, v106, v102, s79
	v_perm_b32 v80, v2, v0, s71
	v_perm_b32 v0, v2, v0, s80
	v_dot4c_i32_i8_e32 v145, v0, v68
	v_perm_b32 v0, v3, v1, s71
	v_dot4c_i32_i8_e32 v84, v0, v68
	v_perm_b32 v0, v3, v1, s80
	v_dot4c_i32_i8_e32 v85, v0, v68
	v_perm_b32 v0, v99, v95, s78
	v_perm_b32 v2, v107, v103, s78
	v_dot4c_i32_i8_e32 v144, v80, v68
	v_perm_b32 v1, v99, v95, s79
	v_perm_b32 v3, v107, v103, s79
	v_perm_b32 v80, v2, v0, s71
	v_perm_b32 v0, v2, v0, s80
	v_dot4c_i32_i8_e32 v87, v0, v68
	v_perm_b32 v0, v3, v1, s71
	v_dot4c_i32_i8_e32 v88, v0, v68
	v_perm_b32 v0, v3, v1, s80
	v_dot4c_i32_i8_e32 v89, v0, v68
	s_waitcnt vmcnt(6)
	v_perm_b32 v0, v112, v108, s78
	s_waitcnt vmcnt(4)
	v_perm_b32 v2, v120, v116, s78
	v_dot4c_i32_i8_e32 v86, v80, v68
	v_perm_b32 v1, v112, v108, s79
	v_perm_b32 v3, v120, v116, s79
	v_perm_b32 v80, v2, v0, s71
	v_perm_b32 v0, v2, v0, s80
	v_dot4c_i32_i8_e32 v141, v0, v69
	v_perm_b32 v0, v3, v1, s71
	v_dot4c_i32_i8_e32 v142, v0, v69
	v_perm_b32 v0, v3, v1, s80
	v_dot4c_i32_i8_e32 v5, v0, v69
	v_perm_b32 v0, v113, v109, s78
	v_perm_b32 v2, v121, v117, s78
	v_dot4c_i32_i8_e32 v140, v80, v69
	v_perm_b32 v1, v113, v109, s79
	v_perm_b32 v3, v121, v117, s79
	v_perm_b32 v80, v2, v0, s71
	v_perm_b32 v0, v2, v0, s80
	v_dot4c_i32_i8_e32 v7, v0, v69
	v_perm_b32 v0, v3, v1, s71
	v_dot4c_i32_i8_e32 v79, v0, v69
	v_perm_b32 v0, v3, v1, s80
	v_dot4c_i32_i8_e32 v143, v0, v69
	v_perm_b32 v0, v114, v110, s78
	v_perm_b32 v2, v122, v118, s78
	v_dot4c_i32_i8_e32 v6, v80, v69
	v_perm_b32 v1, v114, v110, s79
	v_perm_b32 v3, v122, v118, s79
	v_perm_b32 v80, v2, v0, s71
	v_perm_b32 v0, v2, v0, s80
	v_dot4c_i32_i8_e32 v145, v0, v69
	v_perm_b32 v0, v3, v1, s71
	v_dot4c_i32_i8_e32 v84, v0, v69
	v_perm_b32 v0, v3, v1, s80
	v_dot4c_i32_i8_e32 v85, v0, v69
	v_perm_b32 v0, v115, v111, s78
	v_perm_b32 v2, v123, v119, s78
	v_dot4c_i32_i8_e32 v144, v80, v69
	v_perm_b32 v1, v115, v111, s79
	v_perm_b32 v3, v123, v119, s79
	v_perm_b32 v80, v2, v0, s71
	v_perm_b32 v0, v2, v0, s80
	v_dot4c_i32_i8_e32 v87, v0, v69
	v_perm_b32 v0, v3, v1, s71
	v_dot4c_i32_i8_e32 v88, v0, v69
	v_perm_b32 v0, v3, v1, s80
	v_dot4c_i32_i8_e32 v89, v0, v69
	s_waitcnt vmcnt(2)
; __device__ __forceinline__ unsigned pk2(float lo, float hi) { unsigned r; asm volatile("v_cvt_pk_bf16_f32 %0, %1, %2" : "=v"(r) : "v"(lo), "v"(hi)); return r; }
; __device__ __forceinline__ float bflo(unsigned u) { return __uint_as_float(u << 16); }
; __device__ __forceinline__ void peer_expert_phase(const Args& a, int layer, LAS unsigned char* lds, int G, int bid) {
;     ...
;                         iac[4 * q + 0] = __builtin_amdgcn_sdot4((int)__builtin_amdgcn_perm(cdlo, ablo, 0x05040100u), (int)W4[i][G4], iac[4 * q + 0], false);
;                         iac[4 * q + 1] = __builtin_amdgcn_sdot4((int)__builtin_amdgcn_perm(cdlo, ablo, 0x07060302u), (int)W4[i][G4], iac[4 * q + 1], false);
;                         iac[4 * q + 2] = __builtin_amdgcn_sdot4((int)__builtin_amdgcn_perm(cdhi, abhi, 0x05040100u), (int)W4[i][G4], iac[4 * q + 2], false);
;                         iac[4 * q + 3] = __builtin_amdgcn_sdot4((int)__builtin_amdgcn_perm(cdhi, abhi, 0x07060302u), (int)W4[i][G4], iac[4 * q + 3], false); }
;                 f32x2 ac[8];
; #pragma unroll
;                 for (int q = 0; q < 8; ++q) ac[q] = (f32x2){(float)iac[2 * q] * wsc[i], (float)iac[2 * q + 1] * wsc[i]};
;                 f32x2 b4_[4], b2_[2], b1_;
; #pragma unroll
;                 for (int q = 0; q < 4; ++q) { const f32x2 snd = (lane & 32) ? ac[q] : ac[q + 4], kp = (lane & 32) ? ac[q + 4] : ac[q]; b4_[q] = (f32x2){kp.x + __shfl_xor(snd.x, 32), kp.y + __shfl_xor(snd.y, 32)}; }
; #pragma unroll
;                 for (int q = 0; q < 2; ++q) { const f32x2 snd = (lane & 16) ? b4_[q] : b4_[q + 2], kp = (lane & 16) ? b4_[q + 2] : b4_[q]; b2_[q] = (f32x2){kp.x + __shfl_xor(snd.x, 16), kp.y + __shfl_xor(snd.y, 16)}; }
;                 { const f32x2 snd = (lane & 8) ? b2_[0] : b2_[1], kp = (lane & 8) ? b2_[1] : b2_[0]; b1_ = (f32x2){kp.x + __shfl_xor(snd.x, 8), kp.y + __shfl_xor(snd.y, 8)}; }
;                 const size_t off = (size_t)tok * DM + s * 128 + 16 * l7 + 2 * g8;
;                 const unsigned hb0 = *(const unsigned*)(H + off); f32x2 hn = {bflo(hb0) + b1_.x, bfhi(hb0) + b1_.y};
;                 if (ok) {
;                     { const unsigned hb1 = pk2(hn.x, hn.y); *(unsigned*)(H + off) = hb1; hn = (f32x2){bflo(hb1), bfhi(hb1)}; }
;                     ssq[i] += hn.x * hn.x + hn.y * hn.y; hgm[i] = fmaxf(hgm[i], fmaxf(fabsf(hn.x * gsl.x), fabsf(hn.y * gsl.y))); }
	v_perm_b32 v0, v128, v124, s78
	s_waitcnt vmcnt(0)
	v_perm_b32 v2, v136, v132, s78
	v_dot4c_i32_i8_e32 v86, v80, v69
	v_perm_b32 v1, v128, v124, s79
	v_perm_b32 v3, v136, v132, s79
	v_perm_b32 v80, v2, v0, s71
	v_perm_b32 v0, v2, v0, s80
	v_dot4c_i32_i8_e32 v141, v0, v70
	v_perm_b32 v0, v3, v1, s71
	v_dot4c_i32_i8_e32 v142, v0, v70
	v_perm_b32 v0, v3, v1, s80
	v_dot4c_i32_i8_e32 v5, v0, v70
	v_perm_b32 v0, v129, v125, s78
	v_perm_b32 v2, v137, v133, s78
	v_dot4c_i32_i8_e32 v140, v80, v70
	v_perm_b32 v1, v129, v125, s79
	v_perm_b32 v3, v137, v133, s79
	v_perm_b32 v80, v2, v0, s71
	v_perm_b32 v0, v2, v0, s80
	v_dot4c_i32_i8_e32 v7, v0, v70
	v_perm_b32 v0, v3, v1, s71
	v_dot4c_i32_i8_e32 v79, v0, v70
	v_perm_b32 v0, v3, v1, s80
	v_dot4c_i32_i8_e32 v143, v0, v70
	v_perm_b32 v0, v130, v126, s78
	v_perm_b32 v2, v138, v134, s78
	v_dot4c_i32_i8_e32 v6, v80, v70
	v_perm_b32 v1, v130, v126, s79
	v_perm_b32 v3, v138, v134, s79
	v_perm_b32 v80, v2, v0, s71
	v_perm_b32 v0, v2, v0, s80
	v_dot4c_i32_i8_e32 v145, v0, v70
	v_perm_b32 v0, v3, v1, s71
	v_dot4c_i32_i8_e32 v84, v0, v70
	v_perm_b32 v0, v3, v1, s80
	v_dot4c_i32_i8_e32 v85, v0, v70
	v_perm_b32 v0, v131, v127, s78
	v_perm_b32 v2, v139, v135, s78
	v_dot4c_i32_i8_e32 v144, v80, v70
	v_perm_b32 v1, v131, v127, s79
	v_perm_b32 v3, v139, v135, s79
	v_perm_b32 v80, v2, v0, s71
	v_perm_b32 v0, v2, v0, s80
	v_dot4c_i32_i8_e32 v87, v0, v70
	v_perm_b32 v0, v3, v1, s71
	v_dot4c_i32_i8_e32 v88, v0, v70
	v_perm_b32 v0, v3, v1, s80
	v_dot4c_i32_i8_e32 v89, v0, v70
	v_cvt_f32_i32_e32 v1, v141
	v_cvt_f32_i32_e32 v0, v140
	v_cvt_f32_i32_e32 v83, v145
	v_cvt_f32_i32_e32 v82, v144
	v_dot4c_i32_i8_e32 v86, v80, v70
	v_cvt_f32_i32_e32 v3, v5
	v_cvt_f32_i32_e32 v2, v142
	v_cvt_f32_i32_e32 v85, v85
	v_cvt_f32_i32_e32 v84, v84
	v_cvt_f32_i32_e32 v7, v7
	v_cvt_f32_i32_e32 v6, v6
	v_cvt_f32_i32_e32 v87, v87
	v_cvt_f32_i32_e32 v86, v86
	v_cvt_f32_i32_e32 v81, v143
	v_cvt_f32_i32_e32 v80, v79
	v_cvt_f32_i32_e32 v89, v89
	v_cvt_f32_i32_e32 v88, v88
	v_pk_mul_f32 v[0:1], v[20:21], v[0:1]
	v_pk_mul_f32 v[82:83], v[20:21], v[82:83]
	v_pk_mul_f32 v[2:3], v[20:21], v[2:3]
	v_pk_mul_f32 v[84:85], v[20:21], v[84:85]
	v_cndmask_b32_e64 v5, v1, v83, s[0:1]
	v_cndmask_b32_e64 v79, v0, v82, s[0:1]
	v_pk_mul_f32 v[6:7], v[20:21], v[6:7]
	v_pk_mul_f32 v[86:87], v[20:21], v[86:87]
	ds_bpermute_b32 v90, v29, v79
	ds_bpermute_b32 v91, v29, v5
	v_cndmask_b32_e64 v5, v3, v85, s[0:1]
	v_cndmask_b32_e64 v79, v2, v84, s[0:1]
	v_pk_mul_f32 v[80:81], v[20:21], v[80:81]
	v_pk_mul_f32 v[88:89], v[20:21], v[88:89]
	ds_bpermute_b32 v92, v29, v79
	ds_bpermute_b32 v93, v29, v5
	v_cndmask_b32_e64 v5, v7, v87, s[0:1]
	v_cndmask_b32_e64 v79, v6, v86, s[0:1]
	v_cndmask_b32_e64 v1, v83, v1, s[0:1]
	v_cndmask_b32_e64 v0, v82, v0, s[0:1]
	ds_bpermute_b32 v82, v29, v79
	ds_bpermute_b32 v83, v29, v5
	v_cndmask_b32_e64 v5, v81, v89, s[0:1]
	v_cndmask_b32_e64 v79, v80, v88, s[0:1]
	v_cndmask_b32_e64 v3, v85, v3, s[0:1]
	v_cndmask_b32_e64 v2, v84, v2, s[0:1]
	ds_bpermute_b32 v84, v29, v79
	ds_bpermute_b32 v85, v29, v5
	v_cndmask_b32_e64 v7, v87, v7, s[0:1]
	v_cndmask_b32_e64 v6, v86, v6, s[0:1]
	s_waitcnt lgkmcnt(0)
	v_pk_add_f32 v[0:1], v[0:1], v[90:91]
	v_pk_add_f32 v[6:7], v[6:7], v[82:83]
	v_cndmask_b32_e64 v81, v89, v81, s[0:1]
	v_cndmask_b32_e64 v80, v88, v80, s[0:1]
	v_pk_add_f32 v[2:3], v[2:3], v[92:93]
	v_pk_add_f32 v[80:81], v[80:81], v[84:85]
	v_cndmask_b32_e64 v5, v1, v7, s[2:3]
	v_cndmask_b32_e64 v79, v0, v6, s[2:3]
	v_cndmask_b32_e64 v1, v7, v1, s[2:3]
	ds_bpermute_b32 v83, v30, v5
	v_cndmask_b32_e64 v5, v3, v81, s[2:3]
	v_cndmask_b32_e64 v7, v2, v80, s[2:3]
	ds_bpermute_b32 v82, v30, v79
	ds_bpermute_b32 v84, v30, v7
	ds_bpermute_b32 v85, v30, v5
	v_cndmask_b32_e64 v0, v6, v0, s[2:3]
	v_cndmask_b32_e64 v3, v81, v3, s[2:3]
	v_cndmask_b32_e64 v2, v80, v2, s[2:3]
	s_waitcnt lgkmcnt(2)
	v_pk_add_f32 v[0:1], v[0:1], v[82:83]
	s_waitcnt lgkmcnt(0)
	v_pk_add_f32 v[2:3], v[2:3], v[84:85]
	s_nop 0
	v_cndmask_b32_e64 v6, v1, v3, s[4:5]
	v_cndmask_b32_e64 v5, v0, v2, s[4:5]
	ds_bpermute_b32 v5, v31, v5
	ds_bpermute_b32 v6, v31, v6
	s_cbranch_vccnz .LBB0_2304
	v_lshl_add_u64 v[80:81], v[26:27], 0, s[44:45]
	v_cndmask_b32_e64 v1, v3, v1, s[4:5]
	v_cndmask_b32_e64 v0, v2, v0, s[4:5]
	s_waitcnt lgkmcnt(0)
	v_add_f32_e32 v1, v1, v6
	v_add_f32_e32 v0, v0, v5
	s_waitcnt vmcnt(0)
	v_and_b32_e32 v2, 0xffff0000, v241
	v_lshlrev_b32_e32 v3, 16, v241
	v_add_f32_e32 v1, v1, v2
	v_add_f32_e32 v0, v0, v3
	v_cvt_pk_bf16_f32 v1, v0, v1
	global_store_dword v[80:81], v1, off
	v_lshlrev_b32_e32 v0, 16, v1
	v_and_b32_e32 v1, 0xffff0000, v1
	v_pk_mul_f32 v[0:1], v[0:1], v[0:1]
	s_nop 0
	v_add_f32_e32 v0, v0, v1
	v_add_f32_e32 v61, v61, v0
; __device__ __forceinline__ void peer_expert_phase(const Args& a, int layer, LAS unsigned char* lds, int G, int bid) {
;     ...
;                 for (int c = 0; c < 16; ++c) { const unsigned eo = (unsigned)__shfl((int)(c < 8 ? eoa[i] : eob[i]), (8 * c + g8) & 63); r[c] = *(const u32x4*)(pvs + (eo + lo16)); }
;                 int iac[16];
; #pragma unroll
;                 for (int q = 0; q < 16; ++q) iac[q] = 0;
; #pragma unroll
;                 for (int G4 = 0; G4 < 4; ++G4)
; #pragma unroll
;                     for (int q = 0; q < 4; ++q) {
;                         const unsigned a_ = r[4 * G4][q], b_ = r[4 * G4 + 1][q], c_ = r[4 * G4 + 2][q], d_ = r[4 * G4 + 3][q];
;                         const unsigned ablo = __builtin_amdgcn_perm(b_, a_, 0x05010400u), abhi = __builtin_amdgcn_perm(b_, a_, 0x07030602u), cdlo = __builtin_amdgcn_perm(d_, c_, 0x05010400u), cdhi = __builtin_amdgcn_perm(d_, c_, 0x07030602u);
;                         iac[4 * q + 0] = __builtin_amdgcn_sdot4((int)__builtin_amdgcn_perm(cdlo, ablo, 0x05040100u), (int)W4[i][G4], iac[4 * q + 0], false);
;                         iac[4 * q + 1] = __builtin_amdgcn_sdot4((int)__builtin_amdgcn_perm(cdlo, ablo, 0x07060302u), (int)W4[i][G4], iac[4 * q + 1], false);
;                         iac[4 * q + 2] = __builtin_amdgcn_sdot4((int)__builtin_amdgcn_perm(cdhi, abhi, 0x05040100u), (int)W4[i][G4], iac[4 * q + 2], false);
;                         iac[4 * q + 3] = __builtin_amdgcn_sdot4((int)__builtin_amdgcn_perm(cdhi, abhi, 0x07060302u), (int)W4[i][G4], iac[4 * q + 3], false); }
.LBB0_2304:
	s_waitcnt lgkmcnt(1)
	s_waitcnt lgkmcnt(0)
	global_load_dwordx4 v[0:3], v179, s[22:23]
	s_nop 0
	global_load_dwordx4 v[80:83], v180, s[22:23]
	global_load_dwordx4 v[84:87], v181, s[22:23]
	global_load_dwordx4 v[88:91], v182, s[22:23]
	global_load_dwordx4 v[92:95], v183, s[22:23]
	global_load_dwordx4 v[96:99], v184, s[22:23]
	global_load_dwordx4 v[100:103], v185, s[22:23]
	global_load_dwordx4 v[104:107], v186, s[22:23]
	global_load_dwordx4 v[108:111], v187, s[22:23]
	s_nop 0
	global_load_dwordx4 v[112:115], v188, s[22:23]
	s_nop 0
	global_load_dwordx4 v[116:119], v189, s[22:23]
	s_nop 0
	global_load_dwordx4 v[120:123], v190, s[22:23]
	s_nop 0
	global_load_dwordx4 v[124:127], v191, s[22:23]
	s_nop 0
	global_load_dwordx4 v[128:131], v192, s[22:23]
	s_nop 0
	global_load_dwordx4 v[132:135], v193, s[22:23]
	s_nop 0
	global_load_dwordx4 v[136:139], v194, s[22:23]
	v_mov_b32_e32 v5, 0
	v_mov_b32_e32 v6, 0
	v_mov_b32_e32 v144, 0
	v_mov_b32_e32 v141, 0
	v_mov_b32_e32 v143, 0
	v_mov_b32_e32 v79, 0
	v_mov_b32_e32 v142, 0
	v_mov_b32_e32 v140, 0
	v_mov_b32_e32 v7, 0
	v_mov_b32_e32 v145, 0
	s_andn2_b64 vcc, exec, s[46:47]
	s_waitcnt vmcnt(14)
	v_perm_b32 v146, v80, v0, s78
	v_perm_b32 v0, v80, v0, s79
	s_waitcnt vmcnt(12)
	v_perm_b32 v80, v88, v84, s78
	v_perm_b32 v84, v88, v84, s79
	v_perm_b32 v88, v81, v1, s78
	v_perm_b32 v1, v81, v1, s79
	v_perm_b32 v81, v89, v85, s78
	v_perm_b32 v85, v89, v85, s79
	v_perm_b32 v89, v82, v2, s78
	v_perm_b32 v2, v82, v2, s79
	v_perm_b32 v82, v90, v86, s78
	v_perm_b32 v86, v90, v86, s79
	v_perm_b32 v90, v80, v146, s71
	v_perm_b32 v80, v80, v146, s80
	v_perm_b32 v146, v84, v0, s71
	v_perm_b32 v0, v84, v0, s80
	v_perm_b32 v84, v81, v88, s71
	v_perm_b32 v81, v81, v88, s80
	v_perm_b32 v88, v85, v1, s71
	v_perm_b32 v1, v85, v1, s80
	v_perm_b32 v85, v82, v89, s71
	v_dot4c_i32_i8_e32 v5, v0, v71
	v_dot4c_i32_i8_e32 v6, v84, v71
	v_perm_b32 v0, v86, v2, s71
	v_mov_b32_e32 v84, 0
	v_dot4c_i32_i8_e32 v144, v85, v71
	v_dot4c_i32_i8_e32 v84, v0, v71
	v_perm_b32 v0, v86, v2, s80
	v_mov_b32_e32 v85, 0
	v_dot4c_i32_i8_e32 v85, v0, v71
	v_perm_b32 v0, v83, v3, s78
	v_perm_b32 v2, v91, v87, s78
	v_dot4c_i32_i8_e32 v141, v80, v71
	v_dot4c_i32_i8_e32 v143, v1, v71
	v_perm_b32 v1, v83, v3, s79
	v_perm_b32 v3, v91, v87, s79
	v_perm_b32 v80, v2, v0, s71
	v_perm_b32 v0, v2, v0, s80
	v_mov_b32_e32 v87, 0
	v_dot4c_i32_i8_e32 v79, v88, v71
	v_dot4c_i32_i8_e32 v87, v0, v71
	v_perm_b32 v0, v3, v1, s71
	v_mov_b32_e32 v88, 0
	v_perm_b32 v82, v82, v89, s80
	v_dot4c_i32_i8_e32 v88, v0, v71
	v_perm_b32 v0, v3, v1, s80
	v_mov_b32_e32 v89, 0
	v_mov_b32_e32 v86, 0
	v_dot4c_i32_i8_e32 v89, v0, v71
	s_waitcnt vmcnt(10)
	v_perm_b32 v0, v96, v92, s78
	s_waitcnt vmcnt(8)
	v_perm_b32 v2, v104, v100, s78
	v_dot4c_i32_i8_e32 v86, v80, v71
	v_perm_b32 v1, v96, v92, s79
	v_perm_b32 v3, v104, v100, s79
	v_perm_b32 v80, v2, v0, s71
	v_perm_b32 v0, v2, v0, s80
	v_dot4c_i32_i8_e32 v142, v146, v71
	v_dot4c_i32_i8_e32 v141, v0, v72
	v_perm_b32 v0, v3, v1, s71
	v_dot4c_i32_i8_e32 v142, v0, v72
	v_perm_b32 v0, v3, v1, s80
	v_dot4c_i32_i8_e32 v140, v90, v71
	v_dot4c_i32_i8_e32 v5, v0, v72
	v_perm_b32 v0, v97, v93, s78
	v_perm_b32 v2, v105, v101, s78
	v_dot4c_i32_i8_e32 v7, v81, v71
	v_dot4c_i32_i8_e32 v140, v80, v72
	v_perm_b32 v1, v97, v93, s79
	v_perm_b32 v3, v105, v101, s79
	v_perm_b32 v80, v2, v0, s71
	v_perm_b32 v0, v2, v0, s80
	v_dot4c_i32_i8_e32 v7, v0, v72
	v_perm_b32 v0, v3, v1, s71
	v_dot4c_i32_i8_e32 v79, v0, v72
	v_perm_b32 v0, v3, v1, s80
	v_dot4c_i32_i8_e32 v143, v0, v72
	v_perm_b32 v0, v98, v94, s78
	v_perm_b32 v2, v106, v102, s78
	v_dot4c_i32_i8_e32 v145, v82, v71
	v_dot4c_i32_i8_e32 v6, v80, v72
	v_perm_b32 v1, v98, v94, s79
	v_perm_b32 v3, v106, v102, s79
	v_perm_b32 v80, v2, v0, s71
	v_perm_b32 v0, v2, v0, s80
	v_dot4c_i32_i8_e32 v145, v0, v72
	v_perm_b32 v0, v3, v1, s71
	v_dot4c_i32_i8_e32 v84, v0, v72
	v_perm_b32 v0, v3, v1, s80
	v_dot4c_i32_i8_e32 v85, v0, v72
	v_perm_b32 v0, v99, v95, s78
	v_perm_b32 v2, v107, v103, s78
	v_dot4c_i32_i8_e32 v144, v80, v72
	v_perm_b32 v1, v99, v95, s79
	v_perm_b32 v3, v107, v103, s79
	v_perm_b32 v80, v2, v0, s71
	v_perm_b32 v0, v2, v0, s80
	v_dot4c_i32_i8_e32 v87, v0, v72
	v_perm_b32 v0, v3, v1, s71
	v_dot4c_i32_i8_e32 v88, v0, v72
	v_perm_b32 v0, v3, v1, s80
	v_dot4c_i32_i8_e32 v89, v0, v72
	s_waitcnt vmcnt(6)
	v_perm_b32 v0, v112, v108, s78
	s_waitcnt vmcnt(4)
	v_perm_b32 v2, v120, v116, s78
	v_dot4c_i32_i8_e32 v86, v80, v72
	v_perm_b32 v1, v112, v108, s79
	v_perm_b32 v3, v120, v116, s79
	v_perm_b32 v80, v2, v0, s71
	v_perm_b32 v0, v2, v0, s80
	v_dot4c_i32_i8_e32 v141, v0, v73
	v_perm_b32 v0, v3, v1, s71
	v_dot4c_i32_i8_e32 v142, v0, v73
	v_perm_b32 v0, v3, v1, s80
	v_dot4c_i32_i8_e32 v5, v0, v73
	v_perm_b32 v0, v113, v109, s78
	v_perm_b32 v2, v121, v117, s78
	v_dot4c_i32_i8_e32 v140, v80, v73
	v_perm_b32 v1, v113, v109, s79
	v_perm_b32 v3, v121, v117, s79
	v_perm_b32 v80, v2, v0, s71
	v_perm_b32 v0, v2, v0, s80
	v_dot4c_i32_i8_e32 v7, v0, v73
	v_perm_b32 v0, v3, v1, s71
	v_dot4c_i32_i8_e32 v79, v0, v73
	v_perm_b32 v0, v3, v1, s80
	v_dot4c_i32_i8_e32 v143, v0, v73
	v_perm_b32 v0, v114, v110, s78
	v_perm_b32 v2, v122, v118, s78
	v_dot4c_i32_i8_e32 v6, v80, v73
	v_perm_b32 v1, v114, v110, s79
	v_perm_b32 v3, v122, v118, s79
	v_perm_b32 v80, v2, v0, s71
	v_perm_b32 v0, v2, v0, s80
	v_dot4c_i32_i8_e32 v145, v0, v73
	v_perm_b32 v0, v3, v1, s71
	v_dot4c_i32_i8_e32 v84, v0, v73
	v_perm_b32 v0, v3, v1, s80
	v_dot4c_i32_i8_e32 v85, v0, v73
	v_perm_b32 v0, v115, v111, s78
	v_perm_b32 v2, v123, v119, s78
	v_dot4c_i32_i8_e32 v144, v80, v73
	v_perm_b32 v1, v115, v111, s79
	v_perm_b32 v3, v123, v119, s79
	v_perm_b32 v80, v2, v0, s71
	v_perm_b32 v0, v2, v0, s80
	v_dot4c_i32_i8_e32 v87, v0, v73
	v_perm_b32 v0, v3, v1, s71
	v_dot4c_i32_i8_e32 v88, v0, v73
	v_perm_b32 v0, v3, v1, s80
	v_dot4c_i32_i8_e32 v89, v0, v73
	s_waitcnt vmcnt(2)
; __device__ __forceinline__ unsigned pk2(float lo, float hi) { unsigned r; asm volatile("v_cvt_pk_bf16_f32 %0, %1, %2" : "=v"(r) : "v"(lo), "v"(hi)); return r; }
; __device__ __forceinline__ float bflo(unsigned u) { return __uint_as_float(u << 16); }
; __device__ __forceinline__ void peer_expert_phase(const Args& a, int layer, LAS unsigned char* lds, int G, int bid) {
;     ...
;                         iac[4 * q + 0] = __builtin_amdgcn_sdot4((int)__builtin_amdgcn_perm(cdlo, ablo, 0x05040100u), (int)W4[i][G4], iac[4 * q + 0], false);
;                         iac[4 * q + 1] = __builtin_amdgcn_sdot4((int)__builtin_amdgcn_perm(cdlo, ablo, 0x07060302u), (int)W4[i][G4], iac[4 * q + 1], false);
;                         iac[4 * q + 2] = __builtin_amdgcn_sdot4((int)__builtin_amdgcn_perm(cdhi, abhi, 0x05040100u), (int)W4[i][G4], iac[4 * q + 2], false);
;                         iac[4 * q + 3] = __builtin_amdgcn_sdot4((int)__builtin_amdgcn_perm(cdhi, abhi, 0x07060302u), (int)W4[i][G4], iac[4 * q + 3], false); }
;                 f32x2 ac[8];
; #pragma unroll
;                 for (int q = 0; q < 8; ++q) ac[q] = (f32x2){(float)iac[2 * q] * wsc[i], (float)iac[2 * q + 1] * wsc[i]};
;                 f32x2 b4_[4], b2_[2], b1_;
; #pragma unroll
;                 for (int q = 0; q < 4; ++q) { const f32x2 snd = (lane & 32) ? ac[q] : ac[q + 4], kp = (lane & 32) ? ac[q + 4] : ac[q]; b4_[q] = (f32x2){kp.x + __shfl_xor(snd.x, 32), kp.y + __shfl_xor(snd.y, 32)}; }
; #pragma unroll
;                 for (int q = 0; q < 2; ++q) { const f32x2 snd = (lane & 16) ? b4_[q] : b4_[q + 2], kp = (lane & 16) ? b4_[q + 2] : b4_[q]; b2_[q] = (f32x2){kp.x + __shfl_xor(snd.x, 16), kp.y + __shfl_xor(snd.y, 16)}; }
;                 { const f32x2 snd = (lane & 8) ? b2_[0] : b2_[1], kp = (lane & 8) ? b2_[1] : b2_[0]; b1_ = (f32x2){kp.x + __shfl_xor(snd.x, 8), kp.y + __shfl_xor(snd.y, 8)}; }
;                 const size_t off = (size_t)tok * DM + s * 128 + 16 * l7 + 2 * g8;
;                 const unsigned hb0 = *(const unsigned*)(H + off); f32x2 hn = {bflo(hb0) + b1_.x, bfhi(hb0) + b1_.y};
;                 if (ok) {
;                     { const unsigned hb1 = pk2(hn.x, hn.y); *(unsigned*)(H + off) = hb1; hn = (f32x2){bflo(hb1), bfhi(hb1)}; }
;                     ssq[i] += hn.x * hn.x + hn.y * hn.y; hgm[i] = fmaxf(hgm[i], fmaxf(fabsf(hn.x * gsl.x), fabsf(hn.y * gsl.y))); }
	v_perm_b32 v0, v128, v124, s78
	s_waitcnt vmcnt(0)
	v_perm_b32 v2, v136, v132, s78
	v_dot4c_i32_i8_e32 v86, v80, v73
	v_perm_b32 v1, v128, v124, s79
	v_perm_b32 v3, v136, v132, s79
	v_perm_b32 v80, v2, v0, s71
	v_perm_b32 v0, v2, v0, s80
	v_dot4c_i32_i8_e32 v141, v0, v74
	v_perm_b32 v0, v3, v1, s71
	v_dot4c_i32_i8_e32 v142, v0, v74
	v_perm_b32 v0, v3, v1, s80
	v_dot4c_i32_i8_e32 v5, v0, v74
	v_perm_b32 v0, v129, v125, s78
	v_perm_b32 v2, v137, v133, s78
	v_dot4c_i32_i8_e32 v140, v80, v74
	v_perm_b32 v1, v129, v125, s79
	v_perm_b32 v3, v137, v133, s79
	v_perm_b32 v80, v2, v0, s71
	v_perm_b32 v0, v2, v0, s80
	v_dot4c_i32_i8_e32 v7, v0, v74
	v_perm_b32 v0, v3, v1, s71
	v_dot4c_i32_i8_e32 v79, v0, v74
	v_perm_b32 v0, v3, v1, s80
	v_dot4c_i32_i8_e32 v143, v0, v74
	v_perm_b32 v0, v130, v126, s78
	v_perm_b32 v2, v138, v134, s78
	v_dot4c_i32_i8_e32 v6, v80, v74
	v_perm_b32 v1, v130, v126, s79
	v_perm_b32 v3, v138, v134, s79
	v_perm_b32 v80, v2, v0, s71
	v_perm_b32 v0, v2, v0, s80
	v_dot4c_i32_i8_e32 v145, v0, v74
	v_perm_b32 v0, v3, v1, s71
	v_dot4c_i32_i8_e32 v84, v0, v74
	v_perm_b32 v0, v3, v1, s80
	v_dot4c_i32_i8_e32 v85, v0, v74
	v_perm_b32 v0, v131, v127, s78
	v_perm_b32 v2, v139, v135, s78
	v_dot4c_i32_i8_e32 v144, v80, v74
	v_perm_b32 v1, v131, v127, s79
	v_perm_b32 v3, v139, v135, s79
	v_perm_b32 v80, v2, v0, s71
	v_perm_b32 v0, v2, v0, s80
	v_dot4c_i32_i8_e32 v87, v0, v74
	v_perm_b32 v0, v3, v1, s71
	v_dot4c_i32_i8_e32 v88, v0, v74
	v_perm_b32 v0, v3, v1, s80
	v_dot4c_i32_i8_e32 v89, v0, v74
	v_cvt_f32_i32_e32 v1, v141
	v_cvt_f32_i32_e32 v0, v140
	v_cvt_f32_i32_e32 v83, v145
	v_cvt_f32_i32_e32 v82, v144
	v_dot4c_i32_i8_e32 v86, v80, v74
	v_cvt_f32_i32_e32 v3, v5
	v_cvt_f32_i32_e32 v2, v142
	v_cvt_f32_i32_e32 v85, v85
	v_cvt_f32_i32_e32 v84, v84
	v_cvt_f32_i32_e32 v7, v7
	v_cvt_f32_i32_e32 v6, v6
	v_cvt_f32_i32_e32 v87, v87
	v_cvt_f32_i32_e32 v86, v86
	v_cvt_f32_i32_e32 v81, v143
	v_cvt_f32_i32_e32 v80, v79
	v_cvt_f32_i32_e32 v89, v89
	v_cvt_f32_i32_e32 v88, v88
	v_pk_mul_f32 v[0:1], v[22:23], v[0:1]
	v_pk_mul_f32 v[82:83], v[22:23], v[82:83]
	v_pk_mul_f32 v[2:3], v[22:23], v[2:3]
	v_pk_mul_f32 v[84:85], v[22:23], v[84:85]
	v_cndmask_b32_e64 v5, v1, v83, s[0:1]
	v_cndmask_b32_e64 v79, v0, v82, s[0:1]
	v_pk_mul_f32 v[6:7], v[22:23], v[6:7]
	v_pk_mul_f32 v[86:87], v[22:23], v[86:87]
	ds_bpermute_b32 v90, v29, v79
	ds_bpermute_b32 v91, v29, v5
	v_cndmask_b32_e64 v5, v3, v85, s[0:1]
	v_cndmask_b32_e64 v79, v2, v84, s[0:1]
	v_pk_mul_f32 v[80:81], v[22:23], v[80:81]
	v_pk_mul_f32 v[88:89], v[22:23], v[88:89]
	ds_bpermute_b32 v92, v29, v79
	ds_bpermute_b32 v93, v29, v5
	v_cndmask_b32_e64 v5, v7, v87, s[0:1]
	v_cndmask_b32_e64 v79, v6, v86, s[0:1]
	v_cndmask_b32_e64 v1, v83, v1, s[0:1]
	v_cndmask_b32_e64 v0, v82, v0, s[0:1]
	ds_bpermute_b32 v82, v29, v79
	ds_bpermute_b32 v83, v29, v5
	v_cndmask_b32_e64 v5, v81, v89, s[0:1]
	v_cndmask_b32_e64 v79, v80, v88, s[0:1]
	v_cndmask_b32_e64 v3, v85, v3, s[0:1]
	v_cndmask_b32_e64 v2, v84, v2, s[0:1]
	ds_bpermute_b32 v84, v29, v79
	ds_bpermute_b32 v85, v29, v5
	v_cndmask_b32_e64 v7, v87, v7, s[0:1]
	v_cndmask_b32_e64 v6, v86, v6, s[0:1]
	s_waitcnt lgkmcnt(0)
	v_pk_add_f32 v[0:1], v[0:1], v[90:91]
	v_pk_add_f32 v[6:7], v[6:7], v[82:83]
	v_cndmask_b32_e64 v81, v89, v81, s[0:1]
	v_cndmask_b32_e64 v80, v88, v80, s[0:1]
	v_pk_add_f32 v[2:3], v[2:3], v[92:93]
	v_pk_add_f32 v[80:81], v[80:81], v[84:85]
	v_cndmask_b32_e64 v5, v1, v7, s[2:3]
	v_cndmask_b32_e64 v79, v0, v6, s[2:3]
	v_cndmask_b32_e64 v1, v7, v1, s[2:3]
	ds_bpermute_b32 v83, v30, v5
	v_cndmask_b32_e64 v5, v3, v81, s[2:3]
	v_cndmask_b32_e64 v7, v2, v80, s[2:3]
	ds_bpermute_b32 v82, v30, v79
	ds_bpermute_b32 v84, v30, v7
	ds_bpermute_b32 v85, v30, v5
	v_cndmask_b32_e64 v0, v6, v0, s[2:3]
	v_cndmask_b32_e64 v3, v81, v3, s[2:3]
	v_cndmask_b32_e64 v2, v80, v2, s[2:3]
	s_waitcnt lgkmcnt(2)
	v_pk_add_f32 v[0:1], v[0:1], v[82:83]
	s_waitcnt lgkmcnt(0)
	v_pk_add_f32 v[2:3], v[2:3], v[84:85]
	s_nop 0
	v_cndmask_b32_e64 v6, v1, v3, s[4:5]
	v_cndmask_b32_e64 v5, v0, v2, s[4:5]
	ds_bpermute_b32 v5, v31, v5
	ds_bpermute_b32 v6, v31, v6
	s_cbranch_vccnz .LBB0_2306
	v_lshl_add_u64 v[80:81], v[26:27], 0, s[48:49]
	v_cndmask_b32_e64 v1, v3, v1, s[4:5]
	v_cndmask_b32_e64 v0, v2, v0, s[4:5]
	s_waitcnt lgkmcnt(0)
	v_add_f32_e32 v1, v1, v6
	v_add_f32_e32 v0, v0, v5
	s_waitcnt vmcnt(0)
	v_and_b32_e32 v2, 0xffff0000, v242
	v_lshlrev_b32_e32 v3, 16, v242
	v_add_f32_e32 v1, v1, v2
	v_add_f32_e32 v0, v0, v3
	v_cvt_pk_bf16_f32 v1, v0, v1
	global_store_dword v[80:81], v1, off
	v_lshlrev_b32_e32 v0, 16, v1
	v_and_b32_e32 v1, 0xffff0000, v1
	v_pk_mul_f32 v[0:1], v[0:1], v[0:1]
	s_nop 0
	v_add_f32_e32 v0, v0, v1
	v_add_f32_e32 v60, v60, v0
; __device__ __forceinline__ void peer_expert_phase(const Args& a, int layer, LAS unsigned char* lds, int G, int bid) {
;     ...
;                 for (int c = 0; c < 16; ++c) { const unsigned eo = (unsigned)__shfl((int)(c < 8 ? eoa[i] : eob[i]), (8 * c + g8) & 63); r[c] = *(const u32x4*)(pvs + (eo + lo16)); }
;                 int iac[16];
; #pragma unroll
;                 for (int q = 0; q < 16; ++q) iac[q] = 0;
; #pragma unroll
;                 for (int G4 = 0; G4 < 4; ++G4)
; #pragma unroll
;                     for (int q = 0; q < 4; ++q) {
;                         const unsigned a_ = r[4 * G4][q], b_ = r[4 * G4 + 1][q], c_ = r[4 * G4 + 2][q], d_ = r[4 * G4 + 3][q];
;                         const unsigned ablo = __builtin_amdgcn_perm(b_, a_, 0x05010400u), abhi = __builtin_amdgcn_perm(b_, a_, 0x07030602u), cdlo = __builtin_amdgcn_perm(d_, c_, 0x05010400u), cdhi = __builtin_amdgcn_perm(d_, c_, 0x07030602u);
;                         iac[4 * q + 0] = __builtin_amdgcn_sdot4((int)__builtin_amdgcn_perm(cdlo, ablo, 0x05040100u), (int)W4[i][G4], iac[4 * q + 0], false);
;                         iac[4 * q + 1] = __builtin_amdgcn_sdot4((int)__builtin_amdgcn_perm(cdlo, ablo, 0x07060302u), (int)W4[i][G4], iac[4 * q + 1], false);
;                         iac[4 * q + 2] = __builtin_amdgcn_sdot4((int)__builtin_amdgcn_perm(cdhi, abhi, 0x05040100u), (int)W4[i][G4], iac[4 * q + 2], false);
;                         iac[4 * q + 3] = __builtin_amdgcn_sdot4((int)__builtin_amdgcn_perm(cdhi, abhi, 0x07060302u), (int)W4[i][G4], iac[4 * q + 3], false); }
.LBB0_2306:
	s_waitcnt lgkmcnt(1)
	s_waitcnt lgkmcnt(0)
	global_load_dwordx4 v[0:3], v195, s[22:23]
	s_nop 0
	global_load_dwordx4 v[80:83], v196, s[22:23]
	global_load_dwordx4 v[84:87], v197, s[22:23]
	global_load_dwordx4 v[88:91], v198, s[22:23]
	global_load_dwordx4 v[92:95], v199, s[22:23]
	global_load_dwordx4 v[96:99], v200, s[22:23]
	global_load_dwordx4 v[100:103], v201, s[22:23]
	global_load_dwordx4 v[104:107], v202, s[22:23]
	global_load_dwordx4 v[108:111], v203, s[22:23]
	s_nop 0
	global_load_dwordx4 v[112:115], v204, s[22:23]
	s_nop 0
	global_load_dwordx4 v[116:119], v205, s[22:23]
	s_nop 0
	global_load_dwordx4 v[120:123], v206, s[22:23]
	s_nop 0
	global_load_dwordx4 v[124:127], v207, s[22:23]
	s_nop 0
	global_load_dwordx4 v[128:131], v208, s[22:23]
	s_nop 0
	global_load_dwordx4 v[132:135], v209, s[22:23]
	s_nop 0
	global_load_dwordx4 v[136:139], v210, s[22:23]
	v_mov_b32_e32 v5, 0
	v_mov_b32_e32 v6, 0
	v_mov_b32_e32 v144, 0
	v_mov_b32_e32 v141, 0
	v_mov_b32_e32 v143, 0
	v_mov_b32_e32 v79, 0
	v_mov_b32_e32 v142, 0
	v_mov_b32_e32 v140, 0
	v_mov_b32_e32 v7, 0
	v_mov_b32_e32 v145, 0
	s_andn2_b64 vcc, exec, s[50:51]
	s_waitcnt vmcnt(14)
	v_perm_b32 v146, v80, v0, s78
	v_perm_b32 v0, v80, v0, s79
	s_waitcnt vmcnt(12)
	v_perm_b32 v80, v88, v84, s78
	v_perm_b32 v84, v88, v84, s79
	v_perm_b32 v88, v81, v1, s78
	v_perm_b32 v1, v81, v1, s79
	v_perm_b32 v81, v89, v85, s78
	v_perm_b32 v85, v89, v85, s79
	v_perm_b32 v89, v82, v2, s78
	v_perm_b32 v2, v82, v2, s79
	v_perm_b32 v82, v90, v86, s78
	v_perm_b32 v86, v90, v86, s79
	v_perm_b32 v90, v80, v146, s71
	v_perm_b32 v80, v80, v146, s80
	v_perm_b32 v146, v84, v0, s71
	v_perm_b32 v0, v84, v0, s80
	v_perm_b32 v84, v81, v88, s71
	v_perm_b32 v81, v81, v88, s80
	v_perm_b32 v88, v85, v1, s71
	v_perm_b32 v1, v85, v1, s80
	v_perm_b32 v85, v82, v89, s71
	v_dot4c_i32_i8_e32 v5, v0, v75
	v_dot4c_i32_i8_e32 v6, v84, v75
	v_perm_b32 v0, v86, v2, s71
	v_mov_b32_e32 v84, 0
	v_dot4c_i32_i8_e32 v144, v85, v75
	v_dot4c_i32_i8_e32 v84, v0, v75
	v_perm_b32 v0, v86, v2, s80
	v_mov_b32_e32 v85, 0
	v_dot4c_i32_i8_e32 v85, v0, v75
	v_perm_b32 v0, v83, v3, s78
	v_perm_b32 v2, v91, v87, s78
	v_dot4c_i32_i8_e32 v141, v80, v75
	v_dot4c_i32_i8_e32 v143, v1, v75
	v_perm_b32 v1, v83, v3, s79
	v_perm_b32 v3, v91, v87, s79
	v_perm_b32 v80, v2, v0, s71
	v_perm_b32 v0, v2, v0, s80
	v_mov_b32_e32 v87, 0
	v_dot4c_i32_i8_e32 v79, v88, v75
	v_dot4c_i32_i8_e32 v87, v0, v75
	v_perm_b32 v0, v3, v1, s71
	v_mov_b32_e32 v88, 0
	v_perm_b32 v82, v82, v89, s80
	v_dot4c_i32_i8_e32 v88, v0, v75
	v_perm_b32 v0, v3, v1, s80
	v_mov_b32_e32 v89, 0
	v_mov_b32_e32 v86, 0
	v_dot4c_i32_i8_e32 v89, v0, v75
	s_waitcnt vmcnt(10)
	v_perm_b32 v0, v96, v92, s78
	s_waitcnt vmcnt(8)
	v_perm_b32 v2, v104, v100, s78
	v_dot4c_i32_i8_e32 v86, v80, v75
	v_perm_b32 v1, v96, v92, s79
	v_perm_b32 v3, v104, v100, s79
	v_perm_b32 v80, v2, v0, s71
	v_perm_b32 v0, v2, v0, s80
	v_dot4c_i32_i8_e32 v142, v146, v75
	v_dot4c_i32_i8_e32 v141, v0, v76
	v_perm_b32 v0, v3, v1, s71
	v_dot4c_i32_i8_e32 v142, v0, v76
	v_perm_b32 v0, v3, v1, s80
	v_dot4c_i32_i8_e32 v140, v90, v75
	v_dot4c_i32_i8_e32 v5, v0, v76
	v_perm_b32 v0, v97, v93, s78
	v_perm_b32 v2, v105, v101, s78
	v_dot4c_i32_i8_e32 v7, v81, v75
	v_dot4c_i32_i8_e32 v140, v80, v76
	v_perm_b32 v1, v97, v93, s79
	v_perm_b32 v3, v105, v101, s79
	v_perm_b32 v80, v2, v0, s71
	v_perm_b32 v0, v2, v0, s80
	v_dot4c_i32_i8_e32 v7, v0, v76
	v_perm_b32 v0, v3, v1, s71
	v_dot4c_i32_i8_e32 v79, v0, v76
	v_perm_b32 v0, v3, v1, s80
	v_dot4c_i32_i8_e32 v143, v0, v76
	v_perm_b32 v0, v98, v94, s78
	v_perm_b32 v2, v106, v102, s78
	v_dot4c_i32_i8_e32 v145, v82, v75
	v_dot4c_i32_i8_e32 v6, v80, v76
	v_perm_b32 v1, v98, v94, s79
	v_perm_b32 v3, v106, v102, s79
	v_perm_b32 v80, v2, v0, s71
	v_perm_b32 v0, v2, v0, s80
	v_dot4c_i32_i8_e32 v145, v0, v76
	v_perm_b32 v0, v3, v1, s71
	v_dot4c_i32_i8_e32 v84, v0, v76
	v_perm_b32 v0, v3, v1, s80
	v_dot4c_i32_i8_e32 v85, v0, v76
	v_perm_b32 v0, v99, v95, s78
	v_perm_b32 v2, v107, v103, s78
	v_dot4c_i32_i8_e32 v144, v80, v76
	v_perm_b32 v1, v99, v95, s79
	v_perm_b32 v3, v107, v103, s79
	v_perm_b32 v80, v2, v0, s71
	v_perm_b32 v0, v2, v0, s80
	v_dot4c_i32_i8_e32 v87, v0, v76
	v_perm_b32 v0, v3, v1, s71
	v_dot4c_i32_i8_e32 v88, v0, v76
	v_perm_b32 v0, v3, v1, s80
	v_dot4c_i32_i8_e32 v89, v0, v76
	s_waitcnt vmcnt(6)
	v_perm_b32 v0, v112, v108, s78
	s_waitcnt vmcnt(4)
	v_perm_b32 v2, v120, v116, s78
	v_dot4c_i32_i8_e32 v86, v80, v76
	v_perm_b32 v1, v112, v108, s79
	v_perm_b32 v3, v120, v116, s79
	v_perm_b32 v80, v2, v0, s71
	v_perm_b32 v0, v2, v0, s80
	v_dot4c_i32_i8_e32 v141, v0, v77
	v_perm_b32 v0, v3, v1, s71
	v_dot4c_i32_i8_e32 v142, v0, v77
	v_perm_b32 v0, v3, v1, s80
	v_dot4c_i32_i8_e32 v5, v0, v77
	v_perm_b32 v0, v113, v109, s78
	v_perm_b32 v2, v121, v117, s78
	v_dot4c_i32_i8_e32 v140, v80, v77
	v_perm_b32 v1, v113, v109, s79
	v_perm_b32 v3, v121, v117, s79
	v_perm_b32 v80, v2, v0, s71
	v_perm_b32 v0, v2, v0, s80
	v_dot4c_i32_i8_e32 v7, v0, v77
	v_perm_b32 v0, v3, v1, s71
	v_dot4c_i32_i8_e32 v79, v0, v77
	v_perm_b32 v0, v3, v1, s80
	v_dot4c_i32_i8_e32 v143, v0, v77
	v_perm_b32 v0, v114, v110, s78
	v_perm_b32 v2, v122, v118, s78
	v_dot4c_i32_i8_e32 v6, v80, v77
	v_perm_b32 v1, v114, v110, s79
	v_perm_b32 v3, v122, v118, s79
	v_perm_b32 v80, v2, v0, s71
	v_perm_b32 v0, v2, v0, s80
	v_dot4c_i32_i8_e32 v145, v0, v77
	v_perm_b32 v0, v3, v1, s71
	v_dot4c_i32_i8_e32 v84, v0, v77
	v_perm_b32 v0, v3, v1, s80
	v_dot4c_i32_i8_e32 v85, v0, v77
	v_perm_b32 v0, v115, v111, s78
	v_perm_b32 v2, v123, v119, s78
	v_dot4c_i32_i8_e32 v144, v80, v77
	v_perm_b32 v1, v115, v111, s79
	v_perm_b32 v3, v123, v119, s79
	v_perm_b32 v80, v2, v0, s71
	v_perm_b32 v0, v2, v0, s80
	v_dot4c_i32_i8_e32 v87, v0, v77
	v_perm_b32 v0, v3, v1, s71
	v_dot4c_i32_i8_e32 v88, v0, v77
	v_perm_b32 v0, v3, v1, s80
	v_dot4c_i32_i8_e32 v89, v0, v77
	s_waitcnt vmcnt(2)
; __device__ __forceinline__ unsigned pk2(float lo, float hi) { unsigned r; asm volatile("v_cvt_pk_bf16_f32 %0, %1, %2" : "=v"(r) : "v"(lo), "v"(hi)); return r; }
; __device__ __forceinline__ void peer_expert_phase(const Args& a, int layer, LAS unsigned char* lds, int G, int bid) {
;     ...
;                         iac[4 * q + 0] = __builtin_amdgcn_sdot4((int)__builtin_amdgcn_perm(cdlo, ablo, 0x05040100u), (int)W4[i][G4], iac[4 * q + 0], false);
;                         iac[4 * q + 1] = __builtin_amdgcn_sdot4((int)__builtin_amdgcn_perm(cdlo, ablo, 0x07060302u), (int)W4[i][G4], iac[4 * q + 1], false);
;                         iac[4 * q + 2] = __builtin_amdgcn_sdot4((int)__builtin_amdgcn_perm(cdhi, abhi, 0x05040100u), (int)W4[i][G4], iac[4 * q + 2], false);
;                         iac[4 * q + 3] = __builtin_amdgcn_sdot4((int)__builtin_amdgcn_perm(cdhi, abhi, 0x07060302u), (int)W4[i][G4], iac[4 * q + 3], false); }
;                 f32x2 ac[8];
; #pragma unroll
;                 for (int q = 0; q < 8; ++q) ac[q] = (f32x2){(float)iac[2 * q] * wsc[i], (float)iac[2 * q + 1] * wsc[i]};
;                 f32x2 b4_[4], b2_[2], b1_;
; #pragma unroll
;                 for (int q = 0; q < 4; ++q) { const f32x2 snd = (lane & 32) ? ac[q] : ac[q + 4], kp = (lane & 32) ? ac[q + 4] : ac[q]; b4_[q] = (f32x2){kp.x + __shfl_xor(snd.x, 32), kp.y + __shfl_xor(snd.y, 32)}; }
; #pragma unroll
;                 for (int q = 0; q < 2; ++q) { const f32x2 snd = (lane & 16) ? b4_[q] : b4_[q + 2], kp = (lane & 16) ? b4_[q + 2] : b4_[q]; b2_[q] = (f32x2){kp.x + __shfl_xor(snd.x, 16), kp.y + __shfl_xor(snd.y, 16)}; }
;                 { const f32x2 snd = (lane & 8) ? b2_[0] : b2_[1], kp = (lane & 8) ? b2_[1] : b2_[0]; b1_ = (f32x2){kp.x + __shfl_xor(snd.x, 8), kp.y + __shfl_xor(snd.y, 8)}; }
;                 const size_t off = (size_t)tok * DM + s * 128 + 16 * l7 + 2 * g8;
;                 const unsigned hb0 = *(const unsigned*)(H + off); f32x2 hn = {bflo(hb0) + b1_.x, bfhi(hb0) + b1_.y};
;                 if (ok) {
;                     { const unsigned hb1 = pk2(hn.x, hn.y); *(unsigned*)(H + off) = hb1; hn = (f32x2){bflo(hb1), bfhi(hb1)}; }
;                     ssq[i] += hn.x * hn.x + hn.y * hn.y; hgm[i] = fmaxf(hgm[i], fmaxf(fabsf(hn.x * gsl.x), fabsf(hn.y * gsl.y))); }
;                 __builtin_amdgcn_sched_barrier(0);
;             }
;         }
	v_perm_b32 v0, v128, v124, s78
	s_waitcnt vmcnt(0)
	v_perm_b32 v2, v136, v132, s78
	v_dot4c_i32_i8_e32 v86, v80, v77
	v_perm_b32 v1, v128, v124, s79
	v_perm_b32 v3, v136, v132, s79
	v_perm_b32 v80, v2, v0, s71
	v_perm_b32 v0, v2, v0, s80
	v_dot4c_i32_i8_e32 v141, v0, v78
	v_perm_b32 v0, v3, v1, s71
	v_dot4c_i32_i8_e32 v142, v0, v78
	v_perm_b32 v0, v3, v1, s80
	v_dot4c_i32_i8_e32 v5, v0, v78
	v_perm_b32 v0, v129, v125, s78
	v_perm_b32 v2, v137, v133, s78
	v_dot4c_i32_i8_e32 v140, v80, v78
	v_perm_b32 v1, v129, v125, s79
	v_perm_b32 v3, v137, v133, s79
	v_perm_b32 v80, v2, v0, s71
	v_perm_b32 v0, v2, v0, s80
	v_dot4c_i32_i8_e32 v7, v0, v78
	v_perm_b32 v0, v3, v1, s71
	v_dot4c_i32_i8_e32 v79, v0, v78
	v_perm_b32 v0, v3, v1, s80
	v_dot4c_i32_i8_e32 v143, v0, v78
	v_perm_b32 v0, v130, v126, s78
	v_perm_b32 v2, v138, v134, s78
	v_dot4c_i32_i8_e32 v6, v80, v78
	v_perm_b32 v1, v130, v126, s79
	v_perm_b32 v3, v138, v134, s79
	v_perm_b32 v80, v2, v0, s71
	v_perm_b32 v0, v2, v0, s80
	v_dot4c_i32_i8_e32 v145, v0, v78
	v_perm_b32 v0, v3, v1, s71
	v_dot4c_i32_i8_e32 v84, v0, v78
	v_perm_b32 v0, v3, v1, s80
	v_dot4c_i32_i8_e32 v85, v0, v78
	v_perm_b32 v0, v131, v127, s78
	v_perm_b32 v2, v139, v135, s78
	v_dot4c_i32_i8_e32 v144, v80, v78
	v_perm_b32 v1, v131, v127, s79
	v_perm_b32 v3, v139, v135, s79
	v_perm_b32 v80, v2, v0, s71
	v_perm_b32 v0, v2, v0, s80
	v_dot4c_i32_i8_e32 v87, v0, v78
	v_perm_b32 v0, v3, v1, s71
	v_dot4c_i32_i8_e32 v88, v0, v78
	v_perm_b32 v0, v3, v1, s80
	v_dot4c_i32_i8_e32 v89, v0, v78
	v_cvt_f32_i32_e32 v1, v141
	v_cvt_f32_i32_e32 v0, v140
	v_cvt_f32_i32_e32 v83, v145
	v_cvt_f32_i32_e32 v82, v144
	v_dot4c_i32_i8_e32 v86, v80, v78
	v_cvt_f32_i32_e32 v3, v5
	v_cvt_f32_i32_e32 v2, v142
	v_cvt_f32_i32_e32 v85, v85
	v_cvt_f32_i32_e32 v84, v84
	v_cvt_f32_i32_e32 v7, v7
	v_cvt_f32_i32_e32 v6, v6
	v_cvt_f32_i32_e32 v87, v87
	v_cvt_f32_i32_e32 v86, v86
	v_cvt_f32_i32_e32 v81, v143
	v_cvt_f32_i32_e32 v80, v79
	v_cvt_f32_i32_e32 v89, v89
	v_cvt_f32_i32_e32 v88, v88
	v_pk_mul_f32 v[0:1], v[24:25], v[0:1]
	v_pk_mul_f32 v[82:83], v[24:25], v[82:83]
	v_pk_mul_f32 v[2:3], v[24:25], v[2:3]
	v_pk_mul_f32 v[84:85], v[24:25], v[84:85]
	v_cndmask_b32_e64 v5, v1, v83, s[0:1]
	v_cndmask_b32_e64 v79, v0, v82, s[0:1]
	v_pk_mul_f32 v[6:7], v[24:25], v[6:7]
	v_pk_mul_f32 v[86:87], v[24:25], v[86:87]
	ds_bpermute_b32 v90, v29, v79
	ds_bpermute_b32 v91, v29, v5
	v_cndmask_b32_e64 v5, v3, v85, s[0:1]
	v_cndmask_b32_e64 v79, v2, v84, s[0:1]
	v_pk_mul_f32 v[80:81], v[24:25], v[80:81]
	v_pk_mul_f32 v[88:89], v[24:25], v[88:89]
	ds_bpermute_b32 v92, v29, v79
	ds_bpermute_b32 v93, v29, v5
	v_cndmask_b32_e64 v5, v7, v87, s[0:1]
	v_cndmask_b32_e64 v79, v6, v86, s[0:1]
	v_cndmask_b32_e64 v1, v83, v1, s[0:1]
	v_cndmask_b32_e64 v0, v82, v0, s[0:1]
	ds_bpermute_b32 v82, v29, v79
	ds_bpermute_b32 v83, v29, v5
	v_cndmask_b32_e64 v5, v81, v89, s[0:1]
	v_cndmask_b32_e64 v79, v80, v88, s[0:1]
	v_cndmask_b32_e64 v3, v85, v3, s[0:1]
	v_cndmask_b32_e64 v2, v84, v2, s[0:1]
	ds_bpermute_b32 v84, v29, v79
	ds_bpermute_b32 v85, v29, v5
	v_cndmask_b32_e64 v7, v87, v7, s[0:1]
	v_cndmask_b32_e64 v6, v86, v6, s[0:1]
	s_waitcnt lgkmcnt(0)
	v_pk_add_f32 v[0:1], v[0:1], v[90:91]
	v_pk_add_f32 v[6:7], v[6:7], v[82:83]
	v_cndmask_b32_e64 v81, v89, v81, s[0:1]
	v_cndmask_b32_e64 v80, v88, v80, s[0:1]
	v_pk_add_f32 v[2:3], v[2:3], v[92:93]
	v_pk_add_f32 v[80:81], v[80:81], v[84:85]
	v_cndmask_b32_e64 v5, v1, v7, s[2:3]
	v_cndmask_b32_e64 v79, v0, v6, s[2:3]
	v_cndmask_b32_e64 v1, v7, v1, s[2:3]
	ds_bpermute_b32 v83, v30, v5
	v_cndmask_b32_e64 v5, v3, v81, s[2:3]
	v_cndmask_b32_e64 v7, v2, v80, s[2:3]
	ds_bpermute_b32 v82, v30, v79
	ds_bpermute_b32 v84, v30, v7
	ds_bpermute_b32 v85, v30, v5
	v_cndmask_b32_e64 v0, v6, v0, s[2:3]
	v_cndmask_b32_e64 v3, v81, v3, s[2:3]
	v_cndmask_b32_e64 v2, v80, v2, s[2:3]
	s_waitcnt lgkmcnt(2)
	v_pk_add_f32 v[0:1], v[0:1], v[82:83]
	s_waitcnt lgkmcnt(0)
	v_pk_add_f32 v[2:3], v[2:3], v[84:85]
	s_nop 0
	v_cndmask_b32_e64 v6, v1, v3, s[4:5]
	v_cndmask_b32_e64 v5, v0, v2, s[4:5]
	ds_bpermute_b32 v5, v31, v5
	ds_bpermute_b32 v6, v31, v6
	s_cbranch_vccnz .LBB0_2301
	v_lshl_add_u64 v[26:27], v[26:27], 0, s[52:53]
	v_cndmask_b32_e64 v1, v3, v1, s[4:5]
	v_cndmask_b32_e64 v0, v2, v0, s[4:5]
	s_waitcnt lgkmcnt(0)
	v_add_f32_e32 v1, v1, v6
	v_add_f32_e32 v0, v0, v5
	s_waitcnt vmcnt(0)
	v_and_b32_e32 v2, 0xffff0000, v243
	v_lshlrev_b32_e32 v3, 16, v243
	v_add_f32_e32 v1, v1, v2
	v_add_f32_e32 v0, v0, v3
	v_cvt_pk_bf16_f32 v1, v0, v1
	global_store_dword v[26:27], v1, off
	v_lshlrev_b32_e32 v0, 16, v1
	v_and_b32_e32 v1, 0xffff0000, v1
	v_pk_mul_f32 v[0:1], v[0:1], v[0:1]
	s_nop 0
	v_add_f32_e32 v0, v0, v1
	v_add_f32_e32 v59, v59, v0
	s_branch .LBB0_2301
